# GEMM K-loops: 105 of 160 LDS-DMA loads rewritten to SGPR-base + 32-bit lane-offset (SADDR) form, 94 64-bit VALU address adds removed from the load segments
# baseline (speedup 1.0000x reference)
.LBB0_378:
	s_add_u32 s28, s36, 0xfff80080
	s_addc_u32 s29, s37, -1
	s_add_i32 s42, 0, 0x10000
	s_cmp_eq_u32 vcc_hi, 28
	s_cselect_b32 s53, s11, s29
	s_cselect_b32 s52, s21, s28
	s_cselect_b32 s51, s41, s79
	s_cselect_b32 s50, vcc_lo, s78
	s_add_i32 s43, 0, 0x14000
	v_add_u32_e32 v140, s42, v169
	v_add_u32_e32 v173, s43, v169
	ds_read_b128 v[128:131], v140
	ds_read_b128 v[132:135], v140 offset:1024
	ds_read_b128 v[136:139], v140 offset:2048
	ds_read_b128 v[140:143], v140 offset:3072
	ds_read_b128 v[156:159], v173
	ds_read_b128 v[160:163], v173 offset:1024
	ds_read_b128 v[164:167], v173 offset:2048
	ds_read_b128 v[174:177], v173 offset:3072
	s_add_i32 m0, s88, 0xc000
	ds_read_b128 v[178:181], v172
	ds_read_b128 v[194:197], v172 offset:1024
	ds_read_b128 v[198:201], v172 offset:2048
	ds_read_b128 v[202:205], v172 offset:3072
	ds_read_b128 v[206:209], v172 offset:4096
	ds_read_b128 v[224:227], v172 offset:5120
	ds_read_b128 v[228:231], v172 offset:6144
	ds_read_b128 v[232:235], v172 offset:7168
	global_load_lds_dwordx4 v152, s[36:37]
	s_add_i32 m0, s88, 0xe000
	s_nop 0
	global_load_lds_dwordx4 v154, s[36:37]
	s_waitcnt vmcnt(8)
	s_waitcnt lgkmcnt(0)
	s_barrier
	s_setprio 1
	s_waitcnt lgkmcnt(0)
	v_mfma_f32_16x16x32_bf16 v[124:127], v[128:131], v[178:181], v[124:127]
	v_mfma_f32_16x16x32_bf16 v[120:123], v[136:139], v[178:181], v[120:123]
	v_mfma_f32_16x16x32_bf16 v[116:119], v[128:131], v[198:201], v[116:119]
	v_mfma_f32_16x16x32_bf16 v[108:111], v[136:139], v[198:201], v[108:111]
	v_mfma_f32_16x16x32_bf16 v[100:103], v[128:131], v[206:209], v[100:103]
	v_mfma_f32_16x16x32_bf16 v[92:95], v[136:139], v[206:209], v[92:95]
	v_mfma_f32_16x16x32_bf16 v[84:87], v[128:131], v[228:231], v[84:87]
	v_mfma_f32_16x16x32_bf16 v[76:79], v[136:139], v[228:231], v[76:79]
	v_mfma_f32_16x16x32_bf16 v[124:127], v[132:135], v[194:197], v[124:127]
	v_mfma_f32_16x16x32_bf16 v[120:123], v[140:143], v[194:197], v[120:123]
	v_mfma_f32_16x16x32_bf16 v[116:119], v[132:135], v[202:205], v[116:119]
	v_mfma_f32_16x16x32_bf16 v[108:111], v[140:143], v[202:205], v[108:111]
	v_mfma_f32_16x16x32_bf16 v[100:103], v[132:135], v[224:227], v[100:103]
	v_mfma_f32_16x16x32_bf16 v[92:95], v[140:143], v[224:227], v[92:95]
	v_mfma_f32_16x16x32_bf16 v[84:87], v[132:135], v[232:235], v[84:87]
	v_mfma_f32_16x16x32_bf16 v[76:79], v[140:143], v[232:235], v[76:79]
	s_setprio 0
	s_setprio 1
	v_mfma_f32_16x16x32_bf16 v[112:115], v[156:159], v[178:181], v[112:115]
	v_mfma_f32_16x16x32_bf16 v[104:107], v[164:167], v[178:181], v[104:107]
	v_mfma_f32_16x16x32_bf16 v[96:99], v[156:159], v[198:201], v[96:99]
	v_mfma_f32_16x16x32_bf16 v[88:91], v[164:167], v[198:201], v[88:91]
	v_mfma_f32_16x16x32_bf16 v[80:83], v[156:159], v[206:209], v[80:83]
	v_mfma_f32_16x16x32_bf16 v[72:75], v[164:167], v[206:209], v[72:75]
	v_mfma_f32_16x16x32_bf16 v[68:71], v[156:159], v[228:231], v[68:71]
	v_mfma_f32_16x16x32_bf16 v[64:67], v[164:167], v[228:231], v[64:67]
	v_mfma_f32_16x16x32_bf16 v[112:115], v[160:163], v[194:197], v[112:115]
	v_mfma_f32_16x16x32_bf16 v[104:107], v[174:177], v[194:197], v[104:107]
	v_mfma_f32_16x16x32_bf16 v[96:99], v[160:163], v[202:205], v[96:99]
	v_mfma_f32_16x16x32_bf16 v[88:91], v[174:177], v[202:205], v[88:91]
	v_mfma_f32_16x16x32_bf16 v[80:83], v[160:163], v[224:227], v[80:83]
	v_mfma_f32_16x16x32_bf16 v[72:75], v[174:177], v[224:227], v[72:75]
	v_mfma_f32_16x16x32_bf16 v[68:71], v[160:163], v[232:235], v[68:71]
	v_mfma_f32_16x16x32_bf16 v[64:67], v[174:177], v[232:235], v[64:67]
	s_setprio 0
	s_barrier
	s_add_i32 s28, s42, s62
	s_mov_b32 m0, s28
	ds_read_b128 v[178:181], v172 offset:16384
	ds_read_b128 v[194:197], v172 offset:17408
	ds_read_b128 v[198:201], v172 offset:18432
	ds_read_b128 v[202:205], v172 offset:19456
	ds_read_b128 v[206:209], v172 offset:20480
	ds_read_b128 v[224:227], v172 offset:21504
	ds_read_b128 v[228:231], v172 offset:22528
	ds_read_b128 v[232:235], v172 offset:23552
	global_load_lds_dwordx4 v146, s[50:51]
	s_add_i32 m0, s28, 0x2000
	s_add_u32 s28, s50, 0x80000
	s_addc_u32 s29, s51, 0
	s_add_i32 s42, s43, s62
	global_load_lds_dwordx4 v150, s[50:51]
	s_mov_b32 m0, s42
	s_nop 0
	global_load_lds_dwordx4 v146, s[28:29]
	s_add_i32 m0, s42, 0x2000
	s_nop 0
	global_load_lds_dwordx4 v150, s[28:29]
	s_mov_b32 m0, s88
	s_nop 0
	global_load_lds_dwordx4 v144, s[52:53]
	s_mov_b32 m0, s89
	s_nop 0
	global_load_lds_dwordx4 v148, s[52:53]
	s_waitcnt vmcnt(8)
	s_waitcnt lgkmcnt(0)
	s_barrier
	s_setprio 1
	s_waitcnt lgkmcnt(0)
	v_mfma_f32_16x16x32_bf16 v[60:63], v[128:131], v[178:181], v[60:63]
	v_mfma_f32_16x16x32_bf16 v[56:59], v[136:139], v[178:181], v[56:59]
	v_mfma_f32_16x16x32_bf16 v[52:55], v[128:131], v[198:201], v[52:55]
	v_mfma_f32_16x16x32_bf16 v[44:47], v[136:139], v[198:201], v[44:47]
	v_mfma_f32_16x16x32_bf16 v[36:39], v[128:131], v[206:209], v[36:39]
	v_mfma_f32_16x16x32_bf16 v[28:31], v[136:139], v[206:209], v[28:31]
	v_mfma_f32_16x16x32_bf16 v[20:23], v[128:131], v[228:231], v[20:23]
	v_mfma_f32_16x16x32_bf16 v[12:15], v[136:139], v[228:231], v[12:15]
	v_mfma_f32_16x16x32_bf16 v[60:63], v[132:135], v[194:197], v[60:63]
	v_mfma_f32_16x16x32_bf16 v[56:59], v[140:143], v[194:197], v[56:59]
	v_mfma_f32_16x16x32_bf16 v[52:55], v[132:135], v[202:205], v[52:55]
	v_mfma_f32_16x16x32_bf16 v[44:47], v[140:143], v[202:205], v[44:47]
	v_mfma_f32_16x16x32_bf16 v[36:39], v[132:135], v[224:227], v[36:39]
	v_mfma_f32_16x16x32_bf16 v[28:31], v[140:143], v[224:227], v[28:31]
	v_mfma_f32_16x16x32_bf16 v[20:23], v[132:135], v[232:235], v[20:23]
	v_mfma_f32_16x16x32_bf16 v[12:15], v[140:143], v[232:235], v[12:15]
	s_setprio 0
	s_setprio 1
	v_mfma_f32_16x16x32_bf16 v[48:51], v[156:159], v[178:181], v[48:51]
	v_mfma_f32_16x16x32_bf16 v[40:43], v[164:167], v[178:181], v[40:43]
	v_mfma_f32_16x16x32_bf16 v[32:35], v[156:159], v[198:201], v[32:35]
	v_mfma_f32_16x16x32_bf16 v[24:27], v[164:167], v[198:201], v[24:27]
	v_mfma_f32_16x16x32_bf16 v[16:19], v[156:159], v[206:209], v[16:19]
	v_mfma_f32_16x16x32_bf16 v[8:11], v[164:167], v[206:209], v[8:11]
	v_mfma_f32_16x16x32_bf16 v[4:7], v[156:159], v[228:231], v[4:7]
	v_mfma_f32_16x16x32_bf16 v[0:3], v[164:167], v[228:231], v[0:3]
	v_mfma_f32_16x16x32_bf16 v[48:51], v[160:163], v[194:197], v[48:51]
	v_mfma_f32_16x16x32_bf16 v[40:43], v[174:177], v[194:197], v[40:43]
	v_mfma_f32_16x16x32_bf16 v[32:35], v[160:163], v[202:205], v[32:35]
	v_mfma_f32_16x16x32_bf16 v[24:27], v[174:177], v[202:205], v[24:27]
	v_mfma_f32_16x16x32_bf16 v[16:19], v[160:163], v[224:227], v[16:19]
	v_mfma_f32_16x16x32_bf16 v[8:11], v[174:177], v[224:227], v[8:11]
	v_mfma_f32_16x16x32_bf16 v[4:7], v[160:163], v[232:235], v[4:7]
	v_mfma_f32_16x16x32_bf16 v[0:3], v[174:177], v[232:235], v[0:3]
	s_setprio 0
	s_barrier
	s_add_i32 s42, 0, 0x18000
	s_add_i32 s43, 0, 0x1c000
	v_add_u32_e32 v140, s42, v169
	v_add_u32_e32 v173, s43, v169
	ds_read_b128 v[128:131], v140
	ds_read_b128 v[132:135], v140 offset:1024
	ds_read_b128 v[136:139], v140 offset:2048
	ds_read_b128 v[140:143], v140 offset:3072
	ds_read_b128 v[156:159], v173
	ds_read_b128 v[160:163], v173 offset:1024
	ds_read_b128 v[164:167], v173 offset:2048
	ds_read_b128 v[174:177], v173 offset:3072
	s_add_u32 s28, s52, 0x80000
	s_addc_u32 s29, s53, 0
	s_mov_b32 m0, s26
	ds_read_b128 v[178:181], v172 offset:32768
	ds_read_b128 v[194:197], v172 offset:33792
	ds_read_b128 v[198:201], v172 offset:34816
	ds_read_b128 v[202:205], v172 offset:35840
	ds_read_b128 v[206:209], v172 offset:36864
	ds_read_b128 v[224:227], v172 offset:37888
	ds_read_b128 v[228:231], v172 offset:38912
	ds_read_b128 v[232:235], v172 offset:39936
	global_load_lds_dwordx4 v144, s[28:29]
	s_mov_b32 m0, s27
	s_nop 0
	global_load_lds_dwordx4 v148, s[28:29]
	s_waitcnt vmcnt(8)
	s_waitcnt lgkmcnt(0)
	s_barrier
	s_setprio 1
	s_waitcnt lgkmcnt(0)
	v_mfma_f32_16x16x32_bf16 v[124:127], v[128:131], v[178:181], v[124:127]
	v_mfma_f32_16x16x32_bf16 v[120:123], v[136:139], v[178:181], v[120:123]
	v_mfma_f32_16x16x32_bf16 v[116:119], v[128:131], v[198:201], v[116:119]
	v_mfma_f32_16x16x32_bf16 v[108:111], v[136:139], v[198:201], v[108:111]
	v_mfma_f32_16x16x32_bf16 v[100:103], v[128:131], v[206:209], v[100:103]
	v_mfma_f32_16x16x32_bf16 v[92:95], v[136:139], v[206:209], v[92:95]
	v_mfma_f32_16x16x32_bf16 v[84:87], v[128:131], v[228:231], v[84:87]
	v_mfma_f32_16x16x32_bf16 v[76:79], v[136:139], v[228:231], v[76:79]
	v_mfma_f32_16x16x32_bf16 v[124:127], v[132:135], v[194:197], v[124:127]
	v_mfma_f32_16x16x32_bf16 v[120:123], v[140:143], v[194:197], v[120:123]
	v_mfma_f32_16x16x32_bf16 v[116:119], v[132:135], v[202:205], v[116:119]
	v_mfma_f32_16x16x32_bf16 v[108:111], v[140:143], v[202:205], v[108:111]
	v_mfma_f32_16x16x32_bf16 v[100:103], v[132:135], v[224:227], v[100:103]
	v_mfma_f32_16x16x32_bf16 v[92:95], v[140:143], v[224:227], v[92:95]
	v_mfma_f32_16x16x32_bf16 v[84:87], v[132:135], v[232:235], v[84:87]
	v_mfma_f32_16x16x32_bf16 v[76:79], v[140:143], v[232:235], v[76:79]
	s_setprio 0
	s_setprio 1
	v_mfma_f32_16x16x32_bf16 v[112:115], v[156:159], v[178:181], v[112:115]
	v_mfma_f32_16x16x32_bf16 v[104:107], v[164:167], v[178:181], v[104:107]
	v_mfma_f32_16x16x32_bf16 v[96:99], v[156:159], v[198:201], v[96:99]
	v_mfma_f32_16x16x32_bf16 v[88:91], v[164:167], v[198:201], v[88:91]
	v_mfma_f32_16x16x32_bf16 v[80:83], v[156:159], v[206:209], v[80:83]
	v_mfma_f32_16x16x32_bf16 v[72:75], v[164:167], v[206:209], v[72:75]
	v_mfma_f32_16x16x32_bf16 v[68:71], v[156:159], v[228:231], v[68:71]
	v_mfma_f32_16x16x32_bf16 v[64:67], v[164:167], v[228:231], v[64:67]
	v_mfma_f32_16x16x32_bf16 v[112:115], v[160:163], v[194:197], v[112:115]
	v_mfma_f32_16x16x32_bf16 v[104:107], v[174:177], v[194:197], v[104:107]
	v_mfma_f32_16x16x32_bf16 v[96:99], v[160:163], v[202:205], v[96:99]
	v_mfma_f32_16x16x32_bf16 v[88:91], v[174:177], v[202:205], v[88:91]
	v_mfma_f32_16x16x32_bf16 v[80:83], v[160:163], v[224:227], v[80:83]
	v_mfma_f32_16x16x32_bf16 v[72:75], v[174:177], v[224:227], v[72:75]
	v_mfma_f32_16x16x32_bf16 v[68:71], v[160:163], v[232:235], v[68:71]
	v_mfma_f32_16x16x32_bf16 v[64:67], v[174:177], v[232:235], v[64:67]
	s_setprio 0
	s_barrier
	s_add_i32 s28, s42, s62
	s_add_i32 m0, s28, 0xffffff80
	ds_read_b128 v[178:181], v172 offset:49152
	ds_read_b128 v[194:197], v172 offset:50176
	ds_read_b128 v[198:201], v172 offset:51200
	ds_read_b128 v[202:205], v172 offset:52224
	ds_read_b128 v[206:209], v172 offset:53248
	ds_read_b128 v[224:227], v172 offset:54272
	ds_read_b128 v[228:231], v172 offset:55296
	ds_read_b128 v[232:235], v172 offset:56320
	global_load_lds_dwordx4 v146, s[50:51] offset:128
	s_add_i32 m0, s28, 0x1f80
	s_add_u32 s28, s50, 0x80080
	s_addc_u32 s29, s51, 0
	s_add_i32 s42, s43, s62
	global_load_lds_dwordx4 v150, s[50:51] offset:128
	s_mov_b32 m0, s42
	s_nop 0
	global_load_lds_dwordx4 v146, s[28:29]
	s_add_i32 m0, s42, 0x2000
	s_nop 0
	global_load_lds_dwordx4 v150, s[28:29]
	s_add_i32 m0, s94, 0xffffff80
	s_nop 0
	global_load_lds_dwordx4 v144, s[52:53] offset:128
	s_add_i32 m0, s95, 0xffffff80
	s_nop 0
	global_load_lds_dwordx4 v148, s[52:53] offset:128
	s_waitcnt vmcnt(8)
	s_waitcnt lgkmcnt(0)
	s_barrier
	s_setprio 1
	s_waitcnt lgkmcnt(0)
	v_mfma_f32_16x16x32_bf16 v[60:63], v[128:131], v[178:181], v[60:63]
	v_mfma_f32_16x16x32_bf16 v[56:59], v[136:139], v[178:181], v[56:59]
	v_mfma_f32_16x16x32_bf16 v[52:55], v[128:131], v[198:201], v[52:55]
	v_mfma_f32_16x16x32_bf16 v[44:47], v[136:139], v[198:201], v[44:47]
	v_mfma_f32_16x16x32_bf16 v[36:39], v[128:131], v[206:209], v[36:39]
	v_mfma_f32_16x16x32_bf16 v[28:31], v[136:139], v[206:209], v[28:31]
	v_mfma_f32_16x16x32_bf16 v[20:23], v[128:131], v[228:231], v[20:23]
	v_mfma_f32_16x16x32_bf16 v[12:15], v[136:139], v[228:231], v[12:15]
	v_mfma_f32_16x16x32_bf16 v[60:63], v[132:135], v[194:197], v[60:63]
	v_mfma_f32_16x16x32_bf16 v[56:59], v[140:143], v[194:197], v[56:59]
	v_mfma_f32_16x16x32_bf16 v[52:55], v[132:135], v[202:205], v[52:55]
	v_mfma_f32_16x16x32_bf16 v[44:47], v[140:143], v[202:205], v[44:47]
	v_mfma_f32_16x16x32_bf16 v[36:39], v[132:135], v[224:227], v[36:39]
	v_mfma_f32_16x16x32_bf16 v[28:31], v[140:143], v[224:227], v[28:31]
	v_mfma_f32_16x16x32_bf16 v[20:23], v[132:135], v[232:235], v[20:23]
	v_mfma_f32_16x16x32_bf16 v[12:15], v[140:143], v[232:235], v[12:15]
	s_setprio 0
	s_setprio 1
	v_mfma_f32_16x16x32_bf16 v[48:51], v[156:159], v[178:181], v[48:51]
	v_mfma_f32_16x16x32_bf16 v[40:43], v[164:167], v[178:181], v[40:43]
	v_mfma_f32_16x16x32_bf16 v[32:35], v[156:159], v[198:201], v[32:35]
	v_mfma_f32_16x16x32_bf16 v[24:27], v[164:167], v[198:201], v[24:27]
	v_mfma_f32_16x16x32_bf16 v[16:19], v[156:159], v[206:209], v[16:19]
	v_mfma_f32_16x16x32_bf16 v[8:11], v[164:167], v[206:209], v[8:11]
	v_mfma_f32_16x16x32_bf16 v[4:7], v[156:159], v[228:231], v[4:7]
	v_mfma_f32_16x16x32_bf16 v[0:3], v[164:167], v[228:231], v[0:3]
	v_mfma_f32_16x16x32_bf16 v[48:51], v[160:163], v[194:197], v[48:51]
	v_mfma_f32_16x16x32_bf16 v[40:43], v[174:177], v[194:197], v[40:43]
	v_mfma_f32_16x16x32_bf16 v[32:35], v[160:163], v[202:205], v[32:35]
	v_mfma_f32_16x16x32_bf16 v[24:27], v[174:177], v[202:205], v[24:27]
	v_mfma_f32_16x16x32_bf16 v[16:19], v[160:163], v[224:227], v[16:19]
	v_mfma_f32_16x16x32_bf16 v[8:11], v[174:177], v[224:227], v[8:11]
	v_mfma_f32_16x16x32_bf16 v[4:7], v[160:163], v[232:235], v[4:7]
	v_mfma_f32_16x16x32_bf16 v[0:3], v[174:177], v[232:235], v[0:3]
	s_setprio 0
	s_barrier
	s_add_i32 vcc_hi, vcc_hi, 2
	s_add_u32 s36, s36, 0x100
	s_addc_u32 s37, s37, 0
	s_add_u32 s78, s78, 0x100
	s_addc_u32 s79, s79, 0
	s_cmp_gt_u32 vcc_hi, 29
	s_cbranch_scc0 .LBB0_378
	s_and_b64 vcc, exec, s[14:15]
	s_cbranch_vccz .LBB0_381
	s_barrier

.LBB0_682:
	s_add_u32 s18, s16, 0x100
	s_addc_u32 s19, s17, 0
	s_add_u32 s28, s45, s16
	s_addc_u32 s29, s46, s17
	s_cmp_eq_u32 s47, 4
	s_cselect_b32 s36, 0, s18
	s_cselect_b32 s37, 0, s19
	s_cselect_b32 s30, s44, s28
	s_cselect_b32 s31, s9, s29
	s_add_u32 s36, s64, s36
	s_addc_u32 s37, s65, s37
	s_add_i32 s28, 0, 0x10000
	s_add_i32 s29, 0, 0x14000
	v_add_u32_e32 v168, s28, v154
	v_add_u32_e32 v194, s29, v154
	ds_read_b128 v[156:159], v168
	ds_read_b128 v[160:163], v168 offset:1024
	ds_read_b128 v[164:167], v168 offset:2048
	ds_read_b128 v[168:171], v168 offset:3072
	ds_read_b128 v[172:175], v194
	ds_read_b128 v[176:179], v194 offset:1024
	ds_read_b128 v[180:183], v194 offset:2048
	ds_read_b128 v[194:197], v194 offset:3072
	v_lshl_add_u64 v[210:211], v[150:151], 0, s[16:17]
	s_add_i32 m0, s20, 0xc000
	ds_read_b128 v[198:201], v155
	ds_read_b128 v[202:205], v155 offset:1024
	ds_read_b128 v[206:209], v155 offset:2048
	ds_read_b128 v[224:227], v155 offset:3072
	ds_read_b128 v[228:231], v155 offset:4096
	ds_read_b128 v[232:235], v155 offset:5120
	ds_read_b128 v[236:239], v155 offset:6144
	ds_read_b128 v[240:243], v155 offset:7168
	global_load_lds_dwordx4 v[210:211], off
	v_lshl_add_u64 v[210:211], v[152:153], 0, s[16:17]
	s_add_i32 m0, s20, 0xe000
	s_nop 0
	global_load_lds_dwordx4 v[210:211], off
	s_waitcnt vmcnt(8)
	s_waitcnt lgkmcnt(0)
	s_barrier
	s_setprio 1
	s_waitcnt lgkmcnt(0)
	v_mfma_f32_16x16x32_bf16 v[124:127], v[156:159], v[198:201], v[124:127]
	v_mfma_f32_16x16x32_bf16 v[120:123], v[164:167], v[198:201], v[120:123]
	v_mfma_f32_16x16x32_bf16 v[116:119], v[156:159], v[206:209], v[116:119]
	v_mfma_f32_16x16x32_bf16 v[108:111], v[164:167], v[206:209], v[108:111]
	v_mfma_f32_16x16x32_bf16 v[100:103], v[156:159], v[228:231], v[100:103]
	v_mfma_f32_16x16x32_bf16 v[92:95], v[164:167], v[228:231], v[92:95]
	v_mfma_f32_16x16x32_bf16 v[84:87], v[156:159], v[236:239], v[84:87]
	v_mfma_f32_16x16x32_bf16 v[76:79], v[164:167], v[236:239], v[76:79]
	v_mfma_f32_16x16x32_bf16 v[124:127], v[160:163], v[202:205], v[124:127]
	v_mfma_f32_16x16x32_bf16 v[120:123], v[168:171], v[202:205], v[120:123]
	v_mfma_f32_16x16x32_bf16 v[116:119], v[160:163], v[224:227], v[116:119]
	v_mfma_f32_16x16x32_bf16 v[108:111], v[168:171], v[224:227], v[108:111]
	v_mfma_f32_16x16x32_bf16 v[100:103], v[160:163], v[232:235], v[100:103]
	v_mfma_f32_16x16x32_bf16 v[92:95], v[168:171], v[232:235], v[92:95]
	v_mfma_f32_16x16x32_bf16 v[84:87], v[160:163], v[240:243], v[84:87]
	v_mfma_f32_16x16x32_bf16 v[76:79], v[168:171], v[240:243], v[76:79]
	s_setprio 0
	s_setprio 1
	v_mfma_f32_16x16x32_bf16 v[112:115], v[172:175], v[198:201], v[112:115]
	v_mfma_f32_16x16x32_bf16 v[104:107], v[180:183], v[198:201], v[104:107]
	v_mfma_f32_16x16x32_bf16 v[96:99], v[172:175], v[206:209], v[96:99]
	v_mfma_f32_16x16x32_bf16 v[88:91], v[180:183], v[206:209], v[88:91]
	v_mfma_f32_16x16x32_bf16 v[80:83], v[172:175], v[228:231], v[80:83]
	v_mfma_f32_16x16x32_bf16 v[72:75], v[180:183], v[228:231], v[72:75]
	v_mfma_f32_16x16x32_bf16 v[68:71], v[172:175], v[236:239], v[68:71]
	v_mfma_f32_16x16x32_bf16 v[64:67], v[180:183], v[236:239], v[64:67]
	v_mfma_f32_16x16x32_bf16 v[112:115], v[176:179], v[202:205], v[112:115]
	v_mfma_f32_16x16x32_bf16 v[104:107], v[194:197], v[202:205], v[104:107]
	v_mfma_f32_16x16x32_bf16 v[96:99], v[176:179], v[224:227], v[96:99]
	v_mfma_f32_16x16x32_bf16 v[88:91], v[194:197], v[224:227], v[88:91]
	v_mfma_f32_16x16x32_bf16 v[80:83], v[176:179], v[232:235], v[80:83]
	v_mfma_f32_16x16x32_bf16 v[72:75], v[194:197], v[232:235], v[72:75]
	v_mfma_f32_16x16x32_bf16 v[68:71], v[176:179], v[240:243], v[68:71]
	v_mfma_f32_16x16x32_bf16 v[64:67], v[194:197], v[240:243], v[64:67]
	s_setprio 0
	s_barrier
	s_add_i32 s16, s28, s4
	v_lshl_add_u64 v[210:211], s[30:31], 0, v[184:185]
	s_mov_b32 m0, s16
	ds_read_b128 v[198:201], v155 offset:16384
	ds_read_b128 v[202:205], v155 offset:17408
	ds_read_b128 v[206:209], v155 offset:18432
	ds_read_b128 v[224:227], v155 offset:19456
	ds_read_b128 v[228:231], v155 offset:20480
	ds_read_b128 v[232:235], v155 offset:21504
	ds_read_b128 v[236:239], v155 offset:22528
	ds_read_b128 v[240:243], v155 offset:23552
	global_load_lds_dwordx4 v[210:211], off
	s_add_i32 m0, s16, 0x2000
	s_add_u32 s16, s30, 0x20000
	s_addc_u32 s17, s31, 0
	s_add_i32 s28, s29, s4
	global_load_lds_dwordx4 v128, s[30:31]
	v_lshl_add_u64 v[246:247], s[16:17], 0, v[184:185]
	s_mov_b32 m0, s28
	s_nop 0
	global_load_lds_dwordx4 v[246:247], off
	s_add_i32 m0, s28, 0x2000
	s_nop 0
	global_load_lds_dwordx4 v128, s[16:17]
	s_mov_b32 m0, s20
	s_nop 0
	global_load_lds_dwordx4 v132, s[36:37]
	s_mov_b32 m0, s21
	s_nop 0
	global_load_lds_dwordx4 v130, s[36:37]
	s_waitcnt vmcnt(8)
	s_waitcnt lgkmcnt(0)
	s_barrier
	s_setprio 1
	s_waitcnt lgkmcnt(0)
	v_mfma_f32_16x16x32_bf16 v[60:63], v[156:159], v[198:201], v[60:63]
	v_mfma_f32_16x16x32_bf16 v[56:59], v[164:167], v[198:201], v[56:59]
	v_mfma_f32_16x16x32_bf16 v[52:55], v[156:159], v[206:209], v[52:55]
	v_mfma_f32_16x16x32_bf16 v[44:47], v[164:167], v[206:209], v[44:47]
	v_mfma_f32_16x16x32_bf16 v[36:39], v[156:159], v[228:231], v[36:39]
	v_mfma_f32_16x16x32_bf16 v[28:31], v[164:167], v[228:231], v[28:31]
	v_mfma_f32_16x16x32_bf16 v[20:23], v[156:159], v[236:239], v[20:23]
	v_mfma_f32_16x16x32_bf16 v[12:15], v[164:167], v[236:239], v[12:15]
	v_mfma_f32_16x16x32_bf16 v[60:63], v[160:163], v[202:205], v[60:63]
	v_mfma_f32_16x16x32_bf16 v[56:59], v[168:171], v[202:205], v[56:59]
	v_mfma_f32_16x16x32_bf16 v[52:55], v[160:163], v[224:227], v[52:55]
	v_mfma_f32_16x16x32_bf16 v[44:47], v[168:171], v[224:227], v[44:47]
	v_mfma_f32_16x16x32_bf16 v[36:39], v[160:163], v[232:235], v[36:39]
	v_mfma_f32_16x16x32_bf16 v[28:31], v[168:171], v[232:235], v[28:31]
	v_mfma_f32_16x16x32_bf16 v[20:23], v[160:163], v[240:243], v[20:23]
	v_mfma_f32_16x16x32_bf16 v[12:15], v[168:171], v[240:243], v[12:15]
	s_setprio 0
	s_setprio 1
	v_mfma_f32_16x16x32_bf16 v[48:51], v[172:175], v[198:201], v[48:51]
	v_mfma_f32_16x16x32_bf16 v[40:43], v[180:183], v[198:201], v[40:43]
	v_mfma_f32_16x16x32_bf16 v[32:35], v[172:175], v[206:209], v[32:35]
	v_mfma_f32_16x16x32_bf16 v[24:27], v[180:183], v[206:209], v[24:27]
	v_mfma_f32_16x16x32_bf16 v[16:19], v[172:175], v[228:231], v[16:19]
	v_mfma_f32_16x16x32_bf16 v[8:11], v[180:183], v[228:231], v[8:11]
	v_mfma_f32_16x16x32_bf16 v[4:7], v[172:175], v[236:239], v[4:7]
	v_mfma_f32_16x16x32_bf16 v[0:3], v[180:183], v[236:239], v[0:3]
	v_mfma_f32_16x16x32_bf16 v[48:51], v[176:179], v[202:205], v[48:51]
	v_mfma_f32_16x16x32_bf16 v[40:43], v[194:197], v[202:205], v[40:43]
	v_mfma_f32_16x16x32_bf16 v[32:35], v[176:179], v[224:227], v[32:35]
	v_mfma_f32_16x16x32_bf16 v[24:27], v[194:197], v[224:227], v[24:27]
	v_mfma_f32_16x16x32_bf16 v[16:19], v[176:179], v[232:235], v[16:19]
	v_mfma_f32_16x16x32_bf16 v[8:11], v[194:197], v[232:235], v[8:11]
	v_mfma_f32_16x16x32_bf16 v[4:7], v[176:179], v[240:243], v[4:7]
	v_mfma_f32_16x16x32_bf16 v[0:3], v[194:197], v[240:243], v[0:3]
	s_setprio 0
	s_barrier
	s_add_i32 s28, 0, 0x18000
	s_add_i32 s29, 0, 0x1c000
	v_add_u32_e32 v168, s28, v154
	v_add_u32_e32 v194, s29, v154
	ds_read_b128 v[156:159], v168
	ds_read_b128 v[160:163], v168 offset:1024
	ds_read_b128 v[164:167], v168 offset:2048
	ds_read_b128 v[168:171], v168 offset:3072
	ds_read_b128 v[172:175], v194
	ds_read_b128 v[176:179], v194 offset:1024
	ds_read_b128 v[180:183], v194 offset:2048
	ds_read_b128 v[194:197], v194 offset:3072
	s_add_u32 s16, s36, 0x20000
	s_addc_u32 s17, s37, 0
	s_mov_b32 m0, s26
	ds_read_b128 v[198:201], v155 offset:32768
	ds_read_b128 v[202:205], v155 offset:33792
	ds_read_b128 v[206:209], v155 offset:34816
	ds_read_b128 v[224:227], v155 offset:35840
	ds_read_b128 v[228:231], v155 offset:36864
	ds_read_b128 v[232:235], v155 offset:37888
	ds_read_b128 v[236:239], v155 offset:38912
	ds_read_b128 v[240:243], v155 offset:39936
	global_load_lds_dwordx4 v132, s[16:17]
	s_mov_b32 m0, s27
	s_nop 0
	global_load_lds_dwordx4 v130, s[16:17]
	s_waitcnt vmcnt(8)
	s_waitcnt lgkmcnt(0)
	s_barrier
	s_setprio 1
	s_waitcnt lgkmcnt(0)
	v_mfma_f32_16x16x32_bf16 v[124:127], v[156:159], v[198:201], v[124:127]
	v_mfma_f32_16x16x32_bf16 v[120:123], v[164:167], v[198:201], v[120:123]
	v_mfma_f32_16x16x32_bf16 v[116:119], v[156:159], v[206:209], v[116:119]
	v_mfma_f32_16x16x32_bf16 v[108:111], v[164:167], v[206:209], v[108:111]
	v_mfma_f32_16x16x32_bf16 v[100:103], v[156:159], v[228:231], v[100:103]
	v_mfma_f32_16x16x32_bf16 v[92:95], v[164:167], v[228:231], v[92:95]
	v_mfma_f32_16x16x32_bf16 v[84:87], v[156:159], v[236:239], v[84:87]
	v_mfma_f32_16x16x32_bf16 v[76:79], v[164:167], v[236:239], v[76:79]
	v_mfma_f32_16x16x32_bf16 v[124:127], v[160:163], v[202:205], v[124:127]
	v_mfma_f32_16x16x32_bf16 v[120:123], v[168:171], v[202:205], v[120:123]
	v_mfma_f32_16x16x32_bf16 v[116:119], v[160:163], v[224:227], v[116:119]
	v_mfma_f32_16x16x32_bf16 v[108:111], v[168:171], v[224:227], v[108:111]
	v_mfma_f32_16x16x32_bf16 v[100:103], v[160:163], v[232:235], v[100:103]
	v_mfma_f32_16x16x32_bf16 v[92:95], v[168:171], v[232:235], v[92:95]
	v_mfma_f32_16x16x32_bf16 v[84:87], v[160:163], v[240:243], v[84:87]
	v_mfma_f32_16x16x32_bf16 v[76:79], v[168:171], v[240:243], v[76:79]
	s_setprio 0
	s_setprio 1
	v_mfma_f32_16x16x32_bf16 v[112:115], v[172:175], v[198:201], v[112:115]
	v_mfma_f32_16x16x32_bf16 v[104:107], v[180:183], v[198:201], v[104:107]
	v_mfma_f32_16x16x32_bf16 v[96:99], v[172:175], v[206:209], v[96:99]
	v_mfma_f32_16x16x32_bf16 v[88:91], v[180:183], v[206:209], v[88:91]
	v_mfma_f32_16x16x32_bf16 v[80:83], v[172:175], v[228:231], v[80:83]
	v_mfma_f32_16x16x32_bf16 v[72:75], v[180:183], v[228:231], v[72:75]
	v_mfma_f32_16x16x32_bf16 v[68:71], v[172:175], v[236:239], v[68:71]
	v_mfma_f32_16x16x32_bf16 v[64:67], v[180:183], v[236:239], v[64:67]
	v_mfma_f32_16x16x32_bf16 v[112:115], v[176:179], v[202:205], v[112:115]
	v_mfma_f32_16x16x32_bf16 v[104:107], v[194:197], v[202:205], v[104:107]
	v_mfma_f32_16x16x32_bf16 v[96:99], v[176:179], v[224:227], v[96:99]
	v_mfma_f32_16x16x32_bf16 v[88:91], v[194:197], v[224:227], v[88:91]
	v_mfma_f32_16x16x32_bf16 v[80:83], v[176:179], v[232:235], v[80:83]
	v_mfma_f32_16x16x32_bf16 v[72:75], v[194:197], v[232:235], v[72:75]
	v_mfma_f32_16x16x32_bf16 v[68:71], v[176:179], v[240:243], v[68:71]
	v_mfma_f32_16x16x32_bf16 v[64:67], v[194:197], v[240:243], v[64:67]
	s_setprio 0
	s_barrier
	s_add_i32 s16, s28, s4
	v_lshl_add_u64 v[210:211], v[210:211], 0, s[68:69]
	s_mov_b32 m0, s16
	ds_read_b128 v[198:201], v155 offset:49152
	ds_read_b128 v[202:205], v155 offset:50176
	ds_read_b128 v[206:209], v155 offset:51200
	ds_read_b128 v[224:227], v155 offset:52224
	ds_read_b128 v[228:231], v155 offset:53248
	ds_read_b128 v[232:235], v155 offset:54272
	ds_read_b128 v[236:239], v155 offset:55296
	ds_read_b128 v[240:243], v155 offset:56320
	global_load_lds_dwordx4 v[210:211], off
	s_add_i32 m0, s16, 0x1f80
	s_add_u32 s16, s30, 0x20080
	s_addc_u32 s17, s31, 0
	s_add_i32 s28, s29, s4
	global_load_lds_dwordx4 v128, s[30:31] offset:128
	v_lshl_add_u64 v[210:211], s[16:17], 0, v[184:185]
	s_mov_b32 m0, s28
	s_nop 0
	global_load_lds_dwordx4 v[210:211], off
	s_add_i32 m0, s28, 0x2000
	s_nop 0
	global_load_lds_dwordx4 v128, s[16:17]
	s_add_i32 m0, s38, 0xffffff80
	s_nop 0
	global_load_lds_dwordx4 v132, s[36:37] offset:128
	s_add_i32 m0, s39, 0xffffff80
	s_nop 0
	global_load_lds_dwordx4 v130, s[36:37] offset:128
	s_waitcnt vmcnt(8)
	s_waitcnt lgkmcnt(0)
	s_barrier
	s_setprio 1
	s_waitcnt lgkmcnt(0)
	v_mfma_f32_16x16x32_bf16 v[60:63], v[156:159], v[198:201], v[60:63]
	v_mfma_f32_16x16x32_bf16 v[56:59], v[164:167], v[198:201], v[56:59]
	v_mfma_f32_16x16x32_bf16 v[52:55], v[156:159], v[206:209], v[52:55]
	v_mfma_f32_16x16x32_bf16 v[44:47], v[164:167], v[206:209], v[44:47]
	v_mfma_f32_16x16x32_bf16 v[36:39], v[156:159], v[228:231], v[36:39]
	v_mfma_f32_16x16x32_bf16 v[28:31], v[164:167], v[228:231], v[28:31]
	v_mfma_f32_16x16x32_bf16 v[20:23], v[156:159], v[236:239], v[20:23]
	v_mfma_f32_16x16x32_bf16 v[12:15], v[164:167], v[236:239], v[12:15]
	v_mfma_f32_16x16x32_bf16 v[60:63], v[160:163], v[202:205], v[60:63]
	v_mfma_f32_16x16x32_bf16 v[56:59], v[168:171], v[202:205], v[56:59]
	v_mfma_f32_16x16x32_bf16 v[52:55], v[160:163], v[224:227], v[52:55]
	v_mfma_f32_16x16x32_bf16 v[44:47], v[168:171], v[224:227], v[44:47]
	v_mfma_f32_16x16x32_bf16 v[36:39], v[160:163], v[232:235], v[36:39]
	v_mfma_f32_16x16x32_bf16 v[28:31], v[168:171], v[232:235], v[28:31]
	v_mfma_f32_16x16x32_bf16 v[20:23], v[160:163], v[240:243], v[20:23]
	v_mfma_f32_16x16x32_bf16 v[12:15], v[168:171], v[240:243], v[12:15]
	s_setprio 0
	s_setprio 1
	v_mfma_f32_16x16x32_bf16 v[48:51], v[172:175], v[198:201], v[48:51]
	v_mfma_f32_16x16x32_bf16 v[40:43], v[180:183], v[198:201], v[40:43]
	v_mfma_f32_16x16x32_bf16 v[32:35], v[172:175], v[206:209], v[32:35]
	v_mfma_f32_16x16x32_bf16 v[24:27], v[180:183], v[206:209], v[24:27]
	v_mfma_f32_16x16x32_bf16 v[16:19], v[172:175], v[228:231], v[16:19]
	v_mfma_f32_16x16x32_bf16 v[8:11], v[180:183], v[228:231], v[8:11]
	v_mfma_f32_16x16x32_bf16 v[4:7], v[172:175], v[236:239], v[4:7]
	v_mfma_f32_16x16x32_bf16 v[0:3], v[180:183], v[236:239], v[0:3]
	v_mfma_f32_16x16x32_bf16 v[48:51], v[176:179], v[202:205], v[48:51]
	v_mfma_f32_16x16x32_bf16 v[40:43], v[194:197], v[202:205], v[40:43]
	v_mfma_f32_16x16x32_bf16 v[32:35], v[176:179], v[224:227], v[32:35]
	v_mfma_f32_16x16x32_bf16 v[24:27], v[194:197], v[224:227], v[24:27]
	v_mfma_f32_16x16x32_bf16 v[16:19], v[176:179], v[232:235], v[16:19]
	v_mfma_f32_16x16x32_bf16 v[8:11], v[194:197], v[232:235], v[8:11]
	v_mfma_f32_16x16x32_bf16 v[4:7], v[176:179], v[240:243], v[4:7]
	v_mfma_f32_16x16x32_bf16 v[0:3], v[194:197], v[240:243], v[0:3]
	s_setprio 0
	s_barrier
	s_add_i32 s47, s47, 2
	s_cmp_gt_u32 s47, 5
	s_mov_b64 s[16:17], s[18:19]
	s_cbranch_scc0 .LBB0_682
	s_and_b64 vcc, exec, s[6:7]
	s_cbranch_vccz .LBB0_685
	s_barrier

.LBB0_805:
	s_add_u32 s28, s30, 0xfff80080
	s_addc_u32 s29, s31, -1
	s_add_i32 s38, 0, 0x10000
	s_cmp_eq_u32 s78, 28
	s_cselect_b32 s45, s9, s29
	s_cselect_b32 s44, s11, s28
	s_cselect_b32 s41, s60, s63
	s_cselect_b32 s40, s61, s62
	s_add_i32 s39, 0, 0x14000
	v_add_u32_e32 v154, s38, v143
	v_add_u32_e32 v170, s39, v143
	ds_read_b128 v[138:141], v154
	ds_read_b128 v[146:149], v154 offset:1024
	ds_read_b128 v[150:153], v154 offset:2048
	ds_read_b128 v[154:157], v154 offset:3072
	ds_read_b128 v[158:161], v170
	ds_read_b128 v[162:165], v170 offset:1024
	ds_read_b128 v[166:169], v170 offset:2048
	ds_read_b128 v[170:173], v170 offset:3072
	s_add_i32 m0, s21, 0xc000
	ds_read_b128 v[174:177], v145
	ds_read_b128 v[178:181], v145 offset:1024
	ds_read_b128 v[194:197], v145 offset:2048
	ds_read_b128 v[198:201], v145 offset:3072
	ds_read_b128 v[202:205], v145 offset:4096
	ds_read_b128 v[206:209], v145 offset:5120
	ds_read_b128 v[224:227], v145 offset:6144
	ds_read_b128 v[228:231], v145 offset:7168
	global_load_lds_dwordx4 v134, s[30:31]
	s_add_i32 m0, s21, 0xe000
	s_nop 0
	global_load_lds_dwordx4 v136, s[30:31]
	s_waitcnt vmcnt(8)
	s_waitcnt lgkmcnt(0)
	s_barrier
	s_setprio 1
	s_waitcnt lgkmcnt(0)
	v_mfma_f32_16x16x32_bf16 v[124:127], v[138:141], v[174:177], v[124:127]
	v_mfma_f32_16x16x32_bf16 v[120:123], v[150:153], v[174:177], v[120:123]
	v_mfma_f32_16x16x32_bf16 v[116:119], v[138:141], v[194:197], v[116:119]
	v_mfma_f32_16x16x32_bf16 v[104:107], v[150:153], v[194:197], v[104:107]
	v_mfma_f32_16x16x32_bf16 v[100:103], v[138:141], v[202:205], v[100:103]
	v_mfma_f32_16x16x32_bf16 v[88:91], v[150:153], v[202:205], v[88:91]
	v_mfma_f32_16x16x32_bf16 v[84:87], v[138:141], v[224:227], v[84:87]
	v_mfma_f32_16x16x32_bf16 v[72:75], v[150:153], v[224:227], v[72:75]
	v_mfma_f32_16x16x32_bf16 v[124:127], v[146:149], v[178:181], v[124:127]
	v_mfma_f32_16x16x32_bf16 v[120:123], v[154:157], v[178:181], v[120:123]
	v_mfma_f32_16x16x32_bf16 v[116:119], v[146:149], v[198:201], v[116:119]
	v_mfma_f32_16x16x32_bf16 v[104:107], v[154:157], v[198:201], v[104:107]
	v_mfma_f32_16x16x32_bf16 v[100:103], v[146:149], v[206:209], v[100:103]
	v_mfma_f32_16x16x32_bf16 v[88:91], v[154:157], v[206:209], v[88:91]
	v_mfma_f32_16x16x32_bf16 v[84:87], v[146:149], v[228:231], v[84:87]
	v_mfma_f32_16x16x32_bf16 v[72:75], v[154:157], v[228:231], v[72:75]
	s_setprio 0
	s_setprio 1
	v_mfma_f32_16x16x32_bf16 v[112:115], v[158:161], v[174:177], v[112:115]
	v_mfma_f32_16x16x32_bf16 v[108:111], v[166:169], v[174:177], v[108:111]
	v_mfma_f32_16x16x32_bf16 v[96:99], v[158:161], v[194:197], v[96:99]
	v_mfma_f32_16x16x32_bf16 v[92:95], v[166:169], v[194:197], v[92:95]
	v_mfma_f32_16x16x32_bf16 v[80:83], v[158:161], v[202:205], v[80:83]
	v_mfma_f32_16x16x32_bf16 v[76:79], v[166:169], v[202:205], v[76:79]
	v_mfma_f32_16x16x32_bf16 v[68:71], v[158:161], v[224:227], v[68:71]
	v_mfma_f32_16x16x32_bf16 v[64:67], v[166:169], v[224:227], v[64:67]
	v_mfma_f32_16x16x32_bf16 v[112:115], v[162:165], v[178:181], v[112:115]
	v_mfma_f32_16x16x32_bf16 v[108:111], v[170:173], v[178:181], v[108:111]
	v_mfma_f32_16x16x32_bf16 v[96:99], v[162:165], v[198:201], v[96:99]
	v_mfma_f32_16x16x32_bf16 v[92:95], v[170:173], v[198:201], v[92:95]
	v_mfma_f32_16x16x32_bf16 v[80:83], v[162:165], v[206:209], v[80:83]
	v_mfma_f32_16x16x32_bf16 v[76:79], v[170:173], v[206:209], v[76:79]
	v_mfma_f32_16x16x32_bf16 v[68:71], v[162:165], v[228:231], v[68:71]
	v_mfma_f32_16x16x32_bf16 v[64:67], v[170:173], v[228:231], v[64:67]
	s_setprio 0
	s_barrier
	s_add_i32 s28, s38, s20
	v_lshl_add_u64 v[182:183], s[40:41], 0, v[184:185]
	s_mov_b32 m0, s28
	ds_read_b128 v[174:177], v145 offset:16384
	ds_read_b128 v[178:181], v145 offset:17408
	ds_read_b128 v[194:197], v145 offset:18432
	ds_read_b128 v[198:201], v145 offset:19456
	ds_read_b128 v[202:205], v145 offset:20480
	ds_read_b128 v[206:209], v145 offset:21504
	ds_read_b128 v[224:227], v145 offset:22528
	ds_read_b128 v[228:231], v145 offset:23552
	global_load_lds_dwordx4 v[182:183], off
	s_add_i32 m0, s28, 0x2000
	s_add_u32 s28, s40, 0x80000
	s_addc_u32 s29, s41, 0
	s_add_i32 s38, s39, s20
	global_load_lds_dwordx4 v128, s[40:41]
	v_lshl_add_u64 v[216:217], s[28:29], 0, v[184:185]
	s_mov_b32 m0, s38
	s_nop 0
	global_load_lds_dwordx4 v[216:217], off
	s_add_i32 m0, s38, 0x2000
	s_nop 0
	global_load_lds_dwordx4 v128, s[28:29]
	s_mov_b32 m0, s21
	s_nop 0
	global_load_lds_dwordx4 v132, s[44:45]
	s_mov_b32 m0, s46
	s_nop 0
	global_load_lds_dwordx4 v130, s[44:45]
	s_waitcnt vmcnt(8)
	s_waitcnt lgkmcnt(0)
	s_barrier
	s_setprio 1
	s_waitcnt lgkmcnt(0)
	v_mfma_f32_16x16x32_bf16 v[60:63], v[138:141], v[174:177], v[60:63]
	v_mfma_f32_16x16x32_bf16 v[56:59], v[150:153], v[174:177], v[56:59]
	v_mfma_f32_16x16x32_bf16 v[52:55], v[138:141], v[194:197], v[52:55]
	v_mfma_f32_16x16x32_bf16 v[40:43], v[150:153], v[194:197], v[40:43]
	v_mfma_f32_16x16x32_bf16 v[36:39], v[138:141], v[202:205], v[36:39]
	v_mfma_f32_16x16x32_bf16 v[24:27], v[150:153], v[202:205], v[24:27]
	v_mfma_f32_16x16x32_bf16 v[20:23], v[138:141], v[224:227], v[20:23]
	v_mfma_f32_16x16x32_bf16 v[8:11], v[150:153], v[224:227], v[8:11]
	v_mfma_f32_16x16x32_bf16 v[60:63], v[146:149], v[178:181], v[60:63]
	v_mfma_f32_16x16x32_bf16 v[56:59], v[154:157], v[178:181], v[56:59]
	v_mfma_f32_16x16x32_bf16 v[52:55], v[146:149], v[198:201], v[52:55]
	v_mfma_f32_16x16x32_bf16 v[40:43], v[154:157], v[198:201], v[40:43]
	v_mfma_f32_16x16x32_bf16 v[36:39], v[146:149], v[206:209], v[36:39]
	v_mfma_f32_16x16x32_bf16 v[24:27], v[154:157], v[206:209], v[24:27]
	v_mfma_f32_16x16x32_bf16 v[20:23], v[146:149], v[228:231], v[20:23]
	v_mfma_f32_16x16x32_bf16 v[8:11], v[154:157], v[228:231], v[8:11]
	s_setprio 0
	s_setprio 1
	v_mfma_f32_16x16x32_bf16 v[48:51], v[158:161], v[174:177], v[48:51]
	v_mfma_f32_16x16x32_bf16 v[44:47], v[166:169], v[174:177], v[44:47]
	v_mfma_f32_16x16x32_bf16 v[32:35], v[158:161], v[194:197], v[32:35]
	v_mfma_f32_16x16x32_bf16 v[28:31], v[166:169], v[194:197], v[28:31]
	v_mfma_f32_16x16x32_bf16 v[16:19], v[158:161], v[202:205], v[16:19]
	v_mfma_f32_16x16x32_bf16 v[12:15], v[166:169], v[202:205], v[12:15]
	v_mfma_f32_16x16x32_bf16 v[4:7], v[158:161], v[224:227], v[4:7]
	v_mfma_f32_16x16x32_bf16 v[0:3], v[166:169], v[224:227], v[0:3]
	v_mfma_f32_16x16x32_bf16 v[48:51], v[162:165], v[178:181], v[48:51]
	v_mfma_f32_16x16x32_bf16 v[44:47], v[170:173], v[178:181], v[44:47]
	v_mfma_f32_16x16x32_bf16 v[32:35], v[162:165], v[198:201], v[32:35]
	v_mfma_f32_16x16x32_bf16 v[28:31], v[170:173], v[198:201], v[28:31]
	v_mfma_f32_16x16x32_bf16 v[16:19], v[162:165], v[206:209], v[16:19]
	v_mfma_f32_16x16x32_bf16 v[12:15], v[170:173], v[206:209], v[12:15]
	v_mfma_f32_16x16x32_bf16 v[4:7], v[162:165], v[228:231], v[4:7]
	v_mfma_f32_16x16x32_bf16 v[0:3], v[170:173], v[228:231], v[0:3]
	s_setprio 0
	s_barrier
	s_add_i32 s38, 0, 0x18000
	s_add_i32 s39, 0, 0x1c000
	v_add_u32_e32 v154, s38, v143
	v_add_u32_e32 v170, s39, v143
	ds_read_b128 v[138:141], v154
	ds_read_b128 v[146:149], v154 offset:1024
	ds_read_b128 v[150:153], v154 offset:2048
	ds_read_b128 v[154:157], v154 offset:3072
	ds_read_b128 v[158:161], v170
	ds_read_b128 v[162:165], v170 offset:1024
	ds_read_b128 v[166:169], v170 offset:2048
	ds_read_b128 v[170:173], v170 offset:3072
	s_add_u32 s28, s44, 0x80000
	s_addc_u32 s29, s45, 0
	s_mov_b32 m0, s47
	ds_read_b128 v[174:177], v145 offset:32768
	ds_read_b128 v[178:181], v145 offset:33792
	ds_read_b128 v[194:197], v145 offset:34816
	ds_read_b128 v[198:201], v145 offset:35840
	ds_read_b128 v[202:205], v145 offset:36864
	ds_read_b128 v[206:209], v145 offset:37888
	ds_read_b128 v[224:227], v145 offset:38912
	ds_read_b128 v[228:231], v145 offset:39936
	global_load_lds_dwordx4 v132, s[28:29]
	s_mov_b32 m0, s50
	s_nop 0
	global_load_lds_dwordx4 v130, s[28:29]
	s_waitcnt vmcnt(8)
	s_waitcnt lgkmcnt(0)
	s_barrier
	s_setprio 1
	s_waitcnt lgkmcnt(0)
	v_mfma_f32_16x16x32_bf16 v[124:127], v[138:141], v[174:177], v[124:127]
	v_mfma_f32_16x16x32_bf16 v[120:123], v[150:153], v[174:177], v[120:123]
	v_mfma_f32_16x16x32_bf16 v[116:119], v[138:141], v[194:197], v[116:119]
	v_mfma_f32_16x16x32_bf16 v[104:107], v[150:153], v[194:197], v[104:107]
	v_mfma_f32_16x16x32_bf16 v[100:103], v[138:141], v[202:205], v[100:103]
	v_mfma_f32_16x16x32_bf16 v[88:91], v[150:153], v[202:205], v[88:91]
	v_mfma_f32_16x16x32_bf16 v[84:87], v[138:141], v[224:227], v[84:87]
	v_mfma_f32_16x16x32_bf16 v[72:75], v[150:153], v[224:227], v[72:75]
	v_mfma_f32_16x16x32_bf16 v[124:127], v[146:149], v[178:181], v[124:127]
	v_mfma_f32_16x16x32_bf16 v[120:123], v[154:157], v[178:181], v[120:123]
	v_mfma_f32_16x16x32_bf16 v[116:119], v[146:149], v[198:201], v[116:119]
	v_mfma_f32_16x16x32_bf16 v[104:107], v[154:157], v[198:201], v[104:107]
	v_mfma_f32_16x16x32_bf16 v[100:103], v[146:149], v[206:209], v[100:103]
	v_mfma_f32_16x16x32_bf16 v[88:91], v[154:157], v[206:209], v[88:91]
	v_mfma_f32_16x16x32_bf16 v[84:87], v[146:149], v[228:231], v[84:87]
	v_mfma_f32_16x16x32_bf16 v[72:75], v[154:157], v[228:231], v[72:75]
	s_setprio 0
	s_setprio 1
	v_mfma_f32_16x16x32_bf16 v[112:115], v[158:161], v[174:177], v[112:115]
	v_mfma_f32_16x16x32_bf16 v[108:111], v[166:169], v[174:177], v[108:111]
	v_mfma_f32_16x16x32_bf16 v[96:99], v[158:161], v[194:197], v[96:99]
	v_mfma_f32_16x16x32_bf16 v[92:95], v[166:169], v[194:197], v[92:95]
	v_mfma_f32_16x16x32_bf16 v[80:83], v[158:161], v[202:205], v[80:83]
	v_mfma_f32_16x16x32_bf16 v[76:79], v[166:169], v[202:205], v[76:79]
	v_mfma_f32_16x16x32_bf16 v[68:71], v[158:161], v[224:227], v[68:71]
	v_mfma_f32_16x16x32_bf16 v[64:67], v[166:169], v[224:227], v[64:67]
	v_mfma_f32_16x16x32_bf16 v[112:115], v[162:165], v[178:181], v[112:115]
	v_mfma_f32_16x16x32_bf16 v[108:111], v[170:173], v[178:181], v[108:111]
	v_mfma_f32_16x16x32_bf16 v[96:99], v[162:165], v[198:201], v[96:99]
	v_mfma_f32_16x16x32_bf16 v[92:95], v[170:173], v[198:201], v[92:95]
	v_mfma_f32_16x16x32_bf16 v[80:83], v[162:165], v[206:209], v[80:83]
	v_mfma_f32_16x16x32_bf16 v[76:79], v[170:173], v[206:209], v[76:79]
	v_mfma_f32_16x16x32_bf16 v[68:71], v[162:165], v[228:231], v[68:71]
	v_mfma_f32_16x16x32_bf16 v[64:67], v[170:173], v[228:231], v[64:67]
	s_setprio 0
	s_barrier
	s_add_i32 s28, s38, s20
	v_lshl_add_u64 v[182:183], v[182:183], 0, s[68:69]
	s_mov_b32 m0, s28
	ds_read_b128 v[174:177], v145 offset:49152
	ds_read_b128 v[178:181], v145 offset:50176
	ds_read_b128 v[194:197], v145 offset:51200
	ds_read_b128 v[198:201], v145 offset:52224
	ds_read_b128 v[202:205], v145 offset:53248
	ds_read_b128 v[206:209], v145 offset:54272
	ds_read_b128 v[224:227], v145 offset:55296
	ds_read_b128 v[228:231], v145 offset:56320
	global_load_lds_dwordx4 v[182:183], off
	s_add_i32 m0, s28, 0x1f80
	s_add_u32 s28, s40, 0x80080
	s_addc_u32 s29, s41, 0
	s_add_i32 s38, s39, s20
	global_load_lds_dwordx4 v128, s[40:41] offset:128
	v_lshl_add_u64 v[182:183], s[28:29], 0, v[184:185]
	s_mov_b32 m0, s38
	s_nop 0
	global_load_lds_dwordx4 v[182:183], off
	s_add_i32 m0, s38, 0x2000
	s_nop 0
	global_load_lds_dwordx4 v128, s[28:29]
	s_add_i32 m0, s51, 0xffffff80
	s_nop 0
	global_load_lds_dwordx4 v132, s[44:45] offset:128
	s_add_i32 m0, s52, 0xffffff80
	s_nop 0
	global_load_lds_dwordx4 v130, s[44:45] offset:128
	s_waitcnt vmcnt(8)
	s_waitcnt lgkmcnt(0)
	s_barrier
	s_setprio 1
	s_waitcnt lgkmcnt(0)
	v_mfma_f32_16x16x32_bf16 v[60:63], v[138:141], v[174:177], v[60:63]
	v_mfma_f32_16x16x32_bf16 v[56:59], v[150:153], v[174:177], v[56:59]
	v_mfma_f32_16x16x32_bf16 v[52:55], v[138:141], v[194:197], v[52:55]
	v_mfma_f32_16x16x32_bf16 v[40:43], v[150:153], v[194:197], v[40:43]
	v_mfma_f32_16x16x32_bf16 v[36:39], v[138:141], v[202:205], v[36:39]
	v_mfma_f32_16x16x32_bf16 v[24:27], v[150:153], v[202:205], v[24:27]
	v_mfma_f32_16x16x32_bf16 v[20:23], v[138:141], v[224:227], v[20:23]
	v_mfma_f32_16x16x32_bf16 v[8:11], v[150:153], v[224:227], v[8:11]
	v_mfma_f32_16x16x32_bf16 v[60:63], v[146:149], v[178:181], v[60:63]
	v_mfma_f32_16x16x32_bf16 v[56:59], v[154:157], v[178:181], v[56:59]
	v_mfma_f32_16x16x32_bf16 v[52:55], v[146:149], v[198:201], v[52:55]
	v_mfma_f32_16x16x32_bf16 v[40:43], v[154:157], v[198:201], v[40:43]
	v_mfma_f32_16x16x32_bf16 v[36:39], v[146:149], v[206:209], v[36:39]
	v_mfma_f32_16x16x32_bf16 v[24:27], v[154:157], v[206:209], v[24:27]
	v_mfma_f32_16x16x32_bf16 v[20:23], v[146:149], v[228:231], v[20:23]
	v_mfma_f32_16x16x32_bf16 v[8:11], v[154:157], v[228:231], v[8:11]
	s_setprio 0
	s_setprio 1
	v_mfma_f32_16x16x32_bf16 v[48:51], v[158:161], v[174:177], v[48:51]
	v_mfma_f32_16x16x32_bf16 v[44:47], v[166:169], v[174:177], v[44:47]
	v_mfma_f32_16x16x32_bf16 v[32:35], v[158:161], v[194:197], v[32:35]
	v_mfma_f32_16x16x32_bf16 v[28:31], v[166:169], v[194:197], v[28:31]
	v_mfma_f32_16x16x32_bf16 v[16:19], v[158:161], v[202:205], v[16:19]
	v_mfma_f32_16x16x32_bf16 v[12:15], v[166:169], v[202:205], v[12:15]
	v_mfma_f32_16x16x32_bf16 v[4:7], v[158:161], v[224:227], v[4:7]
	v_mfma_f32_16x16x32_bf16 v[0:3], v[166:169], v[224:227], v[0:3]
	v_mfma_f32_16x16x32_bf16 v[48:51], v[162:165], v[178:181], v[48:51]
	v_mfma_f32_16x16x32_bf16 v[44:47], v[170:173], v[178:181], v[44:47]
	v_mfma_f32_16x16x32_bf16 v[32:35], v[162:165], v[198:201], v[32:35]
	v_mfma_f32_16x16x32_bf16 v[28:31], v[170:173], v[198:201], v[28:31]
	v_mfma_f32_16x16x32_bf16 v[16:19], v[162:165], v[206:209], v[16:19]
	v_mfma_f32_16x16x32_bf16 v[12:15], v[170:173], v[206:209], v[12:15]
	v_mfma_f32_16x16x32_bf16 v[4:7], v[162:165], v[228:231], v[4:7]
	v_mfma_f32_16x16x32_bf16 v[0:3], v[170:173], v[228:231], v[0:3]
	s_setprio 0
	s_barrier
	s_add_i32 s78, s78, 2
	s_add_u32 s30, s30, 0x100
	s_addc_u32 s31, s31, 0
	s_add_u32 s62, s62, 0x100
	s_addc_u32 s63, s63, 0
	s_cmp_gt_u32 s78, 29
	s_cbranch_scc0 .LBB0_805
	s_and_b64 vcc, exec, s[6:7]
	s_cbranch_vccz .LBB0_808
	s_barrier

.LBB0_842:
	s_add_u32 s28, s30, 0xfffc0080
	s_addc_u32 s29, s31, -1
	s_add_i32 s42, 0, 0x10000
	s_cmp_eq_u32 s60, 12
	s_cselect_b32 s45, s9, s29
	s_cselect_b32 s44, s11, s28
	s_cselect_b32 s41, s36, s59
	s_cselect_b32 s40, s37, s58
	s_add_i32 s43, 0, 0x14000
	v_add_u32_e32 v154, s42, v147
	v_add_u32_e32 v170, s43, v147
	ds_read_b128 v[138:141], v154
	ds_read_b128 v[142:145], v154 offset:1024
	ds_read_b128 v[150:153], v154 offset:2048
	ds_read_b128 v[154:157], v154 offset:3072
	ds_read_b128 v[158:161], v170
	ds_read_b128 v[162:165], v170 offset:1024
	ds_read_b128 v[166:169], v170 offset:2048
	ds_read_b128 v[170:173], v170 offset:3072
	s_add_i32 m0, s21, 0xc000
	ds_read_b128 v[174:177], v149
	ds_read_b128 v[178:181], v149 offset:1024
	ds_read_b128 v[194:197], v149 offset:2048
	ds_read_b128 v[198:201], v149 offset:3072
	ds_read_b128 v[202:205], v149 offset:4096
	ds_read_b128 v[206:209], v149 offset:5120
	ds_read_b128 v[224:227], v149 offset:6144
	ds_read_b128 v[228:231], v149 offset:7168
	global_load_lds_dwordx4 v134, s[30:31]
	s_add_i32 m0, s21, 0xe000
	s_nop 0
	global_load_lds_dwordx4 v136, s[30:31]
	s_waitcnt vmcnt(8)
	s_waitcnt lgkmcnt(0)
	s_barrier
	s_setprio 1
	s_waitcnt lgkmcnt(0)
	v_mfma_f32_16x16x32_bf16 v[124:127], v[138:141], v[174:177], v[124:127]
	v_mfma_f32_16x16x32_bf16 v[120:123], v[150:153], v[174:177], v[120:123]
	v_mfma_f32_16x16x32_bf16 v[108:111], v[138:141], v[194:197], v[108:111]
	v_mfma_f32_16x16x32_bf16 v[104:107], v[150:153], v[194:197], v[104:107]
	v_mfma_f32_16x16x32_bf16 v[92:95], v[138:141], v[202:205], v[92:95]
	v_mfma_f32_16x16x32_bf16 v[88:91], v[150:153], v[202:205], v[88:91]
	v_mfma_f32_16x16x32_bf16 v[76:79], v[138:141], v[224:227], v[76:79]
	v_mfma_f32_16x16x32_bf16 v[72:75], v[150:153], v[224:227], v[72:75]
	v_mfma_f32_16x16x32_bf16 v[124:127], v[142:145], v[178:181], v[124:127]
	v_mfma_f32_16x16x32_bf16 v[120:123], v[154:157], v[178:181], v[120:123]
	v_mfma_f32_16x16x32_bf16 v[108:111], v[142:145], v[198:201], v[108:111]
	v_mfma_f32_16x16x32_bf16 v[104:107], v[154:157], v[198:201], v[104:107]
	v_mfma_f32_16x16x32_bf16 v[92:95], v[142:145], v[206:209], v[92:95]
	v_mfma_f32_16x16x32_bf16 v[88:91], v[154:157], v[206:209], v[88:91]
	v_mfma_f32_16x16x32_bf16 v[76:79], v[142:145], v[228:231], v[76:79]
	v_mfma_f32_16x16x32_bf16 v[72:75], v[154:157], v[228:231], v[72:75]
	s_setprio 0
	s_setprio 1
	v_mfma_f32_16x16x32_bf16 v[116:119], v[158:161], v[174:177], v[116:119]
	v_mfma_f32_16x16x32_bf16 v[112:115], v[166:169], v[174:177], v[112:115]
	v_mfma_f32_16x16x32_bf16 v[100:103], v[158:161], v[194:197], v[100:103]
	v_mfma_f32_16x16x32_bf16 v[96:99], v[166:169], v[194:197], v[96:99]
	v_mfma_f32_16x16x32_bf16 v[84:87], v[158:161], v[202:205], v[84:87]
	v_mfma_f32_16x16x32_bf16 v[80:83], v[166:169], v[202:205], v[80:83]
	v_mfma_f32_16x16x32_bf16 v[68:71], v[158:161], v[224:227], v[68:71]
	v_mfma_f32_16x16x32_bf16 v[64:67], v[166:169], v[224:227], v[64:67]
	v_mfma_f32_16x16x32_bf16 v[116:119], v[162:165], v[178:181], v[116:119]
	v_mfma_f32_16x16x32_bf16 v[112:115], v[170:173], v[178:181], v[112:115]
	v_mfma_f32_16x16x32_bf16 v[100:103], v[162:165], v[198:201], v[100:103]
	v_mfma_f32_16x16x32_bf16 v[96:99], v[170:173], v[198:201], v[96:99]
	v_mfma_f32_16x16x32_bf16 v[84:87], v[162:165], v[206:209], v[84:87]
	v_mfma_f32_16x16x32_bf16 v[80:83], v[170:173], v[206:209], v[80:83]
	v_mfma_f32_16x16x32_bf16 v[68:71], v[162:165], v[228:231], v[68:71]
	v_mfma_f32_16x16x32_bf16 v[64:67], v[170:173], v[228:231], v[64:67]
	s_setprio 0
	s_barrier
	s_add_i32 s28, s42, s20
	v_lshl_add_u64 v[182:183], s[40:41], 0, v[184:185]
	s_mov_b32 m0, s28
	ds_read_b128 v[174:177], v149 offset:16384
	ds_read_b128 v[178:181], v149 offset:17408
	ds_read_b128 v[194:197], v149 offset:18432
	ds_read_b128 v[198:201], v149 offset:19456
	ds_read_b128 v[202:205], v149 offset:20480
	ds_read_b128 v[206:209], v149 offset:21504
	ds_read_b128 v[224:227], v149 offset:22528
	ds_read_b128 v[228:231], v149 offset:23552
	global_load_lds_dwordx4 v[182:183], off
	s_add_i32 m0, s28, 0x2000
	s_add_u32 s28, s40, 0x40000
	v_lshl_add_u64 v[210:211], s[40:41], 0, v[128:129]
	s_addc_u32 s29, s41, 0
	s_add_i32 s42, s43, s20
	global_load_lds_dwordx4 v128, s[40:41]
	v_lshl_add_u64 v[216:217], s[28:29], 0, v[184:185]
	s_mov_b32 m0, s42
	s_nop 0
	global_load_lds_dwordx4 v[216:217], off
	s_add_i32 m0, s42, 0x2000
	s_nop 0
	global_load_lds_dwordx4 v128, s[28:29]
	s_mov_b32 m0, s21
	s_nop 0
	global_load_lds_dwordx4 v132, s[44:45]
	s_mov_b32 m0, s26
	s_nop 0
	global_load_lds_dwordx4 v130, s[44:45]
	s_waitcnt vmcnt(8)
	s_waitcnt lgkmcnt(0)
	s_barrier
	s_setprio 1
	s_waitcnt lgkmcnt(0)
	v_mfma_f32_16x16x32_bf16 v[60:63], v[138:141], v[174:177], v[60:63]
	v_mfma_f32_16x16x32_bf16 v[56:59], v[150:153], v[174:177], v[56:59]
	v_mfma_f32_16x16x32_bf16 v[44:47], v[138:141], v[194:197], v[44:47]
	v_mfma_f32_16x16x32_bf16 v[40:43], v[150:153], v[194:197], v[40:43]
	v_mfma_f32_16x16x32_bf16 v[28:31], v[138:141], v[202:205], v[28:31]
	v_mfma_f32_16x16x32_bf16 v[24:27], v[150:153], v[202:205], v[24:27]
	v_mfma_f32_16x16x32_bf16 v[12:15], v[138:141], v[224:227], v[12:15]
	v_mfma_f32_16x16x32_bf16 v[8:11], v[150:153], v[224:227], v[8:11]
	v_mfma_f32_16x16x32_bf16 v[60:63], v[142:145], v[178:181], v[60:63]
	v_mfma_f32_16x16x32_bf16 v[56:59], v[154:157], v[178:181], v[56:59]
	v_mfma_f32_16x16x32_bf16 v[44:47], v[142:145], v[198:201], v[44:47]
	v_mfma_f32_16x16x32_bf16 v[40:43], v[154:157], v[198:201], v[40:43]
	v_mfma_f32_16x16x32_bf16 v[28:31], v[142:145], v[206:209], v[28:31]
	v_mfma_f32_16x16x32_bf16 v[24:27], v[154:157], v[206:209], v[24:27]
	v_mfma_f32_16x16x32_bf16 v[12:15], v[142:145], v[228:231], v[12:15]
	v_mfma_f32_16x16x32_bf16 v[8:11], v[154:157], v[228:231], v[8:11]
	s_setprio 0
	s_setprio 1
	v_mfma_f32_16x16x32_bf16 v[52:55], v[158:161], v[174:177], v[52:55]
	v_mfma_f32_16x16x32_bf16 v[48:51], v[166:169], v[174:177], v[48:51]
	v_mfma_f32_16x16x32_bf16 v[36:39], v[158:161], v[194:197], v[36:39]
	v_mfma_f32_16x16x32_bf16 v[32:35], v[166:169], v[194:197], v[32:35]
	v_mfma_f32_16x16x32_bf16 v[20:23], v[158:161], v[202:205], v[20:23]
	v_mfma_f32_16x16x32_bf16 v[16:19], v[166:169], v[202:205], v[16:19]
	v_mfma_f32_16x16x32_bf16 v[4:7], v[158:161], v[224:227], v[4:7]
	v_mfma_f32_16x16x32_bf16 v[0:3], v[166:169], v[224:227], v[0:3]
	v_mfma_f32_16x16x32_bf16 v[52:55], v[162:165], v[178:181], v[52:55]
	v_mfma_f32_16x16x32_bf16 v[48:51], v[170:173], v[178:181], v[48:51]
	v_mfma_f32_16x16x32_bf16 v[36:39], v[162:165], v[198:201], v[36:39]
	v_mfma_f32_16x16x32_bf16 v[32:35], v[170:173], v[198:201], v[32:35]
	v_mfma_f32_16x16x32_bf16 v[20:23], v[162:165], v[206:209], v[20:23]
	v_mfma_f32_16x16x32_bf16 v[16:19], v[170:173], v[206:209], v[16:19]
	v_mfma_f32_16x16x32_bf16 v[4:7], v[162:165], v[228:231], v[4:7]
	v_mfma_f32_16x16x32_bf16 v[0:3], v[170:173], v[228:231], v[0:3]
	s_setprio 0
	s_barrier
	s_add_i32 s42, 0, 0x18000
	s_add_i32 s43, 0, 0x1c000
	v_add_u32_e32 v154, s42, v147
	v_add_u32_e32 v170, s43, v147
	ds_read_b128 v[138:141], v154
	ds_read_b128 v[142:145], v154 offset:1024
	ds_read_b128 v[150:153], v154 offset:2048
	ds_read_b128 v[154:157], v154 offset:3072
	ds_read_b128 v[158:161], v170
	ds_read_b128 v[162:165], v170 offset:1024
	ds_read_b128 v[166:169], v170 offset:2048
	ds_read_b128 v[170:173], v170 offset:3072
	s_add_u32 s28, s44, 0x40000
	s_addc_u32 s29, s45, 0
	s_mov_b32 m0, s27
	ds_read_b128 v[174:177], v149 offset:32768
	ds_read_b128 v[178:181], v149 offset:33792
	ds_read_b128 v[194:197], v149 offset:34816
	ds_read_b128 v[198:201], v149 offset:35840
	ds_read_b128 v[202:205], v149 offset:36864
	ds_read_b128 v[206:209], v149 offset:37888
	ds_read_b128 v[224:227], v149 offset:38912
	ds_read_b128 v[228:231], v149 offset:39936
	global_load_lds_dwordx4 v132, s[28:29]
	s_mov_b32 m0, s46
	s_nop 0
	global_load_lds_dwordx4 v130, s[28:29]
	s_waitcnt vmcnt(8)
	s_waitcnt lgkmcnt(0)
	s_barrier
	s_setprio 1
	s_waitcnt lgkmcnt(0)
	v_mfma_f32_16x16x32_bf16 v[124:127], v[138:141], v[174:177], v[124:127]
	v_mfma_f32_16x16x32_bf16 v[120:123], v[150:153], v[174:177], v[120:123]
	v_mfma_f32_16x16x32_bf16 v[108:111], v[138:141], v[194:197], v[108:111]
	v_mfma_f32_16x16x32_bf16 v[104:107], v[150:153], v[194:197], v[104:107]
	v_mfma_f32_16x16x32_bf16 v[92:95], v[138:141], v[202:205], v[92:95]
	v_mfma_f32_16x16x32_bf16 v[88:91], v[150:153], v[202:205], v[88:91]
	v_mfma_f32_16x16x32_bf16 v[76:79], v[138:141], v[224:227], v[76:79]
	v_mfma_f32_16x16x32_bf16 v[72:75], v[150:153], v[224:227], v[72:75]
	v_mfma_f32_16x16x32_bf16 v[124:127], v[142:145], v[178:181], v[124:127]
	v_mfma_f32_16x16x32_bf16 v[120:123], v[154:157], v[178:181], v[120:123]
	v_mfma_f32_16x16x32_bf16 v[108:111], v[142:145], v[198:201], v[108:111]
	v_mfma_f32_16x16x32_bf16 v[104:107], v[154:157], v[198:201], v[104:107]
	v_mfma_f32_16x16x32_bf16 v[92:95], v[142:145], v[206:209], v[92:95]
	v_mfma_f32_16x16x32_bf16 v[88:91], v[154:157], v[206:209], v[88:91]
	v_mfma_f32_16x16x32_bf16 v[76:79], v[142:145], v[228:231], v[76:79]
	v_mfma_f32_16x16x32_bf16 v[72:75], v[154:157], v[228:231], v[72:75]
	s_setprio 0
	s_setprio 1
	v_mfma_f32_16x16x32_bf16 v[116:119], v[158:161], v[174:177], v[116:119]
	v_mfma_f32_16x16x32_bf16 v[112:115], v[166:169], v[174:177], v[112:115]
	v_mfma_f32_16x16x32_bf16 v[100:103], v[158:161], v[194:197], v[100:103]
	v_mfma_f32_16x16x32_bf16 v[96:99], v[166:169], v[194:197], v[96:99]
	v_mfma_f32_16x16x32_bf16 v[84:87], v[158:161], v[202:205], v[84:87]
	v_mfma_f32_16x16x32_bf16 v[80:83], v[166:169], v[202:205], v[80:83]
	v_mfma_f32_16x16x32_bf16 v[68:71], v[158:161], v[224:227], v[68:71]
	v_mfma_f32_16x16x32_bf16 v[64:67], v[166:169], v[224:227], v[64:67]
	v_mfma_f32_16x16x32_bf16 v[116:119], v[162:165], v[178:181], v[116:119]
	v_mfma_f32_16x16x32_bf16 v[112:115], v[170:173], v[178:181], v[112:115]
	v_mfma_f32_16x16x32_bf16 v[100:103], v[162:165], v[198:201], v[100:103]
	v_mfma_f32_16x16x32_bf16 v[96:99], v[170:173], v[198:201], v[96:99]
	v_mfma_f32_16x16x32_bf16 v[84:87], v[162:165], v[206:209], v[84:87]
	v_mfma_f32_16x16x32_bf16 v[80:83], v[170:173], v[206:209], v[80:83]
	v_mfma_f32_16x16x32_bf16 v[68:71], v[162:165], v[228:231], v[68:71]
	v_mfma_f32_16x16x32_bf16 v[64:67], v[170:173], v[228:231], v[64:67]
	s_setprio 0
	s_barrier
	s_add_i32 s28, s42, s20
	v_lshl_add_u64 v[182:183], v[182:183], 0, s[68:69]
	s_mov_b32 m0, s28
	ds_read_b128 v[174:177], v149 offset:49152
	ds_read_b128 v[178:181], v149 offset:50176
	ds_read_b128 v[194:197], v149 offset:51200
	ds_read_b128 v[198:201], v149 offset:52224
	ds_read_b128 v[202:205], v149 offset:53248
	ds_read_b128 v[206:209], v149 offset:54272
	ds_read_b128 v[224:227], v149 offset:55296
	ds_read_b128 v[228:231], v149 offset:56320
	global_load_lds_dwordx4 v[182:183], off
	s_add_i32 m0, s28, 0x2000
	s_add_u32 s28, s40, 0x40080
	v_lshl_add_u64 v[182:183], v[210:211], 0, s[68:69]
	s_addc_u32 s29, s41, 0
	s_add_i32 s40, s43, s20
	global_load_lds_dwordx4 v[182:183], off
	v_lshl_add_u64 v[182:183], s[28:29], 0, v[184:185]
	s_mov_b32 m0, s40
	s_nop 0
	global_load_lds_dwordx4 v[182:183], off
	s_add_i32 m0, s40, 0x2000
	s_nop 0
	global_load_lds_dwordx4 v128, s[28:29]
	s_add_i32 m0, s47, 0xffffff80
	s_nop 0
	global_load_lds_dwordx4 v132, s[44:45] offset:128
	s_add_i32 m0, s50, 0xffffff80
	s_nop 0
	global_load_lds_dwordx4 v130, s[44:45] offset:128
	s_waitcnt vmcnt(8)
	s_waitcnt lgkmcnt(0)
	s_barrier
	s_setprio 1
	s_waitcnt lgkmcnt(0)
	v_mfma_f32_16x16x32_bf16 v[60:63], v[138:141], v[174:177], v[60:63]
	v_mfma_f32_16x16x32_bf16 v[56:59], v[150:153], v[174:177], v[56:59]
	v_mfma_f32_16x16x32_bf16 v[44:47], v[138:141], v[194:197], v[44:47]
	v_mfma_f32_16x16x32_bf16 v[40:43], v[150:153], v[194:197], v[40:43]
	v_mfma_f32_16x16x32_bf16 v[28:31], v[138:141], v[202:205], v[28:31]
	v_mfma_f32_16x16x32_bf16 v[24:27], v[150:153], v[202:205], v[24:27]
	v_mfma_f32_16x16x32_bf16 v[12:15], v[138:141], v[224:227], v[12:15]
	v_mfma_f32_16x16x32_bf16 v[8:11], v[150:153], v[224:227], v[8:11]
	v_mfma_f32_16x16x32_bf16 v[60:63], v[142:145], v[178:181], v[60:63]
	v_mfma_f32_16x16x32_bf16 v[56:59], v[154:157], v[178:181], v[56:59]
	v_mfma_f32_16x16x32_bf16 v[44:47], v[142:145], v[198:201], v[44:47]
	v_mfma_f32_16x16x32_bf16 v[40:43], v[154:157], v[198:201], v[40:43]
	v_mfma_f32_16x16x32_bf16 v[28:31], v[142:145], v[206:209], v[28:31]
	v_mfma_f32_16x16x32_bf16 v[24:27], v[154:157], v[206:209], v[24:27]
	v_mfma_f32_16x16x32_bf16 v[12:15], v[142:145], v[228:231], v[12:15]
	v_mfma_f32_16x16x32_bf16 v[8:11], v[154:157], v[228:231], v[8:11]
	s_setprio 0
	s_setprio 1
	v_mfma_f32_16x16x32_bf16 v[52:55], v[158:161], v[174:177], v[52:55]
	v_mfma_f32_16x16x32_bf16 v[48:51], v[166:169], v[174:177], v[48:51]
	v_mfma_f32_16x16x32_bf16 v[36:39], v[158:161], v[194:197], v[36:39]
	v_mfma_f32_16x16x32_bf16 v[32:35], v[166:169], v[194:197], v[32:35]
	v_mfma_f32_16x16x32_bf16 v[20:23], v[158:161], v[202:205], v[20:23]
	v_mfma_f32_16x16x32_bf16 v[16:19], v[166:169], v[202:205], v[16:19]
	v_mfma_f32_16x16x32_bf16 v[4:7], v[158:161], v[224:227], v[4:7]
	v_mfma_f32_16x16x32_bf16 v[0:3], v[166:169], v[224:227], v[0:3]
	v_mfma_f32_16x16x32_bf16 v[52:55], v[162:165], v[178:181], v[52:55]
	v_mfma_f32_16x16x32_bf16 v[48:51], v[170:173], v[178:181], v[48:51]
	v_mfma_f32_16x16x32_bf16 v[36:39], v[162:165], v[198:201], v[36:39]
	v_mfma_f32_16x16x32_bf16 v[32:35], v[170:173], v[198:201], v[32:35]
	v_mfma_f32_16x16x32_bf16 v[20:23], v[162:165], v[206:209], v[20:23]
	v_mfma_f32_16x16x32_bf16 v[16:19], v[170:173], v[206:209], v[16:19]
	v_mfma_f32_16x16x32_bf16 v[4:7], v[162:165], v[228:231], v[4:7]
	v_mfma_f32_16x16x32_bf16 v[0:3], v[170:173], v[228:231], v[0:3]
	s_setprio 0
	s_barrier
	s_add_i32 s60, s60, 2
	s_add_u32 s30, s30, 0x100
	s_addc_u32 s31, s31, 0
	s_add_u32 s58, s58, 0x100
	s_addc_u32 s59, s59, 0
	s_cmp_gt_u32 s60, 13
	s_cbranch_scc0 .LBB0_842
	s_and_b64 vcc, exec, s[6:7]
	s_cbranch_vccz .LBB0_845
	s_barrier

.LBB0_991:
	s_add_u32 s28, s40, 0xfff80080
	s_addc_u32 s29, s41, -1
	s_add_i32 s48, 0, 0x10000
	s_cmp_eq_u32 s79, 28
	s_cselect_b32 s45, s11, s29
	s_cselect_b32 s44, s13, s28
	s_cselect_b32 s43, s60, s63
	s_cselect_b32 s42, s61, s62
	s_add_i32 s49, 0, 0x14000
	s_waitcnt vmcnt(0)
	v_add_u32_e32 v60, s48, v169
	v_add_u32_e32 v166, s49, v169
	ds_read_b128 v[40:43], v60
	ds_read_b128 v[44:47], v60 offset:1024
	ds_read_b128 v[56:59], v60 offset:2048
	ds_read_b128 v[60:63], v60 offset:3072
	ds_read_b128 v[144:147], v166
	ds_read_b128 v[148:151], v166 offset:1024
	ds_read_b128 v[162:165], v166 offset:2048
	ds_read_b128 v[172:175], v166 offset:3072
	s_add_i32 m0, s26, 0xc000
	ds_read_b128 v[176:179], v171
	ds_read_b128 v[180:183], v171 offset:1024
	ds_read_b128 v[194:197], v171 offset:2048
	ds_read_b128 v[198:201], v171 offset:3072
	ds_read_b128 v[202:205], v171 offset:4096
	ds_read_b128 v[206:209], v171 offset:5120
	ds_read_b128 v[224:227], v171 offset:6144
	ds_read_b128 v[228:231], v171 offset:7168
	global_load_lds_dwordx4 v158, s[40:41]
	s_add_i32 m0, s26, 0xe000
	s_nop 0
	global_load_lds_dwordx4 v160, s[40:41]
	s_waitcnt vmcnt(8)
	s_waitcnt lgkmcnt(0)
	s_barrier
	s_setprio 1
	s_waitcnt lgkmcnt(0)
	v_mfma_f32_16x16x32_bf16 v[140:143], v[40:43], v[176:179], v[140:143]
	v_mfma_f32_16x16x32_bf16 v[136:139], v[56:59], v[176:179], v[136:139]
	v_mfma_f32_16x16x32_bf16 v[124:127], v[40:43], v[194:197], v[124:127]
	v_mfma_f32_16x16x32_bf16 v[120:123], v[56:59], v[194:197], v[120:123]
	v_mfma_f32_16x16x32_bf16 v[108:111], v[40:43], v[202:205], v[108:111]
	v_mfma_f32_16x16x32_bf16 v[104:107], v[56:59], v[202:205], v[104:107]
	v_mfma_f32_16x16x32_bf16 v[92:95], v[40:43], v[224:227], v[92:95]
	v_mfma_f32_16x16x32_bf16 v[88:91], v[56:59], v[224:227], v[88:91]
	v_mfma_f32_16x16x32_bf16 v[140:143], v[44:47], v[180:183], v[140:143]
	v_mfma_f32_16x16x32_bf16 v[136:139], v[60:63], v[180:183], v[136:139]
	v_mfma_f32_16x16x32_bf16 v[124:127], v[44:47], v[198:201], v[124:127]
	v_mfma_f32_16x16x32_bf16 v[120:123], v[60:63], v[198:201], v[120:123]
	v_mfma_f32_16x16x32_bf16 v[108:111], v[44:47], v[206:209], v[108:111]
	v_mfma_f32_16x16x32_bf16 v[104:107], v[60:63], v[206:209], v[104:107]
	v_mfma_f32_16x16x32_bf16 v[92:95], v[44:47], v[228:231], v[92:95]
	v_mfma_f32_16x16x32_bf16 v[88:91], v[60:63], v[228:231], v[88:91]
	s_setprio 0
	s_setprio 1
	v_mfma_f32_16x16x32_bf16 v[132:135], v[144:147], v[176:179], v[132:135]
	v_mfma_f32_16x16x32_bf16 v[128:131], v[162:165], v[176:179], v[128:131]
	v_mfma_f32_16x16x32_bf16 v[116:119], v[144:147], v[194:197], v[116:119]
	v_mfma_f32_16x16x32_bf16 v[112:115], v[162:165], v[194:197], v[112:115]
	v_mfma_f32_16x16x32_bf16 v[100:103], v[144:147], v[202:205], v[100:103]
	v_mfma_f32_16x16x32_bf16 v[96:99], v[162:165], v[202:205], v[96:99]
	v_mfma_f32_16x16x32_bf16 v[84:87], v[144:147], v[224:227], v[84:87]
	v_mfma_f32_16x16x32_bf16 v[80:83], v[162:165], v[224:227], v[80:83]
	v_mfma_f32_16x16x32_bf16 v[132:135], v[148:151], v[180:183], v[132:135]
	v_mfma_f32_16x16x32_bf16 v[128:131], v[172:175], v[180:183], v[128:131]
	v_mfma_f32_16x16x32_bf16 v[116:119], v[148:151], v[198:201], v[116:119]
	v_mfma_f32_16x16x32_bf16 v[112:115], v[172:175], v[198:201], v[112:115]
	v_mfma_f32_16x16x32_bf16 v[100:103], v[148:151], v[206:209], v[100:103]
	v_mfma_f32_16x16x32_bf16 v[96:99], v[172:175], v[206:209], v[96:99]
	v_mfma_f32_16x16x32_bf16 v[84:87], v[148:151], v[228:231], v[84:87]
	v_mfma_f32_16x16x32_bf16 v[80:83], v[172:175], v[228:231], v[80:83]
	s_setprio 0
	s_barrier
	s_add_i32 s28, s48, s46
	v_lshl_add_u64 v[166:167], s[42:43], 0, v[184:185]
	s_mov_b32 m0, s28
	ds_read_b128 v[176:179], v171 offset:16384
	ds_read_b128 v[180:183], v171 offset:17408
	ds_read_b128 v[194:197], v171 offset:18432
	ds_read_b128 v[198:201], v171 offset:19456
	ds_read_b128 v[202:205], v171 offset:20480
	ds_read_b128 v[206:209], v171 offset:21504
	ds_read_b128 v[224:227], v171 offset:22528
	ds_read_b128 v[228:231], v171 offset:23552
	global_load_lds_dwordx4 v[166:167], off
	s_add_i32 m0, s28, 0x2000
	s_add_u32 s28, s42, 0x80000
	v_lshl_add_u64 v[210:211], s[42:43], 0, v[152:153]
	s_addc_u32 s29, s43, 0
	s_add_i32 s48, s49, s46
	global_load_lds_dwordx4 v152, s[42:43]
	v_lshl_add_u64 v[216:217], s[28:29], 0, v[184:185]
	s_mov_b32 m0, s48
	v_lshl_add_u64 v[218:219], s[44:45], 0, v[154:155]
	global_load_lds_dwordx4 v[216:217], off
	s_add_i32 m0, s48, 0x2000
	s_nop 0
	global_load_lds_dwordx4 v152, s[28:29]
	s_mov_b32 m0, s26
	s_nop 0
	global_load_lds_dwordx4 v156, s[44:45]
	s_mov_b32 m0, s27
	s_nop 0
	global_load_lds_dwordx4 v154, s[44:45]
	s_waitcnt vmcnt(8)
	s_waitcnt lgkmcnt(0)
	s_barrier
	s_setprio 1
	s_waitcnt lgkmcnt(0)
	v_mfma_f32_16x16x32_bf16 v[76:79], v[40:43], v[176:179], v[76:79]
	v_mfma_f32_16x16x32_bf16 v[72:75], v[56:59], v[176:179], v[72:75]
	v_mfma_f32_16x16x32_bf16 v[52:55], v[40:43], v[194:197], v[52:55]
	v_mfma_f32_16x16x32_bf16 v[48:51], v[56:59], v[194:197], v[48:51]
	v_mfma_f32_16x16x32_bf16 v[28:31], v[40:43], v[202:205], v[28:31]
	v_mfma_f32_16x16x32_bf16 v[24:27], v[56:59], v[202:205], v[24:27]
	v_mfma_f32_16x16x32_bf16 v[12:15], v[40:43], v[224:227], v[12:15]
	v_mfma_f32_16x16x32_bf16 v[8:11], v[56:59], v[224:227], v[8:11]
	v_mfma_f32_16x16x32_bf16 v[76:79], v[44:47], v[180:183], v[76:79]
	v_mfma_f32_16x16x32_bf16 v[72:75], v[60:63], v[180:183], v[72:75]
	v_mfma_f32_16x16x32_bf16 v[52:55], v[44:47], v[198:201], v[52:55]
	v_mfma_f32_16x16x32_bf16 v[48:51], v[60:63], v[198:201], v[48:51]
	v_mfma_f32_16x16x32_bf16 v[28:31], v[44:47], v[206:209], v[28:31]
	v_mfma_f32_16x16x32_bf16 v[24:27], v[60:63], v[206:209], v[24:27]
	v_mfma_f32_16x16x32_bf16 v[12:15], v[44:47], v[228:231], v[12:15]
	v_mfma_f32_16x16x32_bf16 v[8:11], v[60:63], v[228:231], v[8:11]
	s_setprio 0
	s_setprio 1
	v_mfma_f32_16x16x32_bf16 v[36:39], v[144:147], v[194:197], v[36:39]
	v_mfma_f32_16x16x32_bf16 v[32:35], v[162:165], v[194:197], v[32:35]
	v_mfma_f32_16x16x32_bf16 v[20:23], v[144:147], v[202:205], v[20:23]
	v_mfma_f32_16x16x32_bf16 v[16:19], v[162:165], v[202:205], v[16:19]
	v_mfma_f32_16x16x32_bf16 v[4:7], v[144:147], v[224:227], v[4:7]
	v_mfma_f32_16x16x32_bf16 v[0:3], v[162:165], v[224:227], v[0:3]
	v_mfma_f32_16x16x32_bf16 v[40:43], v[144:147], v[176:179], v[68:71]
	v_mfma_f32_16x16x32_bf16 v[44:47], v[162:165], v[176:179], v[64:67]
	v_mfma_f32_16x16x32_bf16 v[36:39], v[148:151], v[198:201], v[36:39]
	v_mfma_f32_16x16x32_bf16 v[32:35], v[172:175], v[198:201], v[32:35]
	v_mfma_f32_16x16x32_bf16 v[20:23], v[148:151], v[206:209], v[20:23]
	v_mfma_f32_16x16x32_bf16 v[16:19], v[172:175], v[206:209], v[16:19]
	v_mfma_f32_16x16x32_bf16 v[4:7], v[148:151], v[228:231], v[4:7]
	v_mfma_f32_16x16x32_bf16 v[0:3], v[172:175], v[228:231], v[0:3]
	v_mfma_f32_16x16x32_bf16 v[40:43], v[148:151], v[180:183], v[40:43]
	v_mfma_f32_16x16x32_bf16 v[44:47], v[172:175], v[180:183], v[44:47]
	s_setprio 0
	s_barrier
	s_add_i32 s48, 0, 0x18000
	s_add_i32 s49, 0, 0x1c000
	v_add_u32_e32 v68, s48, v169
	v_add_u32_e32 v172, s49, v169
	ds_read_b128 v[56:59], v68
	ds_read_b128 v[60:63], v68 offset:1024
	ds_read_b128 v[64:67], v68 offset:2048
	ds_read_b128 v[68:71], v68 offset:3072
	ds_read_b128 v[144:147], v172
	ds_read_b128 v[148:151], v172 offset:1024
	ds_read_b128 v[162:165], v172 offset:2048
	ds_read_b128 v[172:175], v172 offset:3072
	s_add_u32 s28, s44, 0x80000
	s_addc_u32 s29, s45, 0
	s_mov_b32 m0, s47
	ds_read_b128 v[176:179], v171 offset:32768
	ds_read_b128 v[180:183], v171 offset:33792
	ds_read_b128 v[194:197], v171 offset:34816
	ds_read_b128 v[198:201], v171 offset:35840
	ds_read_b128 v[202:205], v171 offset:36864
	ds_read_b128 v[206:209], v171 offset:37888
	ds_read_b128 v[224:227], v171 offset:38912
	ds_read_b128 v[228:231], v171 offset:39936
	global_load_lds_dwordx4 v156, s[28:29]
	s_mov_b32 m0, s50
	s_nop 0
	global_load_lds_dwordx4 v154, s[28:29]
	s_waitcnt vmcnt(8)
	s_waitcnt lgkmcnt(0)
	s_barrier
	s_setprio 1
	s_waitcnt lgkmcnt(0)
	v_mfma_f32_16x16x32_bf16 v[140:143], v[56:59], v[176:179], v[140:143]
	v_mfma_f32_16x16x32_bf16 v[136:139], v[64:67], v[176:179], v[136:139]
	v_mfma_f32_16x16x32_bf16 v[124:127], v[56:59], v[194:197], v[124:127]
	v_mfma_f32_16x16x32_bf16 v[120:123], v[64:67], v[194:197], v[120:123]
	v_mfma_f32_16x16x32_bf16 v[108:111], v[56:59], v[202:205], v[108:111]
	v_mfma_f32_16x16x32_bf16 v[104:107], v[64:67], v[202:205], v[104:107]
	v_mfma_f32_16x16x32_bf16 v[92:95], v[56:59], v[224:227], v[92:95]
	v_mfma_f32_16x16x32_bf16 v[88:91], v[64:67], v[224:227], v[88:91]
	v_mfma_f32_16x16x32_bf16 v[140:143], v[60:63], v[180:183], v[140:143]
	v_mfma_f32_16x16x32_bf16 v[136:139], v[68:71], v[180:183], v[136:139]
	v_mfma_f32_16x16x32_bf16 v[124:127], v[60:63], v[198:201], v[124:127]
	v_mfma_f32_16x16x32_bf16 v[120:123], v[68:71], v[198:201], v[120:123]
	v_mfma_f32_16x16x32_bf16 v[108:111], v[60:63], v[206:209], v[108:111]
	v_mfma_f32_16x16x32_bf16 v[104:107], v[68:71], v[206:209], v[104:107]
	v_mfma_f32_16x16x32_bf16 v[92:95], v[60:63], v[228:231], v[92:95]
	v_mfma_f32_16x16x32_bf16 v[88:91], v[68:71], v[228:231], v[88:91]
	s_setprio 0
	s_setprio 1
	v_mfma_f32_16x16x32_bf16 v[132:135], v[144:147], v[176:179], v[132:135]
	v_mfma_f32_16x16x32_bf16 v[128:131], v[162:165], v[176:179], v[128:131]
	v_mfma_f32_16x16x32_bf16 v[116:119], v[144:147], v[194:197], v[116:119]
	v_mfma_f32_16x16x32_bf16 v[112:115], v[162:165], v[194:197], v[112:115]
	v_mfma_f32_16x16x32_bf16 v[100:103], v[144:147], v[202:205], v[100:103]
	v_mfma_f32_16x16x32_bf16 v[96:99], v[162:165], v[202:205], v[96:99]
	v_mfma_f32_16x16x32_bf16 v[84:87], v[144:147], v[224:227], v[84:87]
	v_mfma_f32_16x16x32_bf16 v[80:83], v[162:165], v[224:227], v[80:83]
	v_mfma_f32_16x16x32_bf16 v[132:135], v[148:151], v[180:183], v[132:135]
	v_mfma_f32_16x16x32_bf16 v[128:131], v[172:175], v[180:183], v[128:131]
	v_mfma_f32_16x16x32_bf16 v[116:119], v[148:151], v[198:201], v[116:119]
	v_mfma_f32_16x16x32_bf16 v[112:115], v[172:175], v[198:201], v[112:115]
	v_mfma_f32_16x16x32_bf16 v[100:103], v[148:151], v[206:209], v[100:103]
	v_mfma_f32_16x16x32_bf16 v[96:99], v[172:175], v[206:209], v[96:99]
	v_mfma_f32_16x16x32_bf16 v[84:87], v[148:151], v[228:231], v[84:87]
	v_mfma_f32_16x16x32_bf16 v[80:83], v[172:175], v[228:231], v[80:83]
	s_setprio 0
	s_barrier
	s_add_i32 s28, s48, s46
	v_lshl_add_u64 v[166:167], v[166:167], 0, s[68:69]
	s_mov_b32 m0, s28
	ds_read_b128 v[176:179], v171 offset:49152
	ds_read_b128 v[180:183], v171 offset:50176
	ds_read_b128 v[194:197], v171 offset:51200
	ds_read_b128 v[198:201], v171 offset:52224
	ds_read_b128 v[202:205], v171 offset:53248
	ds_read_b128 v[206:209], v171 offset:54272
	ds_read_b128 v[224:227], v171 offset:55296
	ds_read_b128 v[228:231], v171 offset:56320
	global_load_lds_dwordx4 v[166:167], off
	s_add_i32 m0, s28, 0x2000
	s_add_u32 s28, s42, 0x80080
	v_lshl_add_u64 v[166:167], v[210:211], 0, s[68:69]
	s_addc_u32 s29, s43, 0
	s_add_i32 s42, s49, s46
	global_load_lds_dwordx4 v[166:167], off
	v_lshl_add_u64 v[166:167], s[28:29], 0, v[184:185]
	s_mov_b32 m0, s42
	s_nop 0
	global_load_lds_dwordx4 v[166:167], off
	s_add_i32 m0, s42, 0x2000
	s_nop 0
	global_load_lds_dwordx4 v152, s[28:29]
	s_add_i32 m0, s53, 0xffffff80
	s_nop 0
	global_load_lds_dwordx4 v156, s[44:45] offset:128
	v_lshl_add_u64 v[166:167], v[218:219], 0, s[68:69]
	s_add_i32 m0, s58, 0xffffff80
	s_nop 0
	global_load_lds_dwordx4 v154, s[44:45] offset:128
	s_waitcnt vmcnt(8)
	s_waitcnt lgkmcnt(0)
	s_barrier
	s_setprio 1
	s_waitcnt lgkmcnt(0)
	v_mfma_f32_16x16x32_bf16 v[76:79], v[56:59], v[176:179], v[76:79]
	v_mfma_f32_16x16x32_bf16 v[72:75], v[64:67], v[176:179], v[72:75]
	v_mfma_f32_16x16x32_bf16 v[52:55], v[56:59], v[194:197], v[52:55]
	v_mfma_f32_16x16x32_bf16 v[48:51], v[64:67], v[194:197], v[48:51]
	v_mfma_f32_16x16x32_bf16 v[28:31], v[56:59], v[202:205], v[28:31]
	v_mfma_f32_16x16x32_bf16 v[24:27], v[64:67], v[202:205], v[24:27]
	v_mfma_f32_16x16x32_bf16 v[12:15], v[56:59], v[224:227], v[12:15]
	v_mfma_f32_16x16x32_bf16 v[8:11], v[64:67], v[224:227], v[8:11]
	v_mfma_f32_16x16x32_bf16 v[76:79], v[60:63], v[180:183], v[76:79]
	v_mfma_f32_16x16x32_bf16 v[72:75], v[68:71], v[180:183], v[72:75]
	v_mfma_f32_16x16x32_bf16 v[52:55], v[60:63], v[198:201], v[52:55]
	v_mfma_f32_16x16x32_bf16 v[48:51], v[68:71], v[198:201], v[48:51]
	v_mfma_f32_16x16x32_bf16 v[28:31], v[60:63], v[206:209], v[28:31]
	v_mfma_f32_16x16x32_bf16 v[24:27], v[68:71], v[206:209], v[24:27]
	v_mfma_f32_16x16x32_bf16 v[12:15], v[60:63], v[228:231], v[12:15]
	v_mfma_f32_16x16x32_bf16 v[8:11], v[68:71], v[228:231], v[8:11]
	s_setprio 0
	s_setprio 1
	v_mfma_f32_16x16x32_bf16 v[40:43], v[144:147], v[176:179], v[40:43]
	v_mfma_f32_16x16x32_bf16 v[68:71], v[148:151], v[180:183], v[40:43]
	v_mfma_f32_16x16x32_bf16 v[40:43], v[162:165], v[176:179], v[44:47]
	v_mfma_f32_16x16x32_bf16 v[36:39], v[144:147], v[194:197], v[36:39]
	v_mfma_f32_16x16x32_bf16 v[32:35], v[162:165], v[194:197], v[32:35]
	v_mfma_f32_16x16x32_bf16 v[20:23], v[144:147], v[202:205], v[20:23]
	v_mfma_f32_16x16x32_bf16 v[16:19], v[162:165], v[202:205], v[16:19]
	v_mfma_f32_16x16x32_bf16 v[4:7], v[144:147], v[224:227], v[4:7]
	v_mfma_f32_16x16x32_bf16 v[0:3], v[162:165], v[224:227], v[0:3]
	v_mfma_f32_16x16x32_bf16 v[64:67], v[172:175], v[180:183], v[40:43]
	v_mfma_f32_16x16x32_bf16 v[36:39], v[148:151], v[198:201], v[36:39]
	v_mfma_f32_16x16x32_bf16 v[32:35], v[172:175], v[198:201], v[32:35]
	v_mfma_f32_16x16x32_bf16 v[20:23], v[148:151], v[206:209], v[20:23]
	v_mfma_f32_16x16x32_bf16 v[16:19], v[172:175], v[206:209], v[16:19]
	v_mfma_f32_16x16x32_bf16 v[4:7], v[148:151], v[228:231], v[4:7]
	v_mfma_f32_16x16x32_bf16 v[0:3], v[172:175], v[228:231], v[0:3]
	s_setprio 0
	s_barrier
	s_add_i32 s79, s79, 2
	s_add_u32 s40, s40, 0x100
	s_addc_u32 s41, s41, 0
	s_add_u32 s62, s62, 0x100
	s_addc_u32 s63, s63, 0
	s_cmp_gt_u32 s79, 29
	s_cbranch_scc0 .LBB0_991
	s_and_b64 vcc, exec, s[8:9]
	s_cbranch_vccz .LBB0_994
	s_barrier

.LBB0_1419:
	s_add_u32 s28, s24, 0xfff80080
	s_addc_u32 s29, s25, -1
	s_add_i32 s48, 0, 0x10000
	s_cmp_eq_u32 s17, 28
	s_cselect_b32 s31, s9, s29
	s_cselect_b32 s30, s11, s28
	s_cselect_b64 vcc, -1, 0
	s_add_i32 s28, 0, 0x14000
	v_add_u32_e32 v164, s48, v147
	v_add_u32_e32 v180, s28, v147
	ds_read_b128 v[152:155], v164
	ds_read_b128 v[156:159], v164 offset:1024
	ds_read_b128 v[160:163], v164 offset:2048
	ds_read_b128 v[164:167], v164 offset:3072
	ds_read_b128 v[168:171], v180
	ds_read_b128 v[172:175], v180 offset:1024
	ds_read_b128 v[176:179], v180 offset:2048
	ds_read_b128 v[180:183], v180 offset:3072
	v_cndmask_b32_e32 v211, v145, v150, vcc
	v_cndmask_b32_e32 v210, v144, v151, vcc
	s_add_i32 m0, s19, 0xc000
	ds_read_b128 v[194:197], v149
	ds_read_b128 v[198:201], v149 offset:1024
	ds_read_b128 v[202:205], v149 offset:2048
	ds_read_b128 v[206:209], v149 offset:3072
	ds_read_b128 v[224:227], v149 offset:4096
	ds_read_b128 v[228:231], v149 offset:5120
	ds_read_b128 v[232:235], v149 offset:6144
	ds_read_b128 v[236:239], v149 offset:7168
	global_load_lds_dwordx4 v136, s[24:25]
	s_add_i32 m0, s19, 0xe000
	s_nop 0
	global_load_lds_dwordx4 v138, s[24:25]
	s_waitcnt vmcnt(8)
	s_waitcnt lgkmcnt(0)
	s_barrier
	s_setprio 1
	s_waitcnt lgkmcnt(0)
	v_mfma_f32_16x16x32_bf16 v[124:127], v[152:155], v[194:197], v[124:127]
	v_mfma_f32_16x16x32_bf16 v[116:119], v[160:163], v[194:197], v[116:119]
	v_mfma_f32_16x16x32_bf16 v[108:111], v[152:155], v[202:205], v[108:111]
	v_mfma_f32_16x16x32_bf16 v[100:103], v[160:163], v[202:205], v[100:103]
	v_mfma_f32_16x16x32_bf16 v[92:95], v[152:155], v[224:227], v[92:95]
	v_mfma_f32_16x16x32_bf16 v[84:87], v[160:163], v[224:227], v[84:87]
	v_mfma_f32_16x16x32_bf16 v[76:79], v[152:155], v[232:235], v[76:79]
	v_mfma_f32_16x16x32_bf16 v[68:71], v[160:163], v[232:235], v[68:71]
	v_mfma_f32_16x16x32_bf16 v[124:127], v[156:159], v[198:201], v[124:127]
	v_mfma_f32_16x16x32_bf16 v[116:119], v[164:167], v[198:201], v[116:119]
	v_mfma_f32_16x16x32_bf16 v[108:111], v[156:159], v[206:209], v[108:111]
	v_mfma_f32_16x16x32_bf16 v[100:103], v[164:167], v[206:209], v[100:103]
	v_mfma_f32_16x16x32_bf16 v[92:95], v[156:159], v[228:231], v[92:95]
	v_mfma_f32_16x16x32_bf16 v[84:87], v[164:167], v[228:231], v[84:87]
	v_mfma_f32_16x16x32_bf16 v[76:79], v[156:159], v[236:239], v[76:79]
	v_mfma_f32_16x16x32_bf16 v[68:71], v[164:167], v[236:239], v[68:71]
	s_setprio 0
	s_setprio 1
	v_mfma_f32_16x16x32_bf16 v[120:123], v[168:171], v[194:197], v[120:123]
	v_mfma_f32_16x16x32_bf16 v[112:115], v[176:179], v[194:197], v[112:115]
	v_mfma_f32_16x16x32_bf16 v[104:107], v[168:171], v[202:205], v[104:107]
	v_mfma_f32_16x16x32_bf16 v[96:99], v[176:179], v[202:205], v[96:99]
	v_mfma_f32_16x16x32_bf16 v[88:91], v[168:171], v[224:227], v[88:91]
	v_mfma_f32_16x16x32_bf16 v[80:83], v[176:179], v[224:227], v[80:83]
	v_mfma_f32_16x16x32_bf16 v[72:75], v[168:171], v[232:235], v[72:75]
	v_mfma_f32_16x16x32_bf16 v[64:67], v[176:179], v[232:235], v[64:67]
	v_mfma_f32_16x16x32_bf16 v[120:123], v[172:175], v[198:201], v[120:123]
	v_mfma_f32_16x16x32_bf16 v[112:115], v[180:183], v[198:201], v[112:115]
	v_mfma_f32_16x16x32_bf16 v[104:107], v[172:175], v[206:209], v[104:107]
	v_mfma_f32_16x16x32_bf16 v[96:99], v[180:183], v[206:209], v[96:99]
	v_mfma_f32_16x16x32_bf16 v[88:91], v[172:175], v[228:231], v[88:91]
	v_mfma_f32_16x16x32_bf16 v[80:83], v[180:183], v[228:231], v[80:83]
	v_mfma_f32_16x16x32_bf16 v[72:75], v[172:175], v[236:239], v[72:75]
	v_mfma_f32_16x16x32_bf16 v[64:67], v[180:183], v[236:239], v[64:67]
	s_setprio 0
	s_barrier
	s_add_i32 s29, s48, s50
	v_lshl_add_u64 v[216:217], v[210:211], 0, v[130:131]
	s_mov_b32 m0, s29
	ds_read_b128 v[194:197], v149 offset:16384
	ds_read_b128 v[198:201], v149 offset:17408
	ds_read_b128 v[202:205], v149 offset:18432
	ds_read_b128 v[206:209], v149 offset:19456
	ds_read_b128 v[224:227], v149 offset:20480
	ds_read_b128 v[228:231], v149 offset:21504
	ds_read_b128 v[232:235], v149 offset:22528
	ds_read_b128 v[236:239], v149 offset:23552
	global_load_lds_dwordx4 v[216:217], off
	v_lshl_add_u64 v[218:219], v[210:211], 0, v[134:135]
	s_add_i32 m0, s29, 0x2000
	v_lshl_add_u64 v[220:221], v[210:211], 0, s[72:73]
	s_add_i32 s28, s28, s50
	global_load_lds_dwordx4 v[218:219], off
	v_lshl_add_u64 v[240:241], v[220:221], 0, v[130:131]
	s_mov_b32 m0, s28
	v_lshl_add_u64 v[220:221], v[220:221], 0, v[134:135]
	global_load_lds_dwordx4 v[240:241], off
	s_add_i32 m0, s28, 0x2000
	v_lshl_add_u64 v[240:241], s[30:31], 0, v[132:133]
	global_load_lds_dwordx4 v[220:221], off
	s_mov_b32 m0, s19
	s_nop 0
	global_load_lds_dwordx4 v128, s[30:31]
	s_mov_b32 m0, s51
	s_nop 0
	global_load_lds_dwordx4 v132, s[30:31]
	s_waitcnt vmcnt(8)
	s_waitcnt lgkmcnt(0)
	s_barrier
	s_setprio 1
	s_waitcnt lgkmcnt(0)
	v_mfma_f32_16x16x32_bf16 v[60:63], v[152:155], v[194:197], v[60:63]
	v_mfma_f32_16x16x32_bf16 v[52:55], v[160:163], v[194:197], v[52:55]
	v_mfma_f32_16x16x32_bf16 v[44:47], v[152:155], v[202:205], v[44:47]
	v_mfma_f32_16x16x32_bf16 v[36:39], v[160:163], v[202:205], v[36:39]
	v_mfma_f32_16x16x32_bf16 v[28:31], v[152:155], v[224:227], v[28:31]
	v_mfma_f32_16x16x32_bf16 v[20:23], v[160:163], v[224:227], v[20:23]
	v_mfma_f32_16x16x32_bf16 v[12:15], v[152:155], v[232:235], v[12:15]
	v_mfma_f32_16x16x32_bf16 v[4:7], v[160:163], v[232:235], v[4:7]
	v_mfma_f32_16x16x32_bf16 v[60:63], v[156:159], v[198:201], v[60:63]
	v_mfma_f32_16x16x32_bf16 v[52:55], v[164:167], v[198:201], v[52:55]
	v_mfma_f32_16x16x32_bf16 v[44:47], v[156:159], v[206:209], v[44:47]
	v_mfma_f32_16x16x32_bf16 v[36:39], v[164:167], v[206:209], v[36:39]
	v_mfma_f32_16x16x32_bf16 v[28:31], v[156:159], v[228:231], v[28:31]
	v_mfma_f32_16x16x32_bf16 v[20:23], v[164:167], v[228:231], v[20:23]
	v_mfma_f32_16x16x32_bf16 v[12:15], v[156:159], v[236:239], v[12:15]
	v_mfma_f32_16x16x32_bf16 v[4:7], v[164:167], v[236:239], v[4:7]
	s_setprio 0
	s_setprio 1
	v_mfma_f32_16x16x32_bf16 v[56:59], v[168:171], v[194:197], v[56:59]
	v_mfma_f32_16x16x32_bf16 v[48:51], v[176:179], v[194:197], v[48:51]
	v_mfma_f32_16x16x32_bf16 v[40:43], v[168:171], v[202:205], v[40:43]
	v_mfma_f32_16x16x32_bf16 v[32:35], v[176:179], v[202:205], v[32:35]
	v_mfma_f32_16x16x32_bf16 v[24:27], v[168:171], v[224:227], v[24:27]
	v_mfma_f32_16x16x32_bf16 v[16:19], v[176:179], v[224:227], v[16:19]
	v_mfma_f32_16x16x32_bf16 v[8:11], v[168:171], v[232:235], v[8:11]
	v_mfma_f32_16x16x32_bf16 v[0:3], v[176:179], v[232:235], v[0:3]
	v_mfma_f32_16x16x32_bf16 v[56:59], v[172:175], v[198:201], v[56:59]
	v_mfma_f32_16x16x32_bf16 v[48:51], v[180:183], v[198:201], v[48:51]
	v_mfma_f32_16x16x32_bf16 v[40:43], v[172:175], v[206:209], v[40:43]
	v_mfma_f32_16x16x32_bf16 v[32:35], v[180:183], v[206:209], v[32:35]
	v_mfma_f32_16x16x32_bf16 v[24:27], v[172:175], v[228:231], v[24:27]
	v_mfma_f32_16x16x32_bf16 v[16:19], v[180:183], v[228:231], v[16:19]
	v_mfma_f32_16x16x32_bf16 v[8:11], v[172:175], v[236:239], v[8:11]
	v_mfma_f32_16x16x32_bf16 v[0:3], v[180:183], v[236:239], v[0:3]
	s_setprio 0
	s_barrier
	s_add_i32 s48, 0, 0x18000
	s_add_i32 s49, 0, 0x1c000
	v_add_u32_e32 v164, s48, v147
	v_add_u32_e32 v180, s49, v147
	ds_read_b128 v[152:155], v164
	ds_read_b128 v[156:159], v164 offset:1024
	ds_read_b128 v[160:163], v164 offset:2048
	ds_read_b128 v[164:167], v164 offset:3072
	ds_read_b128 v[168:171], v180
	ds_read_b128 v[172:175], v180 offset:1024
	ds_read_b128 v[176:179], v180 offset:2048
	ds_read_b128 v[180:183], v180 offset:3072
	s_add_u32 s28, s30, 0x80000
	s_addc_u32 s29, s31, 0
	s_mov_b32 m0, s52
	ds_read_b128 v[194:197], v149 offset:32768
	ds_read_b128 v[198:201], v149 offset:33792
	ds_read_b128 v[202:205], v149 offset:34816
	ds_read_b128 v[206:209], v149 offset:35840
	ds_read_b128 v[224:227], v149 offset:36864
	ds_read_b128 v[228:231], v149 offset:37888
	ds_read_b128 v[232:235], v149 offset:38912
	ds_read_b128 v[236:239], v149 offset:39936
	global_load_lds_dwordx4 v128, s[28:29]
	s_mov_b32 m0, s53
	s_nop 0
	global_load_lds_dwordx4 v132, s[28:29]
	s_waitcnt vmcnt(8)
	s_waitcnt lgkmcnt(0)
	s_barrier
	s_setprio 1
	s_waitcnt lgkmcnt(0)
	v_mfma_f32_16x16x32_bf16 v[124:127], v[152:155], v[194:197], v[124:127]
	v_mfma_f32_16x16x32_bf16 v[116:119], v[160:163], v[194:197], v[116:119]
	v_mfma_f32_16x16x32_bf16 v[108:111], v[152:155], v[202:205], v[108:111]
	v_mfma_f32_16x16x32_bf16 v[100:103], v[160:163], v[202:205], v[100:103]
	v_mfma_f32_16x16x32_bf16 v[92:95], v[152:155], v[224:227], v[92:95]
	v_mfma_f32_16x16x32_bf16 v[84:87], v[160:163], v[224:227], v[84:87]
	v_mfma_f32_16x16x32_bf16 v[76:79], v[152:155], v[232:235], v[76:79]
	v_mfma_f32_16x16x32_bf16 v[68:71], v[160:163], v[232:235], v[68:71]
	v_mfma_f32_16x16x32_bf16 v[124:127], v[156:159], v[198:201], v[124:127]
	v_mfma_f32_16x16x32_bf16 v[116:119], v[164:167], v[198:201], v[116:119]
	v_mfma_f32_16x16x32_bf16 v[108:111], v[156:159], v[206:209], v[108:111]
	v_mfma_f32_16x16x32_bf16 v[100:103], v[164:167], v[206:209], v[100:103]
	v_mfma_f32_16x16x32_bf16 v[92:95], v[156:159], v[228:231], v[92:95]
	v_mfma_f32_16x16x32_bf16 v[84:87], v[164:167], v[228:231], v[84:87]
	v_mfma_f32_16x16x32_bf16 v[76:79], v[156:159], v[236:239], v[76:79]
	v_mfma_f32_16x16x32_bf16 v[68:71], v[164:167], v[236:239], v[68:71]
	s_setprio 0
	s_setprio 1
	v_mfma_f32_16x16x32_bf16 v[120:123], v[168:171], v[194:197], v[120:123]
	v_mfma_f32_16x16x32_bf16 v[112:115], v[176:179], v[194:197], v[112:115]
	v_mfma_f32_16x16x32_bf16 v[104:107], v[168:171], v[202:205], v[104:107]
	v_mfma_f32_16x16x32_bf16 v[96:99], v[176:179], v[202:205], v[96:99]
	v_mfma_f32_16x16x32_bf16 v[88:91], v[168:171], v[224:227], v[88:91]
	v_mfma_f32_16x16x32_bf16 v[80:83], v[176:179], v[224:227], v[80:83]
	v_mfma_f32_16x16x32_bf16 v[72:75], v[168:171], v[232:235], v[72:75]
	v_mfma_f32_16x16x32_bf16 v[64:67], v[176:179], v[232:235], v[64:67]
	v_mfma_f32_16x16x32_bf16 v[120:123], v[172:175], v[198:201], v[120:123]
	v_mfma_f32_16x16x32_bf16 v[112:115], v[180:183], v[198:201], v[112:115]
	v_mfma_f32_16x16x32_bf16 v[104:107], v[172:175], v[206:209], v[104:107]
	v_mfma_f32_16x16x32_bf16 v[96:99], v[180:183], v[206:209], v[96:99]
	v_mfma_f32_16x16x32_bf16 v[88:91], v[172:175], v[228:231], v[88:91]
	v_mfma_f32_16x16x32_bf16 v[80:83], v[180:183], v[228:231], v[80:83]
	v_mfma_f32_16x16x32_bf16 v[72:75], v[172:175], v[236:239], v[72:75]
	v_mfma_f32_16x16x32_bf16 v[64:67], v[180:183], v[236:239], v[64:67]
	s_setprio 0
	s_barrier
	s_add_i32 s28, s48, s50
	v_lshl_add_u64 v[216:217], v[216:217], 0, s[68:69]
	s_mov_b32 m0, s28
	ds_read_b128 v[194:197], v149 offset:49152
	ds_read_b128 v[198:201], v149 offset:50176
	ds_read_b128 v[202:205], v149 offset:51200
	ds_read_b128 v[206:209], v149 offset:52224
	ds_read_b128 v[224:227], v149 offset:53248
	ds_read_b128 v[228:231], v149 offset:54272
	ds_read_b128 v[232:235], v149 offset:55296
	ds_read_b128 v[236:239], v149 offset:56320
	global_load_lds_dwordx4 v[216:217], off
	v_lshl_add_u64 v[216:217], v[218:219], 0, s[68:69]
	s_add_i32 m0, s28, 0x2000
	v_lshl_add_u64 v[210:211], v[210:211], 0, s[74:75]
	s_add_i32 s28, s49, s50
	global_load_lds_dwordx4 v[216:217], off
	v_lshl_add_u64 v[216:217], v[210:211], 0, v[130:131]
	s_mov_b32 m0, s28
	v_lshl_add_u64 v[210:211], v[210:211], 0, v[134:135]
	global_load_lds_dwordx4 v[216:217], off
	s_add_i32 m0, s28, 0x2000
	s_nop 0
	global_load_lds_dwordx4 v[210:211], off
	s_add_i32 m0, s58, 0xffffff80
	s_nop 0
	global_load_lds_dwordx4 v128, s[30:31] offset:128
	v_lshl_add_u64 v[210:211], v[240:241], 0, s[68:69]
	s_add_i32 m0, s59, 0xffffff80
	s_nop 0
	global_load_lds_dwordx4 v132, s[30:31] offset:128
	s_waitcnt vmcnt(8)
	s_waitcnt lgkmcnt(0)
	s_barrier
	s_setprio 1
	s_waitcnt lgkmcnt(0)
	v_mfma_f32_16x16x32_bf16 v[60:63], v[152:155], v[194:197], v[60:63]
	v_mfma_f32_16x16x32_bf16 v[52:55], v[160:163], v[194:197], v[52:55]
	v_mfma_f32_16x16x32_bf16 v[44:47], v[152:155], v[202:205], v[44:47]
	v_mfma_f32_16x16x32_bf16 v[36:39], v[160:163], v[202:205], v[36:39]
	v_mfma_f32_16x16x32_bf16 v[28:31], v[152:155], v[224:227], v[28:31]
	v_mfma_f32_16x16x32_bf16 v[20:23], v[160:163], v[224:227], v[20:23]
	v_mfma_f32_16x16x32_bf16 v[12:15], v[152:155], v[232:235], v[12:15]
	v_mfma_f32_16x16x32_bf16 v[4:7], v[160:163], v[232:235], v[4:7]
	v_mfma_f32_16x16x32_bf16 v[60:63], v[156:159], v[198:201], v[60:63]
	v_mfma_f32_16x16x32_bf16 v[52:55], v[164:167], v[198:201], v[52:55]
	v_mfma_f32_16x16x32_bf16 v[44:47], v[156:159], v[206:209], v[44:47]
	v_mfma_f32_16x16x32_bf16 v[36:39], v[164:167], v[206:209], v[36:39]
	v_mfma_f32_16x16x32_bf16 v[28:31], v[156:159], v[228:231], v[28:31]
	v_mfma_f32_16x16x32_bf16 v[20:23], v[164:167], v[228:231], v[20:23]
	v_mfma_f32_16x16x32_bf16 v[12:15], v[156:159], v[236:239], v[12:15]
	v_mfma_f32_16x16x32_bf16 v[4:7], v[164:167], v[236:239], v[4:7]
	s_setprio 0
	s_setprio 1
	v_mfma_f32_16x16x32_bf16 v[56:59], v[168:171], v[194:197], v[56:59]
	v_mfma_f32_16x16x32_bf16 v[48:51], v[176:179], v[194:197], v[48:51]
	v_mfma_f32_16x16x32_bf16 v[40:43], v[168:171], v[202:205], v[40:43]
	v_mfma_f32_16x16x32_bf16 v[32:35], v[176:179], v[202:205], v[32:35]
	v_mfma_f32_16x16x32_bf16 v[24:27], v[168:171], v[224:227], v[24:27]
	v_mfma_f32_16x16x32_bf16 v[16:19], v[176:179], v[224:227], v[16:19]
	v_mfma_f32_16x16x32_bf16 v[8:11], v[168:171], v[232:235], v[8:11]
	v_mfma_f32_16x16x32_bf16 v[0:3], v[176:179], v[232:235], v[0:3]
	v_mfma_f32_16x16x32_bf16 v[56:59], v[172:175], v[198:201], v[56:59]
	v_mfma_f32_16x16x32_bf16 v[48:51], v[180:183], v[198:201], v[48:51]
	v_mfma_f32_16x16x32_bf16 v[40:43], v[172:175], v[206:209], v[40:43]
	v_mfma_f32_16x16x32_bf16 v[32:35], v[180:183], v[206:209], v[32:35]
	v_mfma_f32_16x16x32_bf16 v[24:27], v[172:175], v[228:231], v[24:27]
	v_mfma_f32_16x16x32_bf16 v[16:19], v[180:183], v[228:231], v[16:19]
	v_mfma_f32_16x16x32_bf16 v[8:11], v[172:175], v[236:239], v[8:11]
	v_mfma_f32_16x16x32_bf16 v[0:3], v[180:183], v[236:239], v[0:3]
	s_setprio 0
	s_barrier
	s_add_i32 s17, s17, 2
	s_add_u32 s24, s24, 0x100
	s_addc_u32 s25, s25, 0
	s_cmp_gt_u32 s17, 29
	v_lshl_add_u64 v[144:145], v[144:145], 0, s[76:77]
	s_cbranch_scc0 .LBB0_1419
	s_and_b64 vcc, exec, s[6:7]
	s_cbranch_vccz .LBB0_1422
	s_barrier

.LBB0_1491:
	s_add_u32 s14, s12, 0x100
	s_addc_u32 s15, s13, 0
	s_add_i32 s28, 0, 0x10000
	s_cmp_eq_u32 s59, 40
	s_cselect_b32 s17, s53, s15
	s_cselect_b32 s16, s58, s14
	s_cselect_b64 vcc, -1, 0
	s_add_i32 s29, 0, 0x14000
	v_add_u32_e32 v164, s28, v147
	v_add_u32_e32 v180, s29, v147
	ds_read_b128 v[152:155], v164
	ds_read_b128 v[156:159], v164 offset:1024
	ds_read_b128 v[160:163], v164 offset:2048
	ds_read_b128 v[164:167], v164 offset:3072
	ds_read_b128 v[168:171], v180
	ds_read_b128 v[172:175], v180 offset:1024
	ds_read_b128 v[176:179], v180 offset:2048
	ds_read_b128 v[180:183], v180 offset:3072
	v_cndmask_b32_e32 v211, v145, v150, vcc
	v_cndmask_b32_e32 v210, v144, v151, vcc
	v_lshl_add_u64 v[216:217], s[12:13], 0, v[136:137]
	s_add_i32 m0, s40, 0xc000
	ds_read_b128 v[194:197], v149
	ds_read_b128 v[198:201], v149 offset:1024
	ds_read_b128 v[202:205], v149 offset:2048
	ds_read_b128 v[206:209], v149 offset:3072
	ds_read_b128 v[224:227], v149 offset:4096
	ds_read_b128 v[228:231], v149 offset:5120
	ds_read_b128 v[232:235], v149 offset:6144
	ds_read_b128 v[236:239], v149 offset:7168
	global_load_lds_dwordx4 v[216:217], off
	v_lshl_add_u64 v[216:217], s[12:13], 0, v[138:139]
	s_add_i32 m0, s40, 0xe000
	s_nop 0
	global_load_lds_dwordx4 v[216:217], off
	s_waitcnt vmcnt(8)
	s_waitcnt lgkmcnt(0)
	s_barrier
	s_setprio 1
	s_waitcnt lgkmcnt(0)
	v_mfma_f32_16x16x32_bf16 v[124:127], v[152:155], v[194:197], v[124:127]
	v_mfma_f32_16x16x32_bf16 v[120:123], v[160:163], v[194:197], v[120:123]
	v_mfma_f32_16x16x32_bf16 v[116:119], v[152:155], v[202:205], v[116:119]
	v_mfma_f32_16x16x32_bf16 v[108:111], v[160:163], v[202:205], v[108:111]
	v_mfma_f32_16x16x32_bf16 v[100:103], v[152:155], v[224:227], v[100:103]
	v_mfma_f32_16x16x32_bf16 v[92:95], v[160:163], v[224:227], v[92:95]
	v_mfma_f32_16x16x32_bf16 v[80:83], v[152:155], v[232:235], v[80:83]
	v_mfma_f32_16x16x32_bf16 v[72:75], v[160:163], v[232:235], v[72:75]
	v_mfma_f32_16x16x32_bf16 v[124:127], v[156:159], v[198:201], v[124:127]
	v_mfma_f32_16x16x32_bf16 v[120:123], v[164:167], v[198:201], v[120:123]
	v_mfma_f32_16x16x32_bf16 v[116:119], v[156:159], v[206:209], v[116:119]
	v_mfma_f32_16x16x32_bf16 v[108:111], v[164:167], v[206:209], v[108:111]
	v_mfma_f32_16x16x32_bf16 v[100:103], v[156:159], v[228:231], v[100:103]
	v_mfma_f32_16x16x32_bf16 v[92:95], v[164:167], v[228:231], v[92:95]
	v_mfma_f32_16x16x32_bf16 v[80:83], v[156:159], v[236:239], v[80:83]
	v_mfma_f32_16x16x32_bf16 v[72:75], v[164:167], v[236:239], v[72:75]
	s_setprio 0
	s_setprio 1
	v_mfma_f32_16x16x32_bf16 v[112:115], v[168:171], v[194:197], v[112:115]
	v_mfma_f32_16x16x32_bf16 v[104:107], v[176:179], v[194:197], v[104:107]
	v_mfma_f32_16x16x32_bf16 v[96:99], v[168:171], v[202:205], v[96:99]
	v_mfma_f32_16x16x32_bf16 v[88:91], v[176:179], v[202:205], v[88:91]
	v_mfma_f32_16x16x32_bf16 v[84:87], v[168:171], v[224:227], v[84:87]
	v_mfma_f32_16x16x32_bf16 v[76:79], v[176:179], v[224:227], v[76:79]
	v_mfma_f32_16x16x32_bf16 v[68:71], v[168:171], v[232:235], v[68:71]
	v_mfma_f32_16x16x32_bf16 v[64:67], v[176:179], v[232:235], v[64:67]
	v_mfma_f32_16x16x32_bf16 v[112:115], v[172:175], v[198:201], v[112:115]
	v_mfma_f32_16x16x32_bf16 v[104:107], v[180:183], v[198:201], v[104:107]
	v_mfma_f32_16x16x32_bf16 v[96:99], v[172:175], v[206:209], v[96:99]
	v_mfma_f32_16x16x32_bf16 v[88:91], v[180:183], v[206:209], v[88:91]
	v_mfma_f32_16x16x32_bf16 v[84:87], v[172:175], v[228:231], v[84:87]
	v_mfma_f32_16x16x32_bf16 v[76:79], v[180:183], v[228:231], v[76:79]
	v_mfma_f32_16x16x32_bf16 v[68:71], v[172:175], v[236:239], v[68:71]
	v_mfma_f32_16x16x32_bf16 v[64:67], v[180:183], v[236:239], v[64:67]
	s_setprio 0
	s_barrier
	s_add_i32 s12, s28, s30
	v_lshl_add_u64 v[216:217], v[210:211], 0, v[132:133]
	s_mov_b32 m0, s12
	ds_read_b128 v[194:197], v149 offset:16384
	ds_read_b128 v[198:201], v149 offset:17408
	ds_read_b128 v[202:205], v149 offset:18432
	ds_read_b128 v[206:209], v149 offset:19456
	ds_read_b128 v[224:227], v149 offset:20480
	ds_read_b128 v[228:231], v149 offset:21504
	ds_read_b128 v[232:235], v149 offset:22528
	ds_read_b128 v[236:239], v149 offset:23552
	global_load_lds_dwordx4 v[216:217], off
	v_lshl_add_u64 v[218:219], v[210:211], 0, v[128:129]
	s_add_i32 m0, s12, 0x2000
	v_lshl_add_u64 v[220:221], v[210:211], 0, s[72:73]
	s_add_i32 s12, s29, s30
	global_load_lds_dwordx4 v[218:219], off
	v_lshl_add_u64 v[240:241], v[220:221], 0, v[132:133]
	s_mov_b32 m0, s12
	v_lshl_add_u64 v[220:221], v[220:221], 0, v[128:129]
	global_load_lds_dwordx4 v[240:241], off
	s_add_i32 m0, s12, 0x2000
	v_lshl_add_u64 v[240:241], s[16:17], 0, v[130:131]
	global_load_lds_dwordx4 v[220:221], off
	s_mov_b32 m0, s40
	s_nop 0
	global_load_lds_dwordx4 v134, s[16:17]
	s_mov_b32 m0, s41
	s_nop 0
	global_load_lds_dwordx4 v130, s[16:17]
	s_waitcnt vmcnt(8)
	s_waitcnt lgkmcnt(0)
	s_barrier
	s_setprio 1
	s_waitcnt lgkmcnt(0)
	v_mfma_f32_16x16x32_bf16 v[60:63], v[152:155], v[194:197], v[60:63]
	v_mfma_f32_16x16x32_bf16 v[56:59], v[160:163], v[194:197], v[56:59]
	v_mfma_f32_16x16x32_bf16 v[52:55], v[152:155], v[202:205], v[52:55]
	v_mfma_f32_16x16x32_bf16 v[44:47], v[160:163], v[202:205], v[44:47]
	v_mfma_f32_16x16x32_bf16 v[36:39], v[152:155], v[224:227], v[36:39]
	v_mfma_f32_16x16x32_bf16 v[28:31], v[160:163], v[224:227], v[28:31]
	v_mfma_f32_16x16x32_bf16 v[20:23], v[152:155], v[232:235], v[20:23]
	v_mfma_f32_16x16x32_bf16 v[12:15], v[160:163], v[232:235], v[12:15]
	v_mfma_f32_16x16x32_bf16 v[60:63], v[156:159], v[198:201], v[60:63]
	v_mfma_f32_16x16x32_bf16 v[56:59], v[164:167], v[198:201], v[56:59]
	v_mfma_f32_16x16x32_bf16 v[52:55], v[156:159], v[206:209], v[52:55]
	v_mfma_f32_16x16x32_bf16 v[44:47], v[164:167], v[206:209], v[44:47]
	v_mfma_f32_16x16x32_bf16 v[36:39], v[156:159], v[228:231], v[36:39]
	v_mfma_f32_16x16x32_bf16 v[28:31], v[164:167], v[228:231], v[28:31]
	v_mfma_f32_16x16x32_bf16 v[20:23], v[156:159], v[236:239], v[20:23]
	v_mfma_f32_16x16x32_bf16 v[12:15], v[164:167], v[236:239], v[12:15]
	s_setprio 0
	s_setprio 1
	v_mfma_f32_16x16x32_bf16 v[48:51], v[168:171], v[194:197], v[48:51]
	v_mfma_f32_16x16x32_bf16 v[40:43], v[176:179], v[194:197], v[40:43]
	v_mfma_f32_16x16x32_bf16 v[32:35], v[168:171], v[202:205], v[32:35]
	v_mfma_f32_16x16x32_bf16 v[24:27], v[176:179], v[202:205], v[24:27]
	v_mfma_f32_16x16x32_bf16 v[16:19], v[168:171], v[224:227], v[16:19]
	v_mfma_f32_16x16x32_bf16 v[8:11], v[176:179], v[224:227], v[8:11]
	v_mfma_f32_16x16x32_bf16 v[4:7], v[168:171], v[232:235], v[4:7]
	v_mfma_f32_16x16x32_bf16 v[0:3], v[176:179], v[232:235], v[0:3]
	v_mfma_f32_16x16x32_bf16 v[48:51], v[172:175], v[198:201], v[48:51]
	v_mfma_f32_16x16x32_bf16 v[40:43], v[180:183], v[198:201], v[40:43]
	v_mfma_f32_16x16x32_bf16 v[32:35], v[172:175], v[206:209], v[32:35]
	v_mfma_f32_16x16x32_bf16 v[24:27], v[180:183], v[206:209], v[24:27]
	v_mfma_f32_16x16x32_bf16 v[16:19], v[172:175], v[228:231], v[16:19]
	v_mfma_f32_16x16x32_bf16 v[8:11], v[180:183], v[228:231], v[8:11]
	v_mfma_f32_16x16x32_bf16 v[4:7], v[172:175], v[236:239], v[4:7]
	v_mfma_f32_16x16x32_bf16 v[0:3], v[180:183], v[236:239], v[0:3]
	s_setprio 0
	s_barrier
	s_add_i32 s28, 0, 0x18000
	s_add_i32 s29, 0, 0x1c000
	v_add_u32_e32 v164, s28, v147
	v_add_u32_e32 v180, s29, v147
	ds_read_b128 v[152:155], v164
	ds_read_b128 v[156:159], v164 offset:1024
	ds_read_b128 v[160:163], v164 offset:2048
	ds_read_b128 v[164:167], v164 offset:3072
	ds_read_b128 v[168:171], v180
	ds_read_b128 v[172:175], v180 offset:1024
	ds_read_b128 v[176:179], v180 offset:2048
	ds_read_b128 v[180:183], v180 offset:3072
	s_add_u32 s12, s16, 0xb0000
	s_addc_u32 s13, s17, 0
	s_mov_b32 m0, s42
	ds_read_b128 v[194:197], v149 offset:32768
	ds_read_b128 v[198:201], v149 offset:33792
	ds_read_b128 v[202:205], v149 offset:34816
	ds_read_b128 v[206:209], v149 offset:35840
	ds_read_b128 v[224:227], v149 offset:36864
	ds_read_b128 v[228:231], v149 offset:37888
	ds_read_b128 v[232:235], v149 offset:38912
	ds_read_b128 v[236:239], v149 offset:39936
	global_load_lds_dwordx4 v134, s[12:13]
	s_mov_b32 m0, s43
	s_nop 0
	global_load_lds_dwordx4 v130, s[12:13]
	s_waitcnt vmcnt(8)
	s_waitcnt lgkmcnt(0)
	s_barrier
	s_setprio 1
	s_waitcnt lgkmcnt(0)
	v_mfma_f32_16x16x32_bf16 v[124:127], v[152:155], v[194:197], v[124:127]
	v_mfma_f32_16x16x32_bf16 v[120:123], v[160:163], v[194:197], v[120:123]
	v_mfma_f32_16x16x32_bf16 v[116:119], v[152:155], v[202:205], v[116:119]
	v_mfma_f32_16x16x32_bf16 v[108:111], v[160:163], v[202:205], v[108:111]
	v_mfma_f32_16x16x32_bf16 v[100:103], v[152:155], v[224:227], v[100:103]
	v_mfma_f32_16x16x32_bf16 v[92:95], v[160:163], v[224:227], v[92:95]
	v_mfma_f32_16x16x32_bf16 v[80:83], v[152:155], v[232:235], v[80:83]
	v_mfma_f32_16x16x32_bf16 v[72:75], v[160:163], v[232:235], v[72:75]
	v_mfma_f32_16x16x32_bf16 v[124:127], v[156:159], v[198:201], v[124:127]
	v_mfma_f32_16x16x32_bf16 v[120:123], v[164:167], v[198:201], v[120:123]
	v_mfma_f32_16x16x32_bf16 v[116:119], v[156:159], v[206:209], v[116:119]
	v_mfma_f32_16x16x32_bf16 v[108:111], v[164:167], v[206:209], v[108:111]
	v_mfma_f32_16x16x32_bf16 v[100:103], v[156:159], v[228:231], v[100:103]
	v_mfma_f32_16x16x32_bf16 v[92:95], v[164:167], v[228:231], v[92:95]
	v_mfma_f32_16x16x32_bf16 v[80:83], v[156:159], v[236:239], v[80:83]
	v_mfma_f32_16x16x32_bf16 v[72:75], v[164:167], v[236:239], v[72:75]
	s_setprio 0
	s_setprio 1
	v_mfma_f32_16x16x32_bf16 v[112:115], v[168:171], v[194:197], v[112:115]
	v_mfma_f32_16x16x32_bf16 v[104:107], v[176:179], v[194:197], v[104:107]
	v_mfma_f32_16x16x32_bf16 v[96:99], v[168:171], v[202:205], v[96:99]
	v_mfma_f32_16x16x32_bf16 v[88:91], v[176:179], v[202:205], v[88:91]
	v_mfma_f32_16x16x32_bf16 v[84:87], v[168:171], v[224:227], v[84:87]
	v_mfma_f32_16x16x32_bf16 v[76:79], v[176:179], v[224:227], v[76:79]
	v_mfma_f32_16x16x32_bf16 v[68:71], v[168:171], v[232:235], v[68:71]
	v_mfma_f32_16x16x32_bf16 v[64:67], v[176:179], v[232:235], v[64:67]
	v_mfma_f32_16x16x32_bf16 v[112:115], v[172:175], v[198:201], v[112:115]
	v_mfma_f32_16x16x32_bf16 v[104:107], v[180:183], v[198:201], v[104:107]
	v_mfma_f32_16x16x32_bf16 v[96:99], v[172:175], v[206:209], v[96:99]
	v_mfma_f32_16x16x32_bf16 v[88:91], v[180:183], v[206:209], v[88:91]
	v_mfma_f32_16x16x32_bf16 v[84:87], v[172:175], v[228:231], v[84:87]
	v_mfma_f32_16x16x32_bf16 v[76:79], v[180:183], v[228:231], v[76:79]
	v_mfma_f32_16x16x32_bf16 v[68:71], v[172:175], v[236:239], v[68:71]
	v_mfma_f32_16x16x32_bf16 v[64:67], v[180:183], v[236:239], v[64:67]
	s_setprio 0
	s_barrier
	s_add_i32 s12, s28, s30
	v_lshl_add_u64 v[216:217], v[216:217], 0, s[68:69]
	s_mov_b32 m0, s12
	ds_read_b128 v[194:197], v149 offset:49152
	ds_read_b128 v[198:201], v149 offset:50176
	ds_read_b128 v[202:205], v149 offset:51200
	ds_read_b128 v[206:209], v149 offset:52224
	ds_read_b128 v[224:227], v149 offset:53248
	ds_read_b128 v[228:231], v149 offset:54272
	ds_read_b128 v[232:235], v149 offset:55296
	ds_read_b128 v[236:239], v149 offset:56320
	global_load_lds_dwordx4 v[216:217], off
	v_lshl_add_u64 v[216:217], v[218:219], 0, s[68:69]
	s_add_i32 m0, s12, 0x2000
	v_lshl_add_u64 v[210:211], v[210:211], 0, s[74:75]
	s_add_i32 s12, s29, s30
	global_load_lds_dwordx4 v[216:217], off
	v_lshl_add_u64 v[216:217], v[210:211], 0, v[132:133]
	s_mov_b32 m0, s12
	v_lshl_add_u64 v[210:211], v[210:211], 0, v[128:129]
	global_load_lds_dwordx4 v[216:217], off
	s_add_i32 m0, s12, 0x2000
	s_nop 0
	global_load_lds_dwordx4 v[210:211], off
	s_add_i32 m0, s44, 0xffffff80
	s_nop 0
	global_load_lds_dwordx4 v134, s[16:17] offset:128
	v_lshl_add_u64 v[210:211], v[240:241], 0, s[68:69]
	s_add_i32 m0, s45, 0xffffff80
	s_nop 0
	global_load_lds_dwordx4 v130, s[16:17] offset:128
	s_waitcnt vmcnt(8)
	s_waitcnt lgkmcnt(0)
	s_barrier
	s_setprio 1
	s_waitcnt lgkmcnt(0)
	v_mfma_f32_16x16x32_bf16 v[60:63], v[152:155], v[194:197], v[60:63]
	v_mfma_f32_16x16x32_bf16 v[56:59], v[160:163], v[194:197], v[56:59]
	v_mfma_f32_16x16x32_bf16 v[52:55], v[152:155], v[202:205], v[52:55]
	v_mfma_f32_16x16x32_bf16 v[44:47], v[160:163], v[202:205], v[44:47]
	v_mfma_f32_16x16x32_bf16 v[36:39], v[152:155], v[224:227], v[36:39]
	v_mfma_f32_16x16x32_bf16 v[28:31], v[160:163], v[224:227], v[28:31]
	v_mfma_f32_16x16x32_bf16 v[20:23], v[152:155], v[232:235], v[20:23]
	v_mfma_f32_16x16x32_bf16 v[12:15], v[160:163], v[232:235], v[12:15]
	v_mfma_f32_16x16x32_bf16 v[60:63], v[156:159], v[198:201], v[60:63]
	v_mfma_f32_16x16x32_bf16 v[56:59], v[164:167], v[198:201], v[56:59]
	v_mfma_f32_16x16x32_bf16 v[52:55], v[156:159], v[206:209], v[52:55]
	v_mfma_f32_16x16x32_bf16 v[44:47], v[164:167], v[206:209], v[44:47]
	v_mfma_f32_16x16x32_bf16 v[36:39], v[156:159], v[228:231], v[36:39]
	v_mfma_f32_16x16x32_bf16 v[28:31], v[164:167], v[228:231], v[28:31]
	v_mfma_f32_16x16x32_bf16 v[20:23], v[156:159], v[236:239], v[20:23]
	v_mfma_f32_16x16x32_bf16 v[12:15], v[164:167], v[236:239], v[12:15]
	s_setprio 0
	s_setprio 1
	v_mfma_f32_16x16x32_bf16 v[48:51], v[168:171], v[194:197], v[48:51]
	v_mfma_f32_16x16x32_bf16 v[40:43], v[176:179], v[194:197], v[40:43]
	v_mfma_f32_16x16x32_bf16 v[32:35], v[168:171], v[202:205], v[32:35]
	v_mfma_f32_16x16x32_bf16 v[24:27], v[176:179], v[202:205], v[24:27]
	v_mfma_f32_16x16x32_bf16 v[16:19], v[168:171], v[224:227], v[16:19]
	v_mfma_f32_16x16x32_bf16 v[8:11], v[176:179], v[224:227], v[8:11]
	v_mfma_f32_16x16x32_bf16 v[4:7], v[168:171], v[232:235], v[4:7]
	v_mfma_f32_16x16x32_bf16 v[0:3], v[176:179], v[232:235], v[0:3]
	v_mfma_f32_16x16x32_bf16 v[48:51], v[172:175], v[198:201], v[48:51]
	v_mfma_f32_16x16x32_bf16 v[40:43], v[180:183], v[198:201], v[40:43]
	v_mfma_f32_16x16x32_bf16 v[32:35], v[172:175], v[206:209], v[32:35]
	v_mfma_f32_16x16x32_bf16 v[24:27], v[180:183], v[206:209], v[24:27]
	v_mfma_f32_16x16x32_bf16 v[16:19], v[172:175], v[228:231], v[16:19]
	v_mfma_f32_16x16x32_bf16 v[8:11], v[180:183], v[228:231], v[8:11]
	v_mfma_f32_16x16x32_bf16 v[4:7], v[172:175], v[236:239], v[4:7]
	v_mfma_f32_16x16x32_bf16 v[0:3], v[180:183], v[236:239], v[0:3]
	s_setprio 0
	s_barrier
	s_add_i32 s59, s59, 2
	v_lshl_add_u64 v[144:145], v[144:145], 0, s[60:61]
	s_cmp_gt_u32 s59, 41
	s_mov_b64 s[12:13], s[14:15]
	s_cbranch_scc0 .LBB0_1491
	s_mov_b64 s[14:15], 0xb0000
	s_and_b64 vcc, exec, s[6:7]
	s_cbranch_vccz .LBB0_1494
	s_barrier

.LBB0_1587:
	s_add_u32 s28, s24, 0xfff80080
	s_addc_u32 s29, s25, -1
	s_add_i32 s48, 0, 0x10000
	s_cmp_eq_u32 s51, 28
	s_cselect_b32 s39, s9, s29
	s_cselect_b32 s38, s11, s28
	s_cselect_b32 s31, s45, s50
	s_cselect_b32 s30, s46, s47
	s_add_i32 s49, 0, 0x14000
	v_add_u32_e32 v154, s48, v139
	v_add_u32_e32 v170, s49, v139
	ds_read_b128 v[142:145], v154
	ds_read_b128 v[146:149], v154 offset:1024
	ds_read_b128 v[150:153], v154 offset:2048
	ds_read_b128 v[154:157], v154 offset:3072
	ds_read_b128 v[158:161], v170
	ds_read_b128 v[162:165], v170 offset:1024
	ds_read_b128 v[166:169], v170 offset:2048
	ds_read_b128 v[170:173], v170 offset:3072
	s_add_i32 m0, s20, 0xc000
	ds_read_b128 v[174:177], v141
	ds_read_b128 v[178:181], v141 offset:1024
	ds_read_b128 v[194:197], v141 offset:2048
	ds_read_b128 v[198:201], v141 offset:3072
	ds_read_b128 v[202:205], v141 offset:4096
	ds_read_b128 v[206:209], v141 offset:5120
	ds_read_b128 v[224:227], v141 offset:6144
	ds_read_b128 v[228:231], v141 offset:7168
	global_load_lds_dwordx4 v134, s[24:25]
	s_add_i32 m0, s20, 0xe000
	s_nop 0
	global_load_lds_dwordx4 v136, s[24:25]
	s_waitcnt vmcnt(8)
	s_waitcnt lgkmcnt(0)
	s_barrier
	s_setprio 1
	s_waitcnt lgkmcnt(0)
	v_mfma_f32_16x16x32_bf16 v[124:127], v[142:145], v[174:177], v[124:127]
	v_mfma_f32_16x16x32_bf16 v[116:119], v[150:153], v[174:177], v[116:119]
	v_mfma_f32_16x16x32_bf16 v[108:111], v[142:145], v[194:197], v[108:111]
	v_mfma_f32_16x16x32_bf16 v[100:103], v[150:153], v[194:197], v[100:103]
	v_mfma_f32_16x16x32_bf16 v[92:95], v[142:145], v[202:205], v[92:95]
	v_mfma_f32_16x16x32_bf16 v[84:87], v[150:153], v[202:205], v[84:87]
	v_mfma_f32_16x16x32_bf16 v[76:79], v[142:145], v[224:227], v[76:79]
	v_mfma_f32_16x16x32_bf16 v[68:71], v[150:153], v[224:227], v[68:71]
	v_mfma_f32_16x16x32_bf16 v[124:127], v[146:149], v[178:181], v[124:127]
	v_mfma_f32_16x16x32_bf16 v[116:119], v[154:157], v[178:181], v[116:119]
	v_mfma_f32_16x16x32_bf16 v[108:111], v[146:149], v[198:201], v[108:111]
	v_mfma_f32_16x16x32_bf16 v[100:103], v[154:157], v[198:201], v[100:103]
	v_mfma_f32_16x16x32_bf16 v[92:95], v[146:149], v[206:209], v[92:95]
	v_mfma_f32_16x16x32_bf16 v[84:87], v[154:157], v[206:209], v[84:87]
	v_mfma_f32_16x16x32_bf16 v[76:79], v[146:149], v[228:231], v[76:79]
	v_mfma_f32_16x16x32_bf16 v[68:71], v[154:157], v[228:231], v[68:71]
	s_setprio 0
	s_setprio 1
	v_mfma_f32_16x16x32_bf16 v[120:123], v[158:161], v[174:177], v[120:123]
	v_mfma_f32_16x16x32_bf16 v[112:115], v[166:169], v[174:177], v[112:115]
	v_mfma_f32_16x16x32_bf16 v[104:107], v[158:161], v[194:197], v[104:107]
	v_mfma_f32_16x16x32_bf16 v[96:99], v[166:169], v[194:197], v[96:99]
	v_mfma_f32_16x16x32_bf16 v[88:91], v[158:161], v[202:205], v[88:91]
	v_mfma_f32_16x16x32_bf16 v[80:83], v[166:169], v[202:205], v[80:83]
	v_mfma_f32_16x16x32_bf16 v[72:75], v[158:161], v[224:227], v[72:75]
	v_mfma_f32_16x16x32_bf16 v[64:67], v[166:169], v[224:227], v[64:67]
	v_mfma_f32_16x16x32_bf16 v[120:123], v[162:165], v[178:181], v[120:123]
	v_mfma_f32_16x16x32_bf16 v[112:115], v[170:173], v[178:181], v[112:115]
	v_mfma_f32_16x16x32_bf16 v[104:107], v[162:165], v[198:201], v[104:107]
	v_mfma_f32_16x16x32_bf16 v[96:99], v[170:173], v[198:201], v[96:99]
	v_mfma_f32_16x16x32_bf16 v[88:91], v[162:165], v[206:209], v[88:91]
	v_mfma_f32_16x16x32_bf16 v[80:83], v[170:173], v[206:209], v[80:83]
	v_mfma_f32_16x16x32_bf16 v[72:75], v[162:165], v[228:231], v[72:75]
	v_mfma_f32_16x16x32_bf16 v[64:67], v[170:173], v[228:231], v[64:67]
	s_setprio 0
	s_barrier
	s_add_i32 s28, s48, s4
	v_lshl_add_u64 v[182:183], s[30:31], 0, v[184:185]
	s_mov_b32 m0, s28
	ds_read_b128 v[174:177], v141 offset:16384
	ds_read_b128 v[178:181], v141 offset:17408
	ds_read_b128 v[194:197], v141 offset:18432
	ds_read_b128 v[198:201], v141 offset:19456
	ds_read_b128 v[202:205], v141 offset:20480
	ds_read_b128 v[206:209], v141 offset:21504
	ds_read_b128 v[224:227], v141 offset:22528
	ds_read_b128 v[228:231], v141 offset:23552
	global_load_lds_dwordx4 v[182:183], off
	s_add_i32 m0, s28, 0x2000
	s_add_u32 s28, s30, 0x80000
	v_lshl_add_u64 v[210:211], s[30:31], 0, v[128:129]
	s_addc_u32 s29, s31, 0
	s_add_i32 s48, s49, s4
	global_load_lds_dwordx4 v128, s[30:31]
	v_lshl_add_u64 v[216:217], s[28:29], 0, v[184:185]
	s_mov_b32 m0, s48
	s_nop 0
	global_load_lds_dwordx4 v[216:217], off
	s_add_i32 m0, s48, 0x2000
	s_nop 0
	global_load_lds_dwordx4 v128, s[28:29]
	s_mov_b32 m0, s20
	s_nop 0
	global_load_lds_dwordx4 v132, s[38:39]
	s_mov_b32 m0, s21
	s_nop 0
	global_load_lds_dwordx4 v130, s[38:39]
	s_waitcnt vmcnt(8)
	s_waitcnt lgkmcnt(0)
	s_barrier
	s_setprio 1
	s_waitcnt lgkmcnt(0)
	v_mfma_f32_16x16x32_bf16 v[60:63], v[142:145], v[174:177], v[60:63]
	v_mfma_f32_16x16x32_bf16 v[52:55], v[150:153], v[174:177], v[52:55]
	v_mfma_f32_16x16x32_bf16 v[44:47], v[142:145], v[194:197], v[44:47]
	v_mfma_f32_16x16x32_bf16 v[36:39], v[150:153], v[194:197], v[36:39]
	v_mfma_f32_16x16x32_bf16 v[28:31], v[142:145], v[202:205], v[28:31]
	v_mfma_f32_16x16x32_bf16 v[20:23], v[150:153], v[202:205], v[20:23]
	v_mfma_f32_16x16x32_bf16 v[12:15], v[142:145], v[224:227], v[12:15]
	v_mfma_f32_16x16x32_bf16 v[4:7], v[150:153], v[224:227], v[4:7]
	v_mfma_f32_16x16x32_bf16 v[60:63], v[146:149], v[178:181], v[60:63]
	v_mfma_f32_16x16x32_bf16 v[52:55], v[154:157], v[178:181], v[52:55]
	v_mfma_f32_16x16x32_bf16 v[44:47], v[146:149], v[198:201], v[44:47]
	v_mfma_f32_16x16x32_bf16 v[36:39], v[154:157], v[198:201], v[36:39]
	v_mfma_f32_16x16x32_bf16 v[28:31], v[146:149], v[206:209], v[28:31]
	v_mfma_f32_16x16x32_bf16 v[20:23], v[154:157], v[206:209], v[20:23]
	v_mfma_f32_16x16x32_bf16 v[12:15], v[146:149], v[228:231], v[12:15]
	v_mfma_f32_16x16x32_bf16 v[4:7], v[154:157], v[228:231], v[4:7]
	s_setprio 0
	s_setprio 1
	v_mfma_f32_16x16x32_bf16 v[56:59], v[158:161], v[174:177], v[56:59]
	v_mfma_f32_16x16x32_bf16 v[48:51], v[166:169], v[174:177], v[48:51]
	v_mfma_f32_16x16x32_bf16 v[40:43], v[158:161], v[194:197], v[40:43]
	v_mfma_f32_16x16x32_bf16 v[32:35], v[166:169], v[194:197], v[32:35]
	v_mfma_f32_16x16x32_bf16 v[24:27], v[158:161], v[202:205], v[24:27]
	v_mfma_f32_16x16x32_bf16 v[16:19], v[166:169], v[202:205], v[16:19]
	v_mfma_f32_16x16x32_bf16 v[8:11], v[158:161], v[224:227], v[8:11]
	v_mfma_f32_16x16x32_bf16 v[0:3], v[166:169], v[224:227], v[0:3]
	v_mfma_f32_16x16x32_bf16 v[56:59], v[162:165], v[178:181], v[56:59]
	v_mfma_f32_16x16x32_bf16 v[48:51], v[170:173], v[178:181], v[48:51]
	v_mfma_f32_16x16x32_bf16 v[40:43], v[162:165], v[198:201], v[40:43]
	v_mfma_f32_16x16x32_bf16 v[32:35], v[170:173], v[198:201], v[32:35]
	v_mfma_f32_16x16x32_bf16 v[24:27], v[162:165], v[206:209], v[24:27]
	v_mfma_f32_16x16x32_bf16 v[16:19], v[170:173], v[206:209], v[16:19]
	v_mfma_f32_16x16x32_bf16 v[8:11], v[162:165], v[228:231], v[8:11]
	v_mfma_f32_16x16x32_bf16 v[0:3], v[170:173], v[228:231], v[0:3]
	s_setprio 0
	s_barrier
	s_add_i32 s48, 0, 0x18000
	s_add_i32 s49, 0, 0x1c000
	v_add_u32_e32 v154, s48, v139
	v_add_u32_e32 v170, s49, v139
	ds_read_b128 v[142:145], v154
	ds_read_b128 v[146:149], v154 offset:1024
	ds_read_b128 v[150:153], v154 offset:2048
	ds_read_b128 v[154:157], v154 offset:3072
	ds_read_b128 v[158:161], v170
	ds_read_b128 v[162:165], v170 offset:1024
	ds_read_b128 v[166:169], v170 offset:2048
	ds_read_b128 v[170:173], v170 offset:3072
	s_add_u32 s28, s38, 0x80000
	s_addc_u32 s29, s39, 0
	s_mov_b32 m0, s26
	ds_read_b128 v[174:177], v141 offset:32768
	ds_read_b128 v[178:181], v141 offset:33792
	ds_read_b128 v[194:197], v141 offset:34816
	ds_read_b128 v[198:201], v141 offset:35840
	ds_read_b128 v[202:205], v141 offset:36864
	ds_read_b128 v[206:209], v141 offset:37888
	ds_read_b128 v[224:227], v141 offset:38912
	ds_read_b128 v[228:231], v141 offset:39936
	global_load_lds_dwordx4 v132, s[28:29]
	s_mov_b32 m0, s27
	s_nop 0
	global_load_lds_dwordx4 v130, s[28:29]
	s_waitcnt vmcnt(8)
	s_waitcnt lgkmcnt(0)
	s_barrier
	s_setprio 1
	s_waitcnt lgkmcnt(0)
	v_mfma_f32_16x16x32_bf16 v[124:127], v[142:145], v[174:177], v[124:127]
	v_mfma_f32_16x16x32_bf16 v[116:119], v[150:153], v[174:177], v[116:119]
	v_mfma_f32_16x16x32_bf16 v[108:111], v[142:145], v[194:197], v[108:111]
	v_mfma_f32_16x16x32_bf16 v[100:103], v[150:153], v[194:197], v[100:103]
	v_mfma_f32_16x16x32_bf16 v[92:95], v[142:145], v[202:205], v[92:95]
	v_mfma_f32_16x16x32_bf16 v[84:87], v[150:153], v[202:205], v[84:87]
	v_mfma_f32_16x16x32_bf16 v[76:79], v[142:145], v[224:227], v[76:79]
	v_mfma_f32_16x16x32_bf16 v[68:71], v[150:153], v[224:227], v[68:71]
	v_mfma_f32_16x16x32_bf16 v[124:127], v[146:149], v[178:181], v[124:127]
	v_mfma_f32_16x16x32_bf16 v[116:119], v[154:157], v[178:181], v[116:119]
	v_mfma_f32_16x16x32_bf16 v[108:111], v[146:149], v[198:201], v[108:111]
	v_mfma_f32_16x16x32_bf16 v[100:103], v[154:157], v[198:201], v[100:103]
	v_mfma_f32_16x16x32_bf16 v[92:95], v[146:149], v[206:209], v[92:95]
	v_mfma_f32_16x16x32_bf16 v[84:87], v[154:157], v[206:209], v[84:87]
	v_mfma_f32_16x16x32_bf16 v[76:79], v[146:149], v[228:231], v[76:79]
	v_mfma_f32_16x16x32_bf16 v[68:71], v[154:157], v[228:231], v[68:71]
	s_setprio 0
	s_setprio 1
	v_mfma_f32_16x16x32_bf16 v[120:123], v[158:161], v[174:177], v[120:123]
	v_mfma_f32_16x16x32_bf16 v[112:115], v[166:169], v[174:177], v[112:115]
	v_mfma_f32_16x16x32_bf16 v[104:107], v[158:161], v[194:197], v[104:107]
	v_mfma_f32_16x16x32_bf16 v[96:99], v[166:169], v[194:197], v[96:99]
	v_mfma_f32_16x16x32_bf16 v[88:91], v[158:161], v[202:205], v[88:91]
	v_mfma_f32_16x16x32_bf16 v[80:83], v[166:169], v[202:205], v[80:83]
	v_mfma_f32_16x16x32_bf16 v[72:75], v[158:161], v[224:227], v[72:75]
	v_mfma_f32_16x16x32_bf16 v[64:67], v[166:169], v[224:227], v[64:67]
	v_mfma_f32_16x16x32_bf16 v[120:123], v[162:165], v[178:181], v[120:123]
	v_mfma_f32_16x16x32_bf16 v[112:115], v[170:173], v[178:181], v[112:115]
	v_mfma_f32_16x16x32_bf16 v[104:107], v[162:165], v[198:201], v[104:107]
	v_mfma_f32_16x16x32_bf16 v[96:99], v[170:173], v[198:201], v[96:99]
	v_mfma_f32_16x16x32_bf16 v[88:91], v[162:165], v[206:209], v[88:91]
	v_mfma_f32_16x16x32_bf16 v[80:83], v[170:173], v[206:209], v[80:83]
	v_mfma_f32_16x16x32_bf16 v[72:75], v[162:165], v[228:231], v[72:75]
	v_mfma_f32_16x16x32_bf16 v[64:67], v[170:173], v[228:231], v[64:67]
	s_setprio 0
	s_barrier
	s_add_i32 s28, s48, s4
	v_lshl_add_u64 v[182:183], v[182:183], 0, s[68:69]
	s_mov_b32 m0, s28
	ds_read_b128 v[174:177], v141 offset:49152
	ds_read_b128 v[178:181], v141 offset:50176
	ds_read_b128 v[194:197], v141 offset:51200
	ds_read_b128 v[198:201], v141 offset:52224
	ds_read_b128 v[202:205], v141 offset:53248
	ds_read_b128 v[206:209], v141 offset:54272
	ds_read_b128 v[224:227], v141 offset:55296
	ds_read_b128 v[228:231], v141 offset:56320
	global_load_lds_dwordx4 v[182:183], off
	s_add_i32 m0, s28, 0x2000
	s_add_u32 s28, s30, 0x80080
	v_lshl_add_u64 v[182:183], v[210:211], 0, s[68:69]
	s_addc_u32 s29, s31, 0
	s_add_i32 s30, s49, s4
	global_load_lds_dwordx4 v[182:183], off
	v_lshl_add_u64 v[182:183], s[28:29], 0, v[184:185]
	s_mov_b32 m0, s30
	s_nop 0
	global_load_lds_dwordx4 v[182:183], off
	s_add_i32 m0, s30, 0x2000
	s_nop 0
	global_load_lds_dwordx4 v128, s[28:29]
	s_add_i32 m0, s40, 0xffffff80
	s_nop 0
	global_load_lds_dwordx4 v132, s[38:39] offset:128
	s_add_i32 m0, s41, 0xffffff80
	s_nop 0
	global_load_lds_dwordx4 v130, s[38:39] offset:128
	s_waitcnt vmcnt(8)
	s_waitcnt lgkmcnt(0)
	s_barrier
	s_setprio 1
	s_waitcnt lgkmcnt(0)
	v_mfma_f32_16x16x32_bf16 v[60:63], v[142:145], v[174:177], v[60:63]
	v_mfma_f32_16x16x32_bf16 v[52:55], v[150:153], v[174:177], v[52:55]
	v_mfma_f32_16x16x32_bf16 v[44:47], v[142:145], v[194:197], v[44:47]
	v_mfma_f32_16x16x32_bf16 v[36:39], v[150:153], v[194:197], v[36:39]
	v_mfma_f32_16x16x32_bf16 v[28:31], v[142:145], v[202:205], v[28:31]
	v_mfma_f32_16x16x32_bf16 v[20:23], v[150:153], v[202:205], v[20:23]
	v_mfma_f32_16x16x32_bf16 v[12:15], v[142:145], v[224:227], v[12:15]
	v_mfma_f32_16x16x32_bf16 v[4:7], v[150:153], v[224:227], v[4:7]
	v_mfma_f32_16x16x32_bf16 v[60:63], v[146:149], v[178:181], v[60:63]
	v_mfma_f32_16x16x32_bf16 v[52:55], v[154:157], v[178:181], v[52:55]
	v_mfma_f32_16x16x32_bf16 v[44:47], v[146:149], v[198:201], v[44:47]
	v_mfma_f32_16x16x32_bf16 v[36:39], v[154:157], v[198:201], v[36:39]
	v_mfma_f32_16x16x32_bf16 v[28:31], v[146:149], v[206:209], v[28:31]
	v_mfma_f32_16x16x32_bf16 v[20:23], v[154:157], v[206:209], v[20:23]
	v_mfma_f32_16x16x32_bf16 v[12:15], v[146:149], v[228:231], v[12:15]
	v_mfma_f32_16x16x32_bf16 v[4:7], v[154:157], v[228:231], v[4:7]
	s_setprio 0
	s_setprio 1
	v_mfma_f32_16x16x32_bf16 v[56:59], v[158:161], v[174:177], v[56:59]
	v_mfma_f32_16x16x32_bf16 v[48:51], v[166:169], v[174:177], v[48:51]
	v_mfma_f32_16x16x32_bf16 v[40:43], v[158:161], v[194:197], v[40:43]
	v_mfma_f32_16x16x32_bf16 v[32:35], v[166:169], v[194:197], v[32:35]
	v_mfma_f32_16x16x32_bf16 v[24:27], v[158:161], v[202:205], v[24:27]
	v_mfma_f32_16x16x32_bf16 v[16:19], v[166:169], v[202:205], v[16:19]
	v_mfma_f32_16x16x32_bf16 v[8:11], v[158:161], v[224:227], v[8:11]
	v_mfma_f32_16x16x32_bf16 v[0:3], v[166:169], v[224:227], v[0:3]
	v_mfma_f32_16x16x32_bf16 v[56:59], v[162:165], v[178:181], v[56:59]
	v_mfma_f32_16x16x32_bf16 v[48:51], v[170:173], v[178:181], v[48:51]
	v_mfma_f32_16x16x32_bf16 v[40:43], v[162:165], v[198:201], v[40:43]
	v_mfma_f32_16x16x32_bf16 v[32:35], v[170:173], v[198:201], v[32:35]
	v_mfma_f32_16x16x32_bf16 v[24:27], v[162:165], v[206:209], v[24:27]
	v_mfma_f32_16x16x32_bf16 v[16:19], v[170:173], v[206:209], v[16:19]
	v_mfma_f32_16x16x32_bf16 v[8:11], v[162:165], v[228:231], v[8:11]
	v_mfma_f32_16x16x32_bf16 v[0:3], v[170:173], v[228:231], v[0:3]
	s_setprio 0
	s_barrier
	s_add_i32 s51, s51, 2
	s_add_u32 s24, s24, 0x100
	s_addc_u32 s25, s25, 0
	s_add_u32 s47, s47, 0x100
	s_addc_u32 s50, s50, 0
	s_cmp_gt_u32 s51, 29
	s_cbranch_scc0 .LBB0_1587
	s_and_b64 vcc, exec, s[6:7]
	s_cbranch_vccz .LBB0_1590
	s_barrier

.LBB0_1661:
	s_add_u32 s24, s18, 0x100
	s_addc_u32 s25, s19, 0
	s_add_i32 s28, 0, 0x10000
	s_cmpk_eq_i32 s61, 0x54
	s_cselect_b32 s39, s51, s25
	s_cselect_b32 s38, s52, s24
	s_cselect_b32 s31, s53, s60
	s_cselect_b32 s30, s58, s59
	s_add_i32 s29, 0, 0x14000
	s_waitcnt vmcnt(0)
	v_add_u32_e32 v84, s28, v163
	v_add_u32_e32 v170, s29, v163
	ds_read_b128 v[64:67], v84
	ds_read_b128 v[68:71], v84 offset:1024
	ds_read_b128 v[80:83], v84 offset:2048
	ds_read_b128 v[84:87], v84 offset:3072
	ds_read_b128 v[154:157], v170
	ds_read_b128 v[158:161], v170 offset:1024
	ds_read_b128 v[166:169], v170 offset:2048
	ds_read_b128 v[170:173], v170 offset:3072
	v_lshl_add_u64 v[182:183], s[18:19], 0, v[150:151]
	s_add_i32 m0, s20, 0xc000
	ds_read_b128 v[174:177], v165
	ds_read_b128 v[178:181], v165 offset:1024
	ds_read_b128 v[194:197], v165 offset:2048
	ds_read_b128 v[198:201], v165 offset:3072
	ds_read_b128 v[202:205], v165 offset:4096
	ds_read_b128 v[206:209], v165 offset:5120
	ds_read_b128 v[224:227], v165 offset:6144
	ds_read_b128 v[228:231], v165 offset:7168
	global_load_lds_dwordx4 v[182:183], off
	v_lshl_add_u64 v[182:183], s[18:19], 0, v[152:153]
	s_add_i32 m0, s20, 0xe000
	s_nop 0
	global_load_lds_dwordx4 v[182:183], off
	s_waitcnt vmcnt(8)
	s_waitcnt lgkmcnt(0)
	s_barrier
	s_setprio 1
	s_waitcnt lgkmcnt(0)
	v_mfma_f32_16x16x32_bf16 v[140:143], v[64:67], v[174:177], v[140:143]
	v_mfma_f32_16x16x32_bf16 v[136:139], v[80:83], v[174:177], v[136:139]
	v_mfma_f32_16x16x32_bf16 v[124:127], v[64:67], v[194:197], v[124:127]
	v_mfma_f32_16x16x32_bf16 v[120:123], v[80:83], v[194:197], v[120:123]
	v_mfma_f32_16x16x32_bf16 v[108:111], v[64:67], v[202:205], v[108:111]
	v_mfma_f32_16x16x32_bf16 v[104:107], v[80:83], v[202:205], v[104:107]
	v_mfma_f32_16x16x32_bf16 v[92:95], v[64:67], v[224:227], v[92:95]
	v_mfma_f32_16x16x32_bf16 v[88:91], v[80:83], v[224:227], v[88:91]
	v_mfma_f32_16x16x32_bf16 v[140:143], v[68:71], v[178:181], v[140:143]
	v_mfma_f32_16x16x32_bf16 v[136:139], v[84:87], v[178:181], v[136:139]
	v_mfma_f32_16x16x32_bf16 v[124:127], v[68:71], v[198:201], v[124:127]
	v_mfma_f32_16x16x32_bf16 v[120:123], v[84:87], v[198:201], v[120:123]
	v_mfma_f32_16x16x32_bf16 v[108:111], v[68:71], v[206:209], v[108:111]
	v_mfma_f32_16x16x32_bf16 v[104:107], v[84:87], v[206:209], v[104:107]
	v_mfma_f32_16x16x32_bf16 v[92:95], v[68:71], v[228:231], v[92:95]
	v_mfma_f32_16x16x32_bf16 v[88:91], v[84:87], v[228:231], v[88:91]
	s_setprio 0
	s_setprio 1
	v_mfma_f32_16x16x32_bf16 v[132:135], v[154:157], v[174:177], v[132:135]
	v_mfma_f32_16x16x32_bf16 v[128:131], v[166:169], v[174:177], v[128:131]
	v_mfma_f32_16x16x32_bf16 v[116:119], v[154:157], v[194:197], v[116:119]
	v_mfma_f32_16x16x32_bf16 v[112:115], v[166:169], v[194:197], v[112:115]
	v_mfma_f32_16x16x32_bf16 v[100:103], v[154:157], v[202:205], v[100:103]
	v_mfma_f32_16x16x32_bf16 v[96:99], v[166:169], v[202:205], v[96:99]
	v_mfma_f32_16x16x32_bf16 v[76:79], v[154:157], v[224:227], v[76:79]
	v_mfma_f32_16x16x32_bf16 v[72:75], v[166:169], v[224:227], v[72:75]
	v_mfma_f32_16x16x32_bf16 v[132:135], v[158:161], v[178:181], v[132:135]
	v_mfma_f32_16x16x32_bf16 v[128:131], v[170:173], v[178:181], v[128:131]
	v_mfma_f32_16x16x32_bf16 v[116:119], v[158:161], v[198:201], v[116:119]
	v_mfma_f32_16x16x32_bf16 v[112:115], v[170:173], v[198:201], v[112:115]
	v_mfma_f32_16x16x32_bf16 v[100:103], v[158:161], v[206:209], v[100:103]
	v_mfma_f32_16x16x32_bf16 v[96:99], v[170:173], v[206:209], v[96:99]
	v_mfma_f32_16x16x32_bf16 v[76:79], v[158:161], v[228:231], v[76:79]
	v_mfma_f32_16x16x32_bf16 v[72:75], v[170:173], v[228:231], v[72:75]
	s_setprio 0
	s_barrier
	s_add_i32 s18, s28, s4
	v_lshl_add_u64 v[182:183], s[30:31], 0, v[184:185]
	s_mov_b32 m0, s18
	ds_read_b128 v[174:177], v165 offset:16384
	ds_read_b128 v[178:181], v165 offset:17408
	ds_read_b128 v[194:197], v165 offset:18432
	ds_read_b128 v[198:201], v165 offset:19456
	ds_read_b128 v[202:205], v165 offset:20480
	ds_read_b128 v[206:209], v165 offset:21504
	ds_read_b128 v[224:227], v165 offset:22528
	ds_read_b128 v[228:231], v165 offset:23552
	global_load_lds_dwordx4 v[182:183], off
	s_add_i32 m0, s18, 0x2000
	s_add_u32 s18, s30, 0x160000
	s_addc_u32 s19, s31, 0
	s_add_i32 s28, s29, s4
	global_load_lds_dwordx4 v144, s[30:31]
	v_lshl_add_u64 v[216:217], s[18:19], 0, v[184:185]
	s_mov_b32 m0, s28
	s_nop 0
	global_load_lds_dwordx4 v[216:217], off
	s_add_i32 m0, s28, 0x2000
	s_nop 0
	global_load_lds_dwordx4 v144, s[18:19]
	s_mov_b32 m0, s20
	s_nop 0
	global_load_lds_dwordx4 v148, s[38:39]
	s_mov_b32 m0, s21
	s_nop 0
	global_load_lds_dwordx4 v146, s[38:39]
	s_waitcnt vmcnt(8)
	s_waitcnt lgkmcnt(0)
	s_barrier
	s_setprio 1
	s_waitcnt lgkmcnt(0)
	v_mfma_f32_16x16x32_bf16 v[60:63], v[64:67], v[174:177], v[60:63]
	v_mfma_f32_16x16x32_bf16 v[56:59], v[80:83], v[174:177], v[56:59]
	v_mfma_f32_16x16x32_bf16 v[44:47], v[64:67], v[194:197], v[44:47]
	v_mfma_f32_16x16x32_bf16 v[40:43], v[80:83], v[194:197], v[40:43]
	v_mfma_f32_16x16x32_bf16 v[28:31], v[64:67], v[202:205], v[28:31]
	v_mfma_f32_16x16x32_bf16 v[24:27], v[80:83], v[202:205], v[24:27]
	v_mfma_f32_16x16x32_bf16 v[12:15], v[64:67], v[224:227], v[12:15]
	v_mfma_f32_16x16x32_bf16 v[8:11], v[80:83], v[224:227], v[8:11]
	v_mfma_f32_16x16x32_bf16 v[60:63], v[68:71], v[178:181], v[60:63]
	v_mfma_f32_16x16x32_bf16 v[56:59], v[84:87], v[178:181], v[56:59]
	v_mfma_f32_16x16x32_bf16 v[44:47], v[68:71], v[198:201], v[44:47]
	v_mfma_f32_16x16x32_bf16 v[40:43], v[84:87], v[198:201], v[40:43]
	v_mfma_f32_16x16x32_bf16 v[28:31], v[68:71], v[206:209], v[28:31]
	v_mfma_f32_16x16x32_bf16 v[24:27], v[84:87], v[206:209], v[24:27]
	v_mfma_f32_16x16x32_bf16 v[12:15], v[68:71], v[228:231], v[12:15]
	v_mfma_f32_16x16x32_bf16 v[8:11], v[84:87], v[228:231], v[8:11]
	s_setprio 0
	s_setprio 1
	v_mfma_f32_16x16x32_bf16 v[52:55], v[154:157], v[174:177], v[52:55]
	v_mfma_f32_16x16x32_bf16 v[48:51], v[166:169], v[174:177], v[48:51]
	v_mfma_f32_16x16x32_bf16 v[36:39], v[154:157], v[194:197], v[36:39]
	v_mfma_f32_16x16x32_bf16 v[32:35], v[166:169], v[194:197], v[32:35]
	v_mfma_f32_16x16x32_bf16 v[20:23], v[154:157], v[202:205], v[20:23]
	v_mfma_f32_16x16x32_bf16 v[16:19], v[166:169], v[202:205], v[16:19]
	v_mfma_f32_16x16x32_bf16 v[4:7], v[154:157], v[224:227], v[4:7]
	v_mfma_f32_16x16x32_bf16 v[0:3], v[166:169], v[224:227], v[0:3]
	v_mfma_f32_16x16x32_bf16 v[52:55], v[158:161], v[178:181], v[52:55]
	v_mfma_f32_16x16x32_bf16 v[48:51], v[170:173], v[178:181], v[48:51]
	v_mfma_f32_16x16x32_bf16 v[36:39], v[158:161], v[198:201], v[36:39]
	v_mfma_f32_16x16x32_bf16 v[32:35], v[170:173], v[198:201], v[32:35]
	v_mfma_f32_16x16x32_bf16 v[20:23], v[158:161], v[206:209], v[20:23]
	v_mfma_f32_16x16x32_bf16 v[16:19], v[170:173], v[206:209], v[16:19]
	v_mfma_f32_16x16x32_bf16 v[4:7], v[158:161], v[228:231], v[4:7]
	v_mfma_f32_16x16x32_bf16 v[0:3], v[170:173], v[228:231], v[0:3]
	s_setprio 0
	s_barrier
	s_add_i32 s28, 0, 0x18000
	s_add_i32 s29, 0, 0x1c000
	v_add_u32_e32 v84, s28, v163
	v_add_u32_e32 v170, s29, v163
	ds_read_b128 v[64:67], v84
	ds_read_b128 v[68:71], v84 offset:1024
	ds_read_b128 v[80:83], v84 offset:2048
	ds_read_b128 v[84:87], v84 offset:3072
	ds_read_b128 v[154:157], v170
	ds_read_b128 v[158:161], v170 offset:1024
	ds_read_b128 v[166:169], v170 offset:2048
	ds_read_b128 v[170:173], v170 offset:3072
	s_add_u32 s18, s38, 0x160000
	s_addc_u32 s19, s39, 0
	s_mov_b32 m0, s26
	ds_read_b128 v[174:177], v165 offset:32768
	ds_read_b128 v[178:181], v165 offset:33792
	ds_read_b128 v[194:197], v165 offset:34816
	ds_read_b128 v[198:201], v165 offset:35840
	ds_read_b128 v[202:205], v165 offset:36864
	ds_read_b128 v[206:209], v165 offset:37888
	ds_read_b128 v[224:227], v165 offset:38912
	ds_read_b128 v[228:231], v165 offset:39936
	global_load_lds_dwordx4 v148, s[18:19]
	s_mov_b32 m0, s27
	s_nop 0
	global_load_lds_dwordx4 v146, s[18:19]
	s_waitcnt vmcnt(8)
	s_waitcnt lgkmcnt(0)
	s_barrier
	s_setprio 1
	s_waitcnt lgkmcnt(0)
	v_mfma_f32_16x16x32_bf16 v[140:143], v[64:67], v[174:177], v[140:143]
	v_mfma_f32_16x16x32_bf16 v[136:139], v[80:83], v[174:177], v[136:139]
	v_mfma_f32_16x16x32_bf16 v[124:127], v[64:67], v[194:197], v[124:127]
	v_mfma_f32_16x16x32_bf16 v[120:123], v[80:83], v[194:197], v[120:123]
	v_mfma_f32_16x16x32_bf16 v[108:111], v[64:67], v[202:205], v[108:111]
	v_mfma_f32_16x16x32_bf16 v[104:107], v[80:83], v[202:205], v[104:107]
	v_mfma_f32_16x16x32_bf16 v[92:95], v[64:67], v[224:227], v[92:95]
	v_mfma_f32_16x16x32_bf16 v[88:91], v[80:83], v[224:227], v[88:91]
	v_mfma_f32_16x16x32_bf16 v[140:143], v[68:71], v[178:181], v[140:143]
	v_mfma_f32_16x16x32_bf16 v[136:139], v[84:87], v[178:181], v[136:139]
	v_mfma_f32_16x16x32_bf16 v[124:127], v[68:71], v[198:201], v[124:127]
	v_mfma_f32_16x16x32_bf16 v[120:123], v[84:87], v[198:201], v[120:123]
	v_mfma_f32_16x16x32_bf16 v[108:111], v[68:71], v[206:209], v[108:111]
	v_mfma_f32_16x16x32_bf16 v[104:107], v[84:87], v[206:209], v[104:107]
	v_mfma_f32_16x16x32_bf16 v[92:95], v[68:71], v[228:231], v[92:95]
	v_mfma_f32_16x16x32_bf16 v[88:91], v[84:87], v[228:231], v[88:91]
	s_setprio 0
	s_setprio 1
	v_mfma_f32_16x16x32_bf16 v[132:135], v[154:157], v[174:177], v[132:135]
	v_mfma_f32_16x16x32_bf16 v[128:131], v[166:169], v[174:177], v[128:131]
	v_mfma_f32_16x16x32_bf16 v[116:119], v[154:157], v[194:197], v[116:119]
	v_mfma_f32_16x16x32_bf16 v[112:115], v[166:169], v[194:197], v[112:115]
	v_mfma_f32_16x16x32_bf16 v[100:103], v[154:157], v[202:205], v[100:103]
	v_mfma_f32_16x16x32_bf16 v[96:99], v[166:169], v[202:205], v[96:99]
	v_mfma_f32_16x16x32_bf16 v[76:79], v[154:157], v[224:227], v[76:79]
	v_mfma_f32_16x16x32_bf16 v[72:75], v[166:169], v[224:227], v[72:75]
	v_mfma_f32_16x16x32_bf16 v[132:135], v[158:161], v[178:181], v[132:135]
	v_mfma_f32_16x16x32_bf16 v[128:131], v[170:173], v[178:181], v[128:131]
	v_mfma_f32_16x16x32_bf16 v[116:119], v[158:161], v[198:201], v[116:119]
	v_mfma_f32_16x16x32_bf16 v[112:115], v[170:173], v[198:201], v[112:115]
	v_mfma_f32_16x16x32_bf16 v[100:103], v[158:161], v[206:209], v[100:103]
	v_mfma_f32_16x16x32_bf16 v[96:99], v[170:173], v[206:209], v[96:99]
	v_mfma_f32_16x16x32_bf16 v[76:79], v[158:161], v[228:231], v[76:79]
	v_mfma_f32_16x16x32_bf16 v[72:75], v[170:173], v[228:231], v[72:75]
	s_setprio 0
	s_barrier
	s_add_i32 s18, s28, s4
	v_lshl_add_u64 v[182:183], v[182:183], 0, s[68:69]
	s_mov_b32 m0, s18
	ds_read_b128 v[174:177], v165 offset:49152
	ds_read_b128 v[178:181], v165 offset:50176
	ds_read_b128 v[194:197], v165 offset:51200
	ds_read_b128 v[198:201], v165 offset:52224
	ds_read_b128 v[202:205], v165 offset:53248
	ds_read_b128 v[206:209], v165 offset:54272
	ds_read_b128 v[224:227], v165 offset:55296
	ds_read_b128 v[228:231], v165 offset:56320
	global_load_lds_dwordx4 v[182:183], off
	s_add_i32 m0, s18, 0x1f80
	s_add_u32 s18, s30, 0x160080
	s_addc_u32 s19, s31, 0
	s_add_i32 s28, s29, s4
	global_load_lds_dwordx4 v144, s[30:31] offset:128
	v_lshl_add_u64 v[182:183], s[18:19], 0, v[184:185]
	s_mov_b32 m0, s28
	s_nop 0
	global_load_lds_dwordx4 v[182:183], off
	s_add_i32 m0, s28, 0x2000
	s_nop 0
	global_load_lds_dwordx4 v144, s[18:19]
	s_add_i32 m0, s42, 0xffffff80
	s_nop 0
	global_load_lds_dwordx4 v148, s[38:39] offset:128
	s_add_i32 m0, s43, 0xffffff80
	s_nop 0
	global_load_lds_dwordx4 v146, s[38:39] offset:128
	s_waitcnt vmcnt(8)
	s_waitcnt lgkmcnt(0)
	s_barrier
	s_setprio 1
	s_waitcnt lgkmcnt(0)
	v_mfma_f32_16x16x32_bf16 v[60:63], v[64:67], v[174:177], v[60:63]
	v_mfma_f32_16x16x32_bf16 v[56:59], v[80:83], v[174:177], v[56:59]
	v_mfma_f32_16x16x32_bf16 v[44:47], v[64:67], v[194:197], v[44:47]
	v_mfma_f32_16x16x32_bf16 v[40:43], v[80:83], v[194:197], v[40:43]
	v_mfma_f32_16x16x32_bf16 v[28:31], v[64:67], v[202:205], v[28:31]
	v_mfma_f32_16x16x32_bf16 v[24:27], v[80:83], v[202:205], v[24:27]
	v_mfma_f32_16x16x32_bf16 v[12:15], v[64:67], v[224:227], v[12:15]
	v_mfma_f32_16x16x32_bf16 v[8:11], v[80:83], v[224:227], v[8:11]
	v_mfma_f32_16x16x32_bf16 v[60:63], v[68:71], v[178:181], v[60:63]
	v_mfma_f32_16x16x32_bf16 v[56:59], v[84:87], v[178:181], v[56:59]
	v_mfma_f32_16x16x32_bf16 v[44:47], v[68:71], v[198:201], v[44:47]
	v_mfma_f32_16x16x32_bf16 v[40:43], v[84:87], v[198:201], v[40:43]
	v_mfma_f32_16x16x32_bf16 v[28:31], v[68:71], v[206:209], v[28:31]
	v_mfma_f32_16x16x32_bf16 v[24:27], v[84:87], v[206:209], v[24:27]
	v_mfma_f32_16x16x32_bf16 v[12:15], v[68:71], v[228:231], v[12:15]
	v_mfma_f32_16x16x32_bf16 v[8:11], v[84:87], v[228:231], v[8:11]
	s_setprio 0
	s_setprio 1
	v_mfma_f32_16x16x32_bf16 v[52:55], v[154:157], v[174:177], v[52:55]
	v_mfma_f32_16x16x32_bf16 v[48:51], v[166:169], v[174:177], v[48:51]
	v_mfma_f32_16x16x32_bf16 v[36:39], v[154:157], v[194:197], v[36:39]
	v_mfma_f32_16x16x32_bf16 v[32:35], v[166:169], v[194:197], v[32:35]
	v_mfma_f32_16x16x32_bf16 v[20:23], v[154:157], v[202:205], v[20:23]
	v_mfma_f32_16x16x32_bf16 v[16:19], v[166:169], v[202:205], v[16:19]
	v_mfma_f32_16x16x32_bf16 v[4:7], v[154:157], v[224:227], v[4:7]
	v_mfma_f32_16x16x32_bf16 v[0:3], v[166:169], v[224:227], v[0:3]
	v_mfma_f32_16x16x32_bf16 v[52:55], v[158:161], v[178:181], v[52:55]
	v_mfma_f32_16x16x32_bf16 v[48:51], v[170:173], v[178:181], v[48:51]
	v_mfma_f32_16x16x32_bf16 v[36:39], v[158:161], v[198:201], v[36:39]
	v_mfma_f32_16x16x32_bf16 v[32:35], v[170:173], v[198:201], v[32:35]
	v_mfma_f32_16x16x32_bf16 v[20:23], v[158:161], v[206:209], v[20:23]
	v_mfma_f32_16x16x32_bf16 v[16:19], v[170:173], v[206:209], v[16:19]
	v_mfma_f32_16x16x32_bf16 v[4:7], v[158:161], v[228:231], v[4:7]
	v_mfma_f32_16x16x32_bf16 v[0:3], v[170:173], v[228:231], v[0:3]
	s_setprio 0
	s_barrier
	s_add_i32 s61, s61, 2
	s_add_u32 s59, s59, 0x100
	s_addc_u32 s60, s60, 0
	s_cmpk_gt_u32 s61, 0x55
	s_mov_b64 s[18:19], s[24:25]
	s_cbranch_scc0 .LBB0_1661
	s_and_b64 vcc, exec, s[8:9]
	s_cbranch_vccz .LBB0_1664
	s_barrier

.LBB0_1741:
	s_add_u32 s38, s36, 0x100
	s_addc_u32 s39, s37, 0
	s_add_i32 s28, 0, 0x10000
	s_cmp_eq_u32 s59, 4
	s_cselect_b32 s43, s11, s39
	s_cselect_b32 s42, s50, s38
	s_cselect_b32 s41, s51, s58
	s_cselect_b32 s40, s52, s53
	s_add_i32 s48, 0, 0x14000
	v_add_u32_e32 v124, s28, v172
	v_add_u32_e32 v170, s48, v172
	ds_read_b128 v[112:115], v124
	ds_read_b128 v[116:119], v124 offset:1024
	ds_read_b128 v[120:123], v124 offset:2048
	ds_read_b128 v[124:127], v124 offset:3072
	ds_read_b128 v[176:179], v170
	ds_read_b128 v[180:183], v170 offset:1024
	ds_read_b128 v[194:197], v170 offset:2048
	ds_read_b128 v[198:201], v170 offset:3072
	v_lshl_add_u64 v[170:171], s[36:37], 0, v[166:167]
	s_add_i32 m0, s20, 0xc000
	ds_read_b128 v[202:205], v174
	ds_read_b128 v[206:209], v174 offset:1024
	ds_read_b128 v[224:227], v174 offset:2048
	ds_read_b128 v[228:231], v174 offset:3072
	ds_read_b128 v[232:235], v174 offset:4096
	ds_read_b128 v[236:239], v174 offset:5120
	ds_read_b128 v[240:243], v174 offset:6144
	ds_read_b128 v[244:247], v174 offset:7168
	global_load_lds_dwordx4 v[170:171], off
	v_lshl_add_u64 v[170:171], s[36:37], 0, v[168:169]
	s_add_i32 m0, s20, 0xe000
	s_nop 0
	global_load_lds_dwordx4 v[170:171], off
	s_waitcnt vmcnt(8)
	s_waitcnt lgkmcnt(0)
	s_barrier
	s_setprio 1
	s_waitcnt lgkmcnt(0)
	v_mfma_f32_16x16x32_bf16 v[140:143], v[112:115], v[202:205], v[140:143]
	v_mfma_f32_16x16x32_bf16 v[136:139], v[120:123], v[202:205], v[136:139]
	v_mfma_f32_16x16x32_bf16 v[108:111], v[112:115], v[224:227], v[108:111]
	v_mfma_f32_16x16x32_bf16 v[104:107], v[120:123], v[224:227], v[104:107]
	v_mfma_f32_16x16x32_bf16 v[92:95], v[112:115], v[232:235], v[92:95]
	v_mfma_f32_16x16x32_bf16 v[88:91], v[120:123], v[232:235], v[88:91]
	v_mfma_f32_16x16x32_bf16 v[76:79], v[112:115], v[240:243], v[76:79]
	v_mfma_f32_16x16x32_bf16 v[72:75], v[120:123], v[240:243], v[72:75]
	v_mfma_f32_16x16x32_bf16 v[140:143], v[116:119], v[206:209], v[140:143]
	v_mfma_f32_16x16x32_bf16 v[136:139], v[124:127], v[206:209], v[136:139]
	v_mfma_f32_16x16x32_bf16 v[108:111], v[116:119], v[228:231], v[108:111]
	v_mfma_f32_16x16x32_bf16 v[104:107], v[124:127], v[228:231], v[104:107]
	v_mfma_f32_16x16x32_bf16 v[92:95], v[116:119], v[236:239], v[92:95]
	v_mfma_f32_16x16x32_bf16 v[88:91], v[124:127], v[236:239], v[88:91]
	v_mfma_f32_16x16x32_bf16 v[76:79], v[116:119], v[244:247], v[76:79]
	v_mfma_f32_16x16x32_bf16 v[72:75], v[124:127], v[244:247], v[72:75]
	s_setprio 0
	s_setprio 1
	v_mfma_f32_16x16x32_bf16 v[132:135], v[176:179], v[202:205], v[132:135]
	v_mfma_f32_16x16x32_bf16 v[128:131], v[194:197], v[202:205], v[128:131]
	v_mfma_f32_16x16x32_bf16 v[100:103], v[176:179], v[224:227], v[100:103]
	v_mfma_f32_16x16x32_bf16 v[96:99], v[194:197], v[224:227], v[96:99]
	v_mfma_f32_16x16x32_bf16 v[84:87], v[176:179], v[232:235], v[84:87]
	v_mfma_f32_16x16x32_bf16 v[80:83], v[194:197], v[232:235], v[80:83]
	v_mfma_f32_16x16x32_bf16 v[68:71], v[176:179], v[240:243], v[68:71]
	v_mfma_f32_16x16x32_bf16 v[64:67], v[194:197], v[240:243], v[64:67]
	v_mfma_f32_16x16x32_bf16 v[132:135], v[180:183], v[206:209], v[132:135]
	v_mfma_f32_16x16x32_bf16 v[128:131], v[198:201], v[206:209], v[128:131]
	v_mfma_f32_16x16x32_bf16 v[100:103], v[180:183], v[228:231], v[100:103]
	v_mfma_f32_16x16x32_bf16 v[96:99], v[198:201], v[228:231], v[96:99]
	v_mfma_f32_16x16x32_bf16 v[84:87], v[180:183], v[236:239], v[84:87]
	v_mfma_f32_16x16x32_bf16 v[80:83], v[198:201], v[236:239], v[80:83]
	v_mfma_f32_16x16x32_bf16 v[68:71], v[180:183], v[244:247], v[68:71]
	v_mfma_f32_16x16x32_bf16 v[64:67], v[198:201], v[244:247], v[64:67]
	s_setprio 0
	s_barrier
	s_add_i32 s28, s28, s4
	v_lshl_add_u64 v[170:171], s[40:41], 0, v[184:185]
	s_mov_b32 m0, s28
	ds_read_b128 v[202:205], v174 offset:16384
	ds_read_b128 v[206:209], v174 offset:17408
	ds_read_b128 v[224:227], v174 offset:18432
	ds_read_b128 v[228:231], v174 offset:19456
	ds_read_b128 v[232:235], v174 offset:20480
	ds_read_b128 v[236:239], v174 offset:21504
	ds_read_b128 v[240:243], v174 offset:22528
	ds_read_b128 v[244:247], v174 offset:23552
	global_load_lds_dwordx4 v[170:171], off
	s_add_i32 m0, s28, 0x2000
	s_add_u32 s28, s40, 0x160000
	s_addc_u32 s29, s41, 0
	s_add_i32 s36, s48, s4
	global_load_lds_dwordx4 v144, s[40:41]
	v_lshl_add_u64 v[216:217], s[28:29], 0, v[184:185]
	s_mov_b32 m0, s36
	v_lshl_add_u64 v[218:219], s[42:43], 0, v[146:147]
	global_load_lds_dwordx4 v[216:217], off
	s_add_i32 m0, s36, 0x2000
	s_nop 0
	global_load_lds_dwordx4 v144, s[28:29]
	s_mov_b32 m0, s20
	s_nop 0
	global_load_lds_dwordx4 v148, s[42:43]
	s_mov_b32 m0, s21
	s_nop 0
	global_load_lds_dwordx4 v146, s[42:43]
	s_waitcnt vmcnt(8)
	s_waitcnt lgkmcnt(0)
	s_barrier
	s_setprio 1
	s_waitcnt lgkmcnt(0)
	v_mfma_f32_16x16x32_bf16 v[60:63], v[112:115], v[202:205], v[60:63]
	v_mfma_f32_16x16x32_bf16 v[56:59], v[120:123], v[202:205], v[56:59]
	v_mfma_f32_16x16x32_bf16 v[44:47], v[112:115], v[224:227], v[44:47]
	v_mfma_f32_16x16x32_bf16 v[40:43], v[120:123], v[224:227], v[40:43]
	v_mfma_f32_16x16x32_bf16 v[36:39], v[112:115], v[232:235], v[36:39]
	v_mfma_f32_16x16x32_bf16 v[28:31], v[120:123], v[232:235], v[28:31]
	v_mfma_f32_16x16x32_bf16 v[20:23], v[112:115], v[240:243], v[20:23]
	v_mfma_f32_16x16x32_bf16 v[12:15], v[120:123], v[240:243], v[12:15]
	v_mfma_f32_16x16x32_bf16 v[60:63], v[116:119], v[206:209], v[60:63]
	v_mfma_f32_16x16x32_bf16 v[56:59], v[124:127], v[206:209], v[56:59]
	v_mfma_f32_16x16x32_bf16 v[44:47], v[116:119], v[228:231], v[44:47]
	v_mfma_f32_16x16x32_bf16 v[40:43], v[124:127], v[228:231], v[40:43]
	v_mfma_f32_16x16x32_bf16 v[36:39], v[116:119], v[236:239], v[36:39]
	v_mfma_f32_16x16x32_bf16 v[28:31], v[124:127], v[236:239], v[28:31]
	v_mfma_f32_16x16x32_bf16 v[20:23], v[116:119], v[244:247], v[20:23]
	v_mfma_f32_16x16x32_bf16 v[12:15], v[124:127], v[244:247], v[12:15]
	s_setprio 0
	s_setprio 1
	v_mfma_f32_16x16x32_bf16 v[52:55], v[176:179], v[202:205], v[52:55]
	v_mfma_f32_16x16x32_bf16 v[48:51], v[194:197], v[202:205], v[48:51]
	v_mfma_f32_16x16x32_bf16 v[32:35], v[176:179], v[224:227], v[32:35]
	v_mfma_f32_16x16x32_bf16 v[24:27], v[194:197], v[224:227], v[24:27]
	v_mfma_f32_16x16x32_bf16 v[16:19], v[176:179], v[232:235], v[16:19]
	v_mfma_f32_16x16x32_bf16 v[8:11], v[194:197], v[232:235], v[8:11]
	v_mfma_f32_16x16x32_bf16 v[4:7], v[176:179], v[240:243], v[4:7]
	v_mfma_f32_16x16x32_bf16 v[0:3], v[194:197], v[240:243], v[0:3]
	v_mfma_f32_16x16x32_bf16 v[52:55], v[180:183], v[206:209], v[52:55]
	v_mfma_f32_16x16x32_bf16 v[48:51], v[198:201], v[206:209], v[48:51]
	v_mfma_f32_16x16x32_bf16 v[32:35], v[180:183], v[228:231], v[32:35]
	v_mfma_f32_16x16x32_bf16 v[24:27], v[198:201], v[228:231], v[24:27]
	v_mfma_f32_16x16x32_bf16 v[16:19], v[180:183], v[236:239], v[16:19]
	v_mfma_f32_16x16x32_bf16 v[8:11], v[198:201], v[236:239], v[8:11]
	v_mfma_f32_16x16x32_bf16 v[4:7], v[180:183], v[244:247], v[4:7]
	v_mfma_f32_16x16x32_bf16 v[0:3], v[198:201], v[244:247], v[0:3]
	s_setprio 0
	s_barrier
	s_add_i32 s36, 0, 0x18000
	s_add_i32 s37, 0, 0x1c000
	v_add_u32_e32 v124, s36, v172
	v_add_u32_e32 v175, s37, v172
	ds_read_b128 v[112:115], v124
	ds_read_b128 v[116:119], v124 offset:1024
	ds_read_b128 v[120:123], v124 offset:2048
	ds_read_b128 v[124:127], v124 offset:3072
	ds_read_b128 v[176:179], v175
	ds_read_b128 v[180:183], v175 offset:1024
	ds_read_b128 v[194:197], v175 offset:2048
	ds_read_b128 v[198:201], v175 offset:3072
	s_add_u32 s28, s42, 0x160000
	s_addc_u32 s29, s43, 0
	s_mov_b32 m0, s26
	ds_read_b128 v[202:205], v174 offset:32768
	ds_read_b128 v[206:209], v174 offset:33792
	ds_read_b128 v[224:227], v174 offset:34816
	ds_read_b128 v[228:231], v174 offset:35840
	ds_read_b128 v[232:235], v174 offset:36864
	ds_read_b128 v[236:239], v174 offset:37888
	ds_read_b128 v[240:243], v174 offset:38912
	ds_read_b128 v[244:247], v174 offset:39936
	global_load_lds_dwordx4 v148, s[28:29]
	s_mov_b32 m0, s27
	s_nop 0
	global_load_lds_dwordx4 v146, s[28:29]
	s_waitcnt vmcnt(8)
	s_waitcnt lgkmcnt(0)
	s_barrier
	s_setprio 1
	s_waitcnt lgkmcnt(0)
	v_mfma_f32_16x16x32_bf16 v[140:143], v[112:115], v[202:205], v[140:143]
	v_mfma_f32_16x16x32_bf16 v[136:139], v[120:123], v[202:205], v[136:139]
	v_mfma_f32_16x16x32_bf16 v[108:111], v[112:115], v[224:227], v[108:111]
	v_mfma_f32_16x16x32_bf16 v[104:107], v[120:123], v[224:227], v[104:107]
	v_mfma_f32_16x16x32_bf16 v[92:95], v[112:115], v[232:235], v[92:95]
	v_mfma_f32_16x16x32_bf16 v[88:91], v[120:123], v[232:235], v[88:91]
	v_mfma_f32_16x16x32_bf16 v[76:79], v[112:115], v[240:243], v[76:79]
	v_mfma_f32_16x16x32_bf16 v[72:75], v[120:123], v[240:243], v[72:75]
	v_mfma_f32_16x16x32_bf16 v[140:143], v[116:119], v[206:209], v[140:143]
	v_mfma_f32_16x16x32_bf16 v[136:139], v[124:127], v[206:209], v[136:139]
	v_mfma_f32_16x16x32_bf16 v[108:111], v[116:119], v[228:231], v[108:111]
	v_mfma_f32_16x16x32_bf16 v[104:107], v[124:127], v[228:231], v[104:107]
	v_mfma_f32_16x16x32_bf16 v[92:95], v[116:119], v[236:239], v[92:95]
	v_mfma_f32_16x16x32_bf16 v[88:91], v[124:127], v[236:239], v[88:91]
	v_mfma_f32_16x16x32_bf16 v[76:79], v[116:119], v[244:247], v[76:79]
	v_mfma_f32_16x16x32_bf16 v[72:75], v[124:127], v[244:247], v[72:75]
	s_setprio 0
	s_setprio 1
	v_mfma_f32_16x16x32_bf16 v[132:135], v[176:179], v[202:205], v[132:135]
	v_mfma_f32_16x16x32_bf16 v[128:131], v[194:197], v[202:205], v[128:131]
	v_mfma_f32_16x16x32_bf16 v[100:103], v[176:179], v[224:227], v[100:103]
	v_mfma_f32_16x16x32_bf16 v[96:99], v[194:197], v[224:227], v[96:99]
	v_mfma_f32_16x16x32_bf16 v[84:87], v[176:179], v[232:235], v[84:87]
	v_mfma_f32_16x16x32_bf16 v[80:83], v[194:197], v[232:235], v[80:83]
	v_mfma_f32_16x16x32_bf16 v[68:71], v[176:179], v[240:243], v[68:71]
	v_mfma_f32_16x16x32_bf16 v[64:67], v[194:197], v[240:243], v[64:67]
	v_mfma_f32_16x16x32_bf16 v[132:135], v[180:183], v[206:209], v[132:135]
	v_mfma_f32_16x16x32_bf16 v[128:131], v[198:201], v[206:209], v[128:131]
	v_mfma_f32_16x16x32_bf16 v[100:103], v[180:183], v[228:231], v[100:103]
	v_mfma_f32_16x16x32_bf16 v[96:99], v[198:201], v[228:231], v[96:99]
	v_mfma_f32_16x16x32_bf16 v[84:87], v[180:183], v[236:239], v[84:87]
	v_mfma_f32_16x16x32_bf16 v[80:83], v[198:201], v[236:239], v[80:83]
	v_mfma_f32_16x16x32_bf16 v[68:71], v[180:183], v[244:247], v[68:71]
	v_mfma_f32_16x16x32_bf16 v[64:67], v[198:201], v[244:247], v[64:67]
	s_setprio 0
	s_barrier
	s_add_i32 s28, s36, s4
	v_lshl_add_u64 v[170:171], v[170:171], 0, s[68:69]
	s_mov_b32 m0, s28
	ds_read_b128 v[202:205], v174 offset:49152
	ds_read_b128 v[206:209], v174 offset:50176
	ds_read_b128 v[224:227], v174 offset:51200
	ds_read_b128 v[228:231], v174 offset:52224
	ds_read_b128 v[232:235], v174 offset:53248
	ds_read_b128 v[236:239], v174 offset:54272
	ds_read_b128 v[240:243], v174 offset:55296
	ds_read_b128 v[244:247], v174 offset:56320
	global_load_lds_dwordx4 v[170:171], off
	s_add_i32 m0, s28, 0x1f80
	s_add_u32 s28, s40, 0x160080
	s_addc_u32 s29, s41, 0
	s_add_i32 s36, s37, s4
	global_load_lds_dwordx4 v144, s[40:41] offset:128
	v_lshl_add_u64 v[170:171], s[28:29], 0, v[184:185]
	s_mov_b32 m0, s36
	s_nop 0
	global_load_lds_dwordx4 v[170:171], off
	s_add_i32 m0, s36, 0x2000
	s_nop 0
	global_load_lds_dwordx4 v144, s[28:29]
	s_add_i32 m0, s44, 0xffffff80
	s_nop 0
	global_load_lds_dwordx4 v148, s[42:43] offset:128
	v_lshl_add_u64 v[170:171], v[218:219], 0, s[68:69]
	s_add_i32 m0, s45, 0xffffff80
	s_nop 0
	global_load_lds_dwordx4 v146, s[42:43] offset:128
	s_waitcnt vmcnt(8)
	s_waitcnt lgkmcnt(0)
	s_barrier
	s_setprio 1
	s_waitcnt lgkmcnt(0)
	v_mfma_f32_16x16x32_bf16 v[60:63], v[112:115], v[202:205], v[60:63]
	v_mfma_f32_16x16x32_bf16 v[56:59], v[120:123], v[202:205], v[56:59]
	v_mfma_f32_16x16x32_bf16 v[44:47], v[112:115], v[224:227], v[44:47]
	v_mfma_f32_16x16x32_bf16 v[40:43], v[120:123], v[224:227], v[40:43]
	v_mfma_f32_16x16x32_bf16 v[36:39], v[112:115], v[232:235], v[36:39]
	v_mfma_f32_16x16x32_bf16 v[28:31], v[120:123], v[232:235], v[28:31]
	v_mfma_f32_16x16x32_bf16 v[20:23], v[112:115], v[240:243], v[20:23]
	v_mfma_f32_16x16x32_bf16 v[12:15], v[120:123], v[240:243], v[12:15]
	v_mfma_f32_16x16x32_bf16 v[60:63], v[116:119], v[206:209], v[60:63]
	v_mfma_f32_16x16x32_bf16 v[56:59], v[124:127], v[206:209], v[56:59]
	v_mfma_f32_16x16x32_bf16 v[44:47], v[116:119], v[228:231], v[44:47]
	v_mfma_f32_16x16x32_bf16 v[40:43], v[124:127], v[228:231], v[40:43]
	v_mfma_f32_16x16x32_bf16 v[36:39], v[116:119], v[236:239], v[36:39]
	v_mfma_f32_16x16x32_bf16 v[28:31], v[124:127], v[236:239], v[28:31]
	v_mfma_f32_16x16x32_bf16 v[20:23], v[116:119], v[244:247], v[20:23]
	v_mfma_f32_16x16x32_bf16 v[12:15], v[124:127], v[244:247], v[12:15]
	s_setprio 0
	s_setprio 1
	v_mfma_f32_16x16x32_bf16 v[52:55], v[176:179], v[202:205], v[52:55]
	v_mfma_f32_16x16x32_bf16 v[48:51], v[194:197], v[202:205], v[48:51]
	v_mfma_f32_16x16x32_bf16 v[32:35], v[176:179], v[224:227], v[32:35]
	v_mfma_f32_16x16x32_bf16 v[24:27], v[194:197], v[224:227], v[24:27]
	v_mfma_f32_16x16x32_bf16 v[16:19], v[176:179], v[232:235], v[16:19]
	v_mfma_f32_16x16x32_bf16 v[8:11], v[194:197], v[232:235], v[8:11]
	v_mfma_f32_16x16x32_bf16 v[4:7], v[176:179], v[240:243], v[4:7]
	v_mfma_f32_16x16x32_bf16 v[0:3], v[194:197], v[240:243], v[0:3]
	v_mfma_f32_16x16x32_bf16 v[52:55], v[180:183], v[206:209], v[52:55]
	v_mfma_f32_16x16x32_bf16 v[48:51], v[198:201], v[206:209], v[48:51]
	v_mfma_f32_16x16x32_bf16 v[32:35], v[180:183], v[228:231], v[32:35]
	v_mfma_f32_16x16x32_bf16 v[24:27], v[198:201], v[228:231], v[24:27]
	v_mfma_f32_16x16x32_bf16 v[16:19], v[180:183], v[236:239], v[16:19]
	v_mfma_f32_16x16x32_bf16 v[8:11], v[198:201], v[236:239], v[8:11]
	v_mfma_f32_16x16x32_bf16 v[4:7], v[180:183], v[244:247], v[4:7]
	v_mfma_f32_16x16x32_bf16 v[0:3], v[198:201], v[244:247], v[0:3]
	s_setprio 0
	s_barrier
	s_add_i32 s59, s59, 2
	s_add_u32 s53, s53, 0x100
	s_addc_u32 s58, s58, 0
	s_cmp_gt_u32 s59, 5
	s_mov_b64 s[36:37], s[38:39]
	s_cbranch_scc0 .LBB0_1741
	s_and_b64 vcc, exec, s[8:9]
	s_cbranch_vccz .LBB0_1744
	s_barrier
